# K-loop: setprio before barrier, drop no-op lgkmcnt waits, setprio 0 after M-end barrier
# speedup vs baseline: 1.0083x; 1.0083x over previous
.LBB0_189:
	s_ashr_i32 s11, s10, 31
	s_lshl_b64 s[14:15], s[10:11], 18
	s_add_u32 s14, s35, s14
	s_addc_u32 s15, s36, s15
	s_and_b64 s[18:19], s[16:17], exec
	ds_read_b128 v[0:3], v130
	ds_read_b128 v[4:7], v130 offset:1024
	ds_read_b128 v[8:11], v130 offset:2048
	ds_read_b128 v[12:15], v130 offset:3072
	ds_read_b128 v[16:19], v131
	ds_read_b128 v[20:23], v131 offset:1024
	ds_read_b128 v[24:27], v131 offset:2048
	ds_read_b128 v[28:31], v131 offset:3072
	s_cselect_b32 s5, s15, s25
	s_cselect_b32 s11, s14, s24
	s_ashr_i32 s13, s12, 31
	s_lshl_b64 s[18:19], s[12:13], 18
	s_add_u32 s18, s33, s18
	s_addc_u32 s19, s34, s19
	s_and_b64 s[26:27], s[16:17], exec
	s_cselect_b32 s13, s19, s23
	s_cselect_b32 s57, s18, s22
	s_add_u32 s26, s24, 0x100
	s_addc_u32 s27, s25, 0
	s_add_u32 s28, s24, 0x180
	s_addc_u32 s29, s25, 0
	s_add_u32 s30, s22, 0x100
	s_addc_u32 s31, s23, 0
	ds_read_b128 v[32:35], v132
	ds_read_b128 v[36:39], v132 offset:1024
	ds_read_b128 v[40:43], v132 offset:2048
	ds_read_b128 v[44:47], v132 offset:3072
	ds_read_b128 v[48:51], v132 offset:4096
	ds_read_b128 v[52:55], v132 offset:5120
	ds_read_b128 v[56:59], v132 offset:6144
	ds_read_b128 v[60:63], v132 offset:7168
	s_add_u32 s58, s24, 0x20080
	s_addc_u32 s59, s25, 0
	s_mov_b32 s60, m0
	s_mov_b32 m0, s53
	s_nop 0
	global_load_lds_dwordx4 v129, s[58:59]
	s_mov_b32 m0, s60
	s_add_u32 s58, s24, 0x30080
	s_addc_u32 s59, s25, 0
	s_mov_b32 s60, m0
	s_mov_b32 m0, s54
	s_nop 0
	global_load_lds_dwordx4 v129, s[58:59]
	s_mov_b32 m0, s60
	s_waitcnt vmcnt(8)
	s_waitcnt lgkmcnt(0)
	s_setprio 1
	s_barrier
	v_mfma_scale_f32_16x16x128_f8f6f4 v[64:67], v[0:7], v[32:39], 0, v133, v133 op_sel_hi:[0,0,0]
	v_mfma_scale_f32_16x16x128_f8f6f4 v[68:71], v[8:15], v[32:39], 0, v133, v133 op_sel_hi:[0,0,0]
	v_mfma_scale_f32_16x16x128_f8f6f4 v[72:75], v[0:7], v[40:47], 0, v133, v133 op_sel_hi:[0,0,0]
	v_mfma_scale_f32_16x16x128_f8f6f4 v[76:79], v[8:15], v[40:47], 0, v133, v133 op_sel_hi:[0,0,0]
	v_mfma_scale_f32_16x16x128_f8f6f4 v[80:83], v[0:7], v[48:55], 0, v133, v133 op_sel_hi:[0,0,0]
	v_mfma_scale_f32_16x16x128_f8f6f4 v[84:87], v[8:15], v[48:55], 0, v133, v133 op_sel_hi:[0,0,0]
	v_mfma_scale_f32_16x16x128_f8f6f4 v[88:91], v[0:7], v[56:63], 0, v133, v133 op_sel_hi:[0,0,0]
	v_mfma_scale_f32_16x16x128_f8f6f4 v[92:95], v[8:15], v[56:63], 0, v133, v133 op_sel_hi:[0,0,0]
	s_setprio 0
	s_setprio 1
	v_mfma_scale_f32_16x16x128_f8f6f4 v[104:107], v[16:23], v[32:39], 0, v133, v133 op_sel_hi:[0,0,0]
	v_mfma_scale_f32_16x16x128_f8f6f4 v[108:111], v[24:31], v[32:39], 0, v133, v133 op_sel_hi:[0,0,0]
	v_mfma_scale_f32_16x16x128_f8f6f4 v[154:157], v[16:23], v[40:47], 0, v133, v133 op_sel_hi:[0,0,0]
	v_mfma_scale_f32_16x16x128_f8f6f4 v[158:161], v[24:31], v[40:47], 0, v133, v133 op_sel_hi:[0,0,0]
	v_mfma_scale_f32_16x16x128_f8f6f4 v[162:165], v[16:23], v[48:55], 0, v133, v133 op_sel_hi:[0,0,0]
	v_mfma_scale_f32_16x16x128_f8f6f4 v[166:169], v[24:31], v[48:55], 0, v133, v133 op_sel_hi:[0,0,0]
	v_mfma_scale_f32_16x16x128_f8f6f4 v[170:173], v[16:23], v[56:63], 0, v133, v133 op_sel_hi:[0,0,0]
	v_mfma_scale_f32_16x16x128_f8f6f4 v[174:177], v[24:31], v[56:63], 0, v133, v133 op_sel_hi:[0,0,0]
	s_barrier
	s_setprio 0
	ds_read_b128 v[32:35], v132 offset:16384
	ds_read_b128 v[36:39], v132 offset:17408
	ds_read_b128 v[40:43], v132 offset:18432
	ds_read_b128 v[44:47], v132 offset:19456
	ds_read_b128 v[48:51], v132 offset:20480
	ds_read_b128 v[52:55], v132 offset:21504
	ds_read_b128 v[56:59], v132 offset:22528
	ds_read_b128 v[60:63], v132 offset:23552
	s_mov_b32 s58, m0
	s_mov_b32 m0, s21
	s_nop 0
	global_load_lds_dwordx4 v129, s[30:31]
	s_mov_b32 m0, s58
	s_add_u32 s30, s22, 0x10100
	s_addc_u32 s31, s23, 0
	s_mov_b32 s58, m0
	s_mov_b32 m0, s38
	s_nop 0
	global_load_lds_dwordx4 v129, s[30:31]
	s_mov_b32 m0, s58
	s_add_u32 s30, s22, 0x20100
	s_addc_u32 s31, s23, 0
	s_mov_b32 s58, m0
	s_mov_b32 m0, s39
	s_nop 0
	global_load_lds_dwordx4 v129, s[30:31]
	s_mov_b32 m0, s58
	s_add_u32 s30, s22, 0x30100
	s_addc_u32 s31, s23, 0
	s_mov_b32 s58, m0
	s_mov_b32 m0, s40
	s_nop 0
	global_load_lds_dwordx4 v129, s[30:31]
	s_mov_b32 m0, s58
	s_mov_b32 s30, m0
	s_mov_b32 m0, s37
	s_nop 0
	global_load_lds_dwordx4 v129, s[26:27]
	s_mov_b32 m0, s30
	s_add_u32 s30, s24, 0x10100
	s_addc_u32 s31, s25, 0
	s_mov_b32 s58, m0
	s_mov_b32 m0, s41
	s_nop 0
	global_load_lds_dwordx4 v129, s[30:31]
	s_mov_b32 m0, s58
	s_waitcnt vmcnt(8)
	s_waitcnt lgkmcnt(0)
	s_setprio 1
	s_barrier
	v_mfma_scale_f32_16x16x128_f8f6f4 v[186:189], v[0:7], v[32:39], 0, v133, v133 op_sel_hi:[0,0,0]
	v_mfma_scale_f32_16x16x128_f8f6f4 v[190:193], v[8:15], v[32:39], 0, v133, v133 op_sel_hi:[0,0,0]
	v_mfma_scale_f32_16x16x128_f8f6f4 v[194:197], v[0:7], v[40:47], 0, v133, v133 op_sel_hi:[0,0,0]
	v_mfma_scale_f32_16x16x128_f8f6f4 v[198:201], v[8:15], v[40:47], 0, v133, v133 op_sel_hi:[0,0,0]
	v_mfma_scale_f32_16x16x128_f8f6f4 v[202:205], v[0:7], v[48:55], 0, v133, v133 op_sel_hi:[0,0,0]
	v_mfma_scale_f32_16x16x128_f8f6f4 v[206:209], v[8:15], v[48:55], 0, v133, v133 op_sel_hi:[0,0,0]
	v_mfma_scale_f32_16x16x128_f8f6f4 v[210:213], v[0:7], v[56:63], 0, v133, v133 op_sel_hi:[0,0,0]
	v_mfma_scale_f32_16x16x128_f8f6f4 v[214:217], v[8:15], v[56:63], 0, v133, v133 op_sel_hi:[0,0,0]
	s_setprio 0
	s_setprio 1
	v_mfma_scale_f32_16x16x128_f8f6f4 v[218:221], v[16:23], v[32:39], 0, v133, v133 op_sel_hi:[0,0,0]
	v_mfma_scale_f32_16x16x128_f8f6f4 v[222:225], v[24:31], v[32:39], 0, v133, v133 op_sel_hi:[0,0,0]
	v_mfma_scale_f32_16x16x128_f8f6f4 v[226:229], v[16:23], v[40:47], 0, v133, v133 op_sel_hi:[0,0,0]
	v_mfma_scale_f32_16x16x128_f8f6f4 v[230:233], v[24:31], v[40:47], 0, v133, v133 op_sel_hi:[0,0,0]
	v_mfma_scale_f32_16x16x128_f8f6f4 v[234:237], v[16:23], v[48:55], 0, v133, v133 op_sel_hi:[0,0,0]
	v_mfma_scale_f32_16x16x128_f8f6f4 v[238:241], v[24:31], v[48:55], 0, v133, v133 op_sel_hi:[0,0,0]
	v_mfma_scale_f32_16x16x128_f8f6f4 v[242:245], v[16:23], v[56:63], 0, v133, v133 op_sel_hi:[0,0,0]
	v_mfma_scale_f32_16x16x128_f8f6f4 v[246:249], v[24:31], v[56:63], 0, v133, v133 op_sel_hi:[0,0,0]
	s_barrier
	s_setprio 0
	ds_read_b128 v[0:3], v134
	ds_read_b128 v[4:7], v134 offset:1024
	ds_read_b128 v[12:15], v134 offset:2048
	ds_read_b128 v[16:19], v134 offset:3072
	ds_read_b128 v[138:141], v135
	ds_read_b128 v[142:145], v135 offset:1024
	ds_read_b128 v[146:149], v135 offset:2048
	ds_read_b128 v[150:153], v135 offset:3072
	ds_read_b128 v[20:23], v132 offset:32768
	ds_read_b128 v[24:27], v132 offset:33792
	ds_read_b128 v[28:31], v132 offset:34816
	ds_read_b128 v[32:35], v132 offset:35840
	ds_read_b128 v[36:39], v132 offset:36864
	ds_read_b128 v[40:43], v132 offset:37888
	ds_read_b128 v[44:47], v132 offset:38912
	ds_read_b128 v[48:51], v132 offset:39936
	s_add_u32 s30, s24, 0x20100
	s_addc_u32 s31, s25, 0
	s_mov_b32 s58, m0
	s_mov_b32 m0, s42
	s_nop 0
	global_load_lds_dwordx4 v129, s[30:31]
	s_mov_b32 m0, s58
	s_add_u32 s30, s24, 0x30100
	s_addc_u32 s31, s25, 0
	s_mov_b32 s58, m0
	s_mov_b32 m0, s43
	s_nop 0
	global_load_lds_dwordx4 v129, s[30:31]
	s_mov_b32 m0, s58
	s_waitcnt vmcnt(8)
	s_waitcnt lgkmcnt(0)
	s_setprio 1
	s_barrier
	v_mfma_scale_f32_16x16x128_f8f6f4 v[112:115], v[0:7], v[20:27], v[64:67], v133, v133 op_sel_hi:[0,0,0]
	v_mfma_scale_f32_16x16x128_f8f6f4 v[116:119], v[12:19], v[20:27], v[68:71], v133, v133 op_sel_hi:[0,0,0]
	v_mfma_scale_f32_16x16x128_f8f6f4 v[96:99], v[0:7], v[28:35], v[72:75], v133, v133 op_sel_hi:[0,0,0]
	v_mfma_scale_f32_16x16x128_f8f6f4 v[100:103], v[12:19], v[28:35], v[76:79], v133, v133 op_sel_hi:[0,0,0]
	v_mfma_scale_f32_16x16x128_f8f6f4 v[80:83], v[0:7], v[36:43], v[80:83], v133, v133 op_sel_hi:[0,0,0]
	v_mfma_scale_f32_16x16x128_f8f6f4 v[84:87], v[12:19], v[36:43], v[84:87], v133, v133 op_sel_hi:[0,0,0]
	v_mfma_scale_f32_16x16x128_f8f6f4 v[64:67], v[0:7], v[44:51], v[88:91], v133, v133 op_sel_hi:[0,0,0]
	v_mfma_scale_f32_16x16x128_f8f6f4 v[72:75], v[12:19], v[44:51], v[92:95], v133, v133 op_sel_hi:[0,0,0]
	s_setprio 0
	s_setprio 1
	v_mfma_scale_f32_16x16x128_f8f6f4 v[120:123], v[138:145], v[20:27], v[104:107], v133, v133 op_sel_hi:[0,0,0]
	v_mfma_scale_f32_16x16x128_f8f6f4 v[124:127], v[146:153], v[20:27], v[108:111], v133, v133 op_sel_hi:[0,0,0]
	v_mfma_scale_f32_16x16x128_f8f6f4 v[104:107], v[138:145], v[28:35], v[154:157], v133, v133 op_sel_hi:[0,0,0]
	v_mfma_scale_f32_16x16x128_f8f6f4 v[108:111], v[146:153], v[28:35], v[158:161], v133, v133 op_sel_hi:[0,0,0]
	v_mfma_scale_f32_16x16x128_f8f6f4 v[88:91], v[138:145], v[36:43], v[162:165], v133, v133 op_sel_hi:[0,0,0]
	v_mfma_scale_f32_16x16x128_f8f6f4 v[92:95], v[146:153], v[36:43], v[166:169], v133, v133 op_sel_hi:[0,0,0]
	v_mfma_scale_f32_16x16x128_f8f6f4 v[68:71], v[138:145], v[44:51], v[170:173], v133, v133 op_sel_hi:[0,0,0]
	v_mfma_scale_f32_16x16x128_f8f6f4 v[76:79], v[146:153], v[44:51], v[174:177], v133, v133 op_sel_hi:[0,0,0]
	s_barrier
	s_setprio 0
	s_add_u32 s30, s22, 0x180
	s_addc_u32 s31, s23, 0
	ds_read_b128 v[154:157], v132 offset:49152
	ds_read_b128 v[158:161], v132 offset:50176
	ds_read_b128 v[162:165], v132 offset:51200
	ds_read_b128 v[166:169], v132 offset:52224
	ds_read_b128 v[170:173], v132 offset:53248
	ds_read_b128 v[174:177], v132 offset:54272
	ds_read_b128 v[178:181], v132 offset:55296
	ds_read_b128 v[182:185], v132 offset:56320
	s_mov_b32 s58, m0
	s_mov_b32 m0, s47
	s_nop 0
	global_load_lds_dwordx4 v129, s[30:31]
	s_mov_b32 m0, s58
	s_add_u32 s30, s22, 0x10180
	s_addc_u32 s31, s23, 0
	s_mov_b32 s58, m0
	s_mov_b32 m0, s48
	s_nop 0
	global_load_lds_dwordx4 v129, s[30:31]
	s_mov_b32 m0, s58
	s_add_u32 s30, s22, 0x20180
	s_addc_u32 s31, s23, 0
	s_mov_b32 s58, m0
	s_mov_b32 m0, s51
	s_nop 0
	global_load_lds_dwordx4 v129, s[30:31]
	s_mov_b32 m0, s58
	s_add_u32 s30, s22, 0x30180
	s_addc_u32 s31, s23, 0
	s_mov_b32 s58, m0
	s_mov_b32 m0, s52
	s_nop 0
	global_load_lds_dwordx4 v129, s[30:31]
	s_mov_b32 m0, s58
	s_mov_b32 s30, m0
	s_mov_b32 m0, s49
	s_nop 0
	global_load_lds_dwordx4 v129, s[28:29]
	s_mov_b32 m0, s30
	s_add_u32 s24, s24, 0x10180
	s_addc_u32 s25, s25, 0
	s_mov_b32 s28, m0
	s_mov_b32 m0, s50
	s_nop 0
	global_load_lds_dwordx4 v129, s[24:25]
	s_mov_b32 m0, s28
	s_waitcnt vmcnt(8)
	s_waitcnt lgkmcnt(0)
	s_setprio 1
	s_barrier
	v_mfma_scale_f32_16x16x128_f8f6f4 v[48:51], v[0:7], v[154:161], v[186:189], v133, v133 op_sel_hi:[0,0,0]
	v_mfma_scale_f32_16x16x128_f8f6f4 v[52:55], v[12:19], v[154:161], v[190:193], v133, v133 op_sel_hi:[0,0,0]
	v_mfma_scale_f32_16x16x128_f8f6f4 v[32:35], v[0:7], v[162:169], v[194:197], v133, v133 op_sel_hi:[0,0,0]
	v_mfma_scale_f32_16x16x128_f8f6f4 v[40:43], v[12:19], v[162:169], v[198:201], v133, v133 op_sel_hi:[0,0,0]
	v_mfma_scale_f32_16x16x128_f8f6f4 v[24:27], v[0:7], v[170:177], v[202:205], v133, v133 op_sel_hi:[0,0,0]
	v_mfma_scale_f32_16x16x128_f8f6f4 v[28:31], v[12:19], v[170:177], v[206:209], v133, v133 op_sel_hi:[0,0,0]
	v_mfma_scale_f32_16x16x128_f8f6f4 v[8:11], v[0:7], v[178:185], v[210:213], v133, v133 op_sel_hi:[0,0,0]
	v_mfma_scale_f32_16x16x128_f8f6f4 v[12:15], v[12:19], v[178:185], v[214:217], v133, v133 op_sel_hi:[0,0,0]
	s_setprio 0
	s_setprio 1
	v_mfma_scale_f32_16x16x128_f8f6f4 v[56:59], v[138:145], v[154:161], v[218:221], v133, v133 op_sel_hi:[0,0,0]
	v_mfma_scale_f32_16x16x128_f8f6f4 v[60:63], v[146:153], v[154:161], v[222:225], v133, v133 op_sel_hi:[0,0,0]
	v_mfma_scale_f32_16x16x128_f8f6f4 v[36:39], v[138:145], v[162:169], v[226:229], v133, v133 op_sel_hi:[0,0,0]
	v_mfma_scale_f32_16x16x128_f8f6f4 v[44:47], v[146:153], v[162:169], v[230:233], v133, v133 op_sel_hi:[0,0,0]
	v_mfma_scale_f32_16x16x128_f8f6f4 v[16:19], v[138:145], v[170:177], v[234:237], v133, v133 op_sel_hi:[0,0,0]
	v_mfma_scale_f32_16x16x128_f8f6f4 v[20:23], v[146:153], v[170:177], v[238:241], v133, v133 op_sel_hi:[0,0,0]
	v_mfma_scale_f32_16x16x128_f8f6f4 v[0:3], v[138:145], v[178:185], v[242:245], v133, v133 op_sel_hi:[0,0,0]
	v_mfma_scale_f32_16x16x128_f8f6f4 v[4:7], v[146:153], v[178:185], v[246:249], v133, v133 op_sel_hi:[0,0,0]
	s_barrier
	s_setprio 0
	s_add_u32 s58, s22, 0x200
	s_addc_u32 s59, s23, 0
	s_mov_b32 s60, 0
.LBB0_190:
	ds_read_b128 v[138:141], v130
	ds_read_b128 v[142:145], v130 offset:1024
	ds_read_b128 v[146:149], v130 offset:2048
	ds_read_b128 v[150:153], v130 offset:3072
	ds_read_b128 v[154:157], v131
	ds_read_b128 v[158:161], v131 offset:1024
	ds_read_b128 v[162:165], v131 offset:2048
	ds_read_b128 v[166:169], v131 offset:3072
	s_add_u32 s22, s26, 0x100
	s_addc_u32 s23, s27, 0
	s_cmp_eq_u32 s60, 4
	s_cselect_b32 s24, s11, s22
	s_cselect_b32 s25, s5, s23
	s_cselect_b32 s30, s57, s58
	s_cselect_b32 s31, s13, s59
	s_add_u32 s28, s24, 0x80
	s_addc_u32 s29, s25, 0
	ds_read_b128 v[170:173], v132
	ds_read_b128 v[174:177], v132 offset:1024
	ds_read_b128 v[178:181], v132 offset:2048
	ds_read_b128 v[182:185], v132 offset:3072
	ds_read_b128 v[186:189], v132 offset:4096
	ds_read_b128 v[190:193], v132 offset:5120
	ds_read_b128 v[194:197], v132 offset:6144
	ds_read_b128 v[198:201], v132 offset:7168
	s_add_u32 s62, s26, 0x20080
	s_addc_u32 s63, s27, 0
	s_mov_b32 s61, m0
	s_mov_b32 m0, s53
	s_nop 0
	global_load_lds_dwordx4 v129, s[62:63]
	s_mov_b32 m0, s61
	s_add_u32 s26, s26, 0x30080
	s_addc_u32 s27, s27, 0
	s_mov_b32 s61, m0
	s_mov_b32 m0, s54
	s_nop 0
	global_load_lds_dwordx4 v129, s[26:27]
	s_mov_b32 m0, s61
	s_waitcnt vmcnt(8)
	s_waitcnt lgkmcnt(0)
	s_setprio 1
	s_barrier
	v_mfma_scale_f32_16x16x128_f8f6f4 v[112:115], v[138:145], v[170:177], v[112:115], v133, v133 op_sel_hi:[0,0,0]
	v_mfma_scale_f32_16x16x128_f8f6f4 v[116:119], v[146:153], v[170:177], v[116:119], v133, v133 op_sel_hi:[0,0,0]
	v_mfma_scale_f32_16x16x128_f8f6f4 v[96:99], v[138:145], v[178:185], v[96:99], v133, v133 op_sel_hi:[0,0,0]
	v_mfma_scale_f32_16x16x128_f8f6f4 v[100:103], v[146:153], v[178:185], v[100:103], v133, v133 op_sel_hi:[0,0,0]
	v_mfma_scale_f32_16x16x128_f8f6f4 v[202:205], v[138:145], v[186:193], v[80:83], v133, v133 op_sel_hi:[0,0,0]
	v_mfma_scale_f32_16x16x128_f8f6f4 v[206:209], v[146:153], v[186:193], v[84:87], v133, v133 op_sel_hi:[0,0,0]
	v_mfma_scale_f32_16x16x128_f8f6f4 v[210:213], v[138:145], v[194:201], v[64:67], v133, v133 op_sel_hi:[0,0,0]
	v_mfma_scale_f32_16x16x128_f8f6f4 v[214:217], v[146:153], v[194:201], v[72:75], v133, v133 op_sel_hi:[0,0,0]
	s_setprio 0
	s_setprio 1
	v_mfma_scale_f32_16x16x128_f8f6f4 v[120:123], v[154:161], v[170:177], v[120:123], v133, v133 op_sel_hi:[0,0,0]
	v_mfma_scale_f32_16x16x128_f8f6f4 v[124:127], v[162:169], v[170:177], v[124:127], v133, v133 op_sel_hi:[0,0,0]
	v_mfma_scale_f32_16x16x128_f8f6f4 v[104:107], v[154:161], v[178:185], v[104:107], v133, v133 op_sel_hi:[0,0,0]
	v_mfma_scale_f32_16x16x128_f8f6f4 v[108:111], v[162:169], v[178:185], v[108:111], v133, v133 op_sel_hi:[0,0,0]
	v_mfma_scale_f32_16x16x128_f8f6f4 v[170:173], v[154:161], v[186:193], v[88:91], v133, v133 op_sel_hi:[0,0,0]
	v_mfma_scale_f32_16x16x128_f8f6f4 v[174:177], v[162:169], v[186:193], v[92:95], v133, v133 op_sel_hi:[0,0,0]
	v_mfma_scale_f32_16x16x128_f8f6f4 v[178:181], v[154:161], v[194:201], v[68:71], v133, v133 op_sel_hi:[0,0,0]
	v_mfma_scale_f32_16x16x128_f8f6f4 v[182:185], v[162:169], v[194:201], v[76:79], v133, v133 op_sel_hi:[0,0,0]
	s_barrier
	s_setprio 0
	ds_read_b128 v[64:67], v132 offset:16384
	s_nop 2
	ds_read_b128 v[68:71], v132 offset:17408
	ds_read_b128 v[72:75], v132 offset:18432
	ds_read_b128 v[76:79], v132 offset:19456
	ds_read_b128 v[80:83], v132 offset:20480
	ds_read_b128 v[84:87], v132 offset:21504
	ds_read_b128 v[88:91], v132 offset:22528
	ds_read_b128 v[92:95], v132 offset:23552
	s_mov_b32 s26, m0
	s_mov_b32 m0, s21
	s_nop 0
	global_load_lds_dwordx4 v129, s[30:31]
	s_mov_b32 m0, s26
	s_add_u32 s26, s30, 0x10000
	s_addc_u32 s27, s31, 0
	s_mov_b32 s61, m0
	s_mov_b32 m0, s38
	s_nop 0
	global_load_lds_dwordx4 v129, s[26:27]
	s_mov_b32 m0, s61
	s_add_u32 s26, s30, 0x20000
	s_addc_u32 s27, s31, 0
	s_mov_b32 s61, m0
	s_mov_b32 m0, s39
	s_nop 0
	global_load_lds_dwordx4 v129, s[26:27]
	s_mov_b32 m0, s61
	s_add_u32 s26, s30, 0x30000
	s_addc_u32 s27, s31, 0
	s_mov_b32 s61, m0
	s_mov_b32 m0, s40
	s_nop 0
	global_load_lds_dwordx4 v129, s[26:27]
	s_mov_b32 m0, s61
	s_mov_b32 s26, m0
	s_mov_b32 m0, s37
	s_nop 0
	global_load_lds_dwordx4 v129, s[24:25]
	s_mov_b32 m0, s26
	s_add_u32 s26, s24, 0x10000
	s_addc_u32 s27, s25, 0
	s_mov_b32 s61, m0
	s_mov_b32 m0, s41
	s_nop 0
	global_load_lds_dwordx4 v129, s[26:27]
	s_mov_b32 m0, s61
	s_waitcnt vmcnt(8)
	s_waitcnt lgkmcnt(0)
	s_setprio 1
	s_barrier
	v_mfma_scale_f32_16x16x128_f8f6f4 v[52:55], v[146:153], v[64:71], v[52:55], v133, v133 op_sel_hi:[0,0,0]
	v_mfma_scale_f32_16x16x128_f8f6f4 v[8:11], v[138:145], v[88:95], v[8:11], v133, v133 op_sel_hi:[0,0,0]
	v_mfma_scale_f32_16x16x128_f8f6f4 v[186:189], v[138:145], v[64:71], v[48:51], v133, v133 op_sel_hi:[0,0,0]
	v_mfma_scale_f32_16x16x128_f8f6f4 v[190:193], v[138:145], v[72:79], v[32:35], v133, v133 op_sel_hi:[0,0,0]
	v_mfma_scale_f32_16x16x128_f8f6f4 v[194:197], v[146:153], v[72:79], v[40:43], v133, v133 op_sel_hi:[0,0,0]
	v_mfma_scale_f32_16x16x128_f8f6f4 v[198:201], v[138:145], v[80:87], v[24:27], v133, v133 op_sel_hi:[0,0,0]
	v_mfma_scale_f32_16x16x128_f8f6f4 v[218:221], v[146:153], v[80:87], v[28:31], v133, v133 op_sel_hi:[0,0,0]
	v_mfma_scale_f32_16x16x128_f8f6f4 v[222:225], v[146:153], v[88:95], v[12:15], v133, v133 op_sel_hi:[0,0,0]
	s_setprio 0
	s_setprio 1
	v_mfma_scale_f32_16x16x128_f8f6f4 v[56:59], v[154:161], v[64:71], v[56:59], v133, v133 op_sel_hi:[0,0,0]
	v_mfma_scale_f32_16x16x128_f8f6f4 v[60:63], v[162:169], v[64:71], v[60:63], v133, v133 op_sel_hi:[0,0,0]
	v_mfma_scale_f32_16x16x128_f8f6f4 v[226:229], v[154:161], v[72:79], v[36:39], v133, v133 op_sel_hi:[0,0,0]
	v_mfma_scale_f32_16x16x128_f8f6f4 v[230:233], v[162:169], v[72:79], v[44:47], v133, v133 op_sel_hi:[0,0,0]
	v_mfma_scale_f32_16x16x128_f8f6f4 v[234:237], v[154:161], v[80:87], v[16:19], v133, v133 op_sel_hi:[0,0,0]
	v_mfma_scale_f32_16x16x128_f8f6f4 v[238:241], v[162:169], v[80:87], v[20:23], v133, v133 op_sel_hi:[0,0,0]
	v_mfma_scale_f32_16x16x128_f8f6f4 v[242:245], v[154:161], v[88:95], v[0:3], v133, v133 op_sel_hi:[0,0,0]
	v_mfma_scale_f32_16x16x128_f8f6f4 v[246:249], v[162:169], v[88:95], v[4:7], v133, v133 op_sel_hi:[0,0,0]
	s_barrier
	s_setprio 0
	s_nop 3
	ds_read_b128 v[0:3], v134
	ds_read_b128 v[4:7], v134 offset:1024
	ds_read_b128 v[12:15], v134 offset:2048
	ds_read_b128 v[16:19], v134 offset:3072
	ds_read_b128 v[138:141], v135
	ds_read_b128 v[142:145], v135 offset:1024
	ds_read_b128 v[146:149], v135 offset:2048
	ds_read_b128 v[150:153], v135 offset:3072
	ds_read_b128 v[20:23], v132 offset:32768
	ds_read_b128 v[24:27], v132 offset:33792
	ds_read_b128 v[28:31], v132 offset:34816
	ds_read_b128 v[32:35], v132 offset:35840
	ds_read_b128 v[36:39], v132 offset:36864
	ds_read_b128 v[40:43], v132 offset:37888
	ds_read_b128 v[44:47], v132 offset:38912
	ds_read_b128 v[48:51], v132 offset:39936
	s_add_u32 s26, s24, 0x20000
	s_addc_u32 s27, s25, 0
	s_mov_b32 s61, m0
	s_mov_b32 m0, s42
	s_nop 0
	global_load_lds_dwordx4 v129, s[26:27]
	s_mov_b32 m0, s61
	s_add_u32 s26, s24, 0x30000
	s_addc_u32 s27, s25, 0
	s_mov_b32 s61, m0
	s_mov_b32 m0, s43
	s_nop 0
	global_load_lds_dwordx4 v129, s[26:27]
	s_mov_b32 m0, s61
	s_waitcnt vmcnt(8)
	s_waitcnt lgkmcnt(0)
	s_setprio 1
	s_barrier
	v_mfma_scale_f32_16x16x128_f8f6f4 v[112:115], v[0:7], v[20:27], v[112:115], v133, v133 op_sel_hi:[0,0,0]
	v_mfma_scale_f32_16x16x128_f8f6f4 v[116:119], v[12:19], v[20:27], v[116:119], v133, v133 op_sel_hi:[0,0,0]
	v_mfma_scale_f32_16x16x128_f8f6f4 v[96:99], v[0:7], v[28:35], v[96:99], v133, v133 op_sel_hi:[0,0,0]
	v_mfma_scale_f32_16x16x128_f8f6f4 v[100:103], v[12:19], v[28:35], v[100:103], v133, v133 op_sel_hi:[0,0,0]
	v_mfma_scale_f32_16x16x128_f8f6f4 v[80:83], v[0:7], v[36:43], v[202:205], v133, v133 op_sel_hi:[0,0,0]
	v_mfma_scale_f32_16x16x128_f8f6f4 v[84:87], v[12:19], v[36:43], v[206:209], v133, v133 op_sel_hi:[0,0,0]
	v_mfma_scale_f32_16x16x128_f8f6f4 v[64:67], v[0:7], v[44:51], v[210:213], v133, v133 op_sel_hi:[0,0,0]
	v_mfma_scale_f32_16x16x128_f8f6f4 v[72:75], v[12:19], v[44:51], v[214:217], v133, v133 op_sel_hi:[0,0,0]
	s_setprio 0
	s_setprio 1
	v_mfma_scale_f32_16x16x128_f8f6f4 v[120:123], v[138:145], v[20:27], v[120:123], v133, v133 op_sel_hi:[0,0,0]
	v_mfma_scale_f32_16x16x128_f8f6f4 v[124:127], v[146:153], v[20:27], v[124:127], v133, v133 op_sel_hi:[0,0,0]
	v_mfma_scale_f32_16x16x128_f8f6f4 v[104:107], v[138:145], v[28:35], v[104:107], v133, v133 op_sel_hi:[0,0,0]
	v_mfma_scale_f32_16x16x128_f8f6f4 v[108:111], v[146:153], v[28:35], v[108:111], v133, v133 op_sel_hi:[0,0,0]
	v_mfma_scale_f32_16x16x128_f8f6f4 v[88:91], v[138:145], v[36:43], v[170:173], v133, v133 op_sel_hi:[0,0,0]
	v_mfma_scale_f32_16x16x128_f8f6f4 v[92:95], v[146:153], v[36:43], v[174:177], v133, v133 op_sel_hi:[0,0,0]
	v_mfma_scale_f32_16x16x128_f8f6f4 v[68:71], v[138:145], v[44:51], v[178:181], v133, v133 op_sel_hi:[0,0,0]
	v_mfma_scale_f32_16x16x128_f8f6f4 v[76:79], v[146:153], v[44:51], v[182:185], v133, v133 op_sel_hi:[0,0,0]
	s_barrier
	s_setprio 0
	s_add_u32 s26, s30, 0x80
	s_addc_u32 s27, s31, 0
	ds_read_b128 v[154:157], v132 offset:49152
	ds_read_b128 v[158:161], v132 offset:50176
	ds_read_b128 v[162:165], v132 offset:51200
	ds_read_b128 v[166:169], v132 offset:52224
	ds_read_b128 v[170:173], v132 offset:53248
	ds_read_b128 v[174:177], v132 offset:54272
	ds_read_b128 v[178:181], v132 offset:55296
	ds_read_b128 v[182:185], v132 offset:56320
	s_mov_b32 s61, m0
	s_mov_b32 m0, s47
	s_nop 0
	global_load_lds_dwordx4 v129, s[26:27]
	s_mov_b32 m0, s61
	s_add_u32 s26, s30, 0x10080
	s_addc_u32 s27, s31, 0
	s_mov_b32 s61, m0
	s_mov_b32 m0, s48
	s_nop 0
	global_load_lds_dwordx4 v129, s[26:27]
	s_mov_b32 m0, s61
	s_add_u32 s26, s30, 0x20080
	s_addc_u32 s27, s31, 0
	s_mov_b32 s61, m0
	s_mov_b32 m0, s51
	s_nop 0
	global_load_lds_dwordx4 v129, s[26:27]
	s_mov_b32 m0, s61
	s_add_u32 s26, s30, 0x30080
	s_addc_u32 s27, s31, 0
	s_mov_b32 s30, m0
	s_mov_b32 m0, s52
	s_nop 0
	global_load_lds_dwordx4 v129, s[26:27]
	s_mov_b32 m0, s30
	s_mov_b32 s26, m0
	s_mov_b32 m0, s49
	s_nop 0
	global_load_lds_dwordx4 v129, s[28:29]
	s_mov_b32 m0, s26
	s_add_u32 s24, s24, 0x10080
	s_addc_u32 s25, s25, 0
	s_mov_b32 s26, m0
	s_mov_b32 m0, s50
	s_nop 0
	global_load_lds_dwordx4 v129, s[24:25]
	s_mov_b32 m0, s26
	s_waitcnt vmcnt(8)
	s_waitcnt lgkmcnt(0)
	s_setprio 1
	s_barrier
	v_mfma_scale_f32_16x16x128_f8f6f4 v[48:51], v[0:7], v[154:161], v[186:189], v133, v133 op_sel_hi:[0,0,0]
	v_mfma_scale_f32_16x16x128_f8f6f4 v[52:55], v[12:19], v[154:161], v[52:55], v133, v133 op_sel_hi:[0,0,0]
	v_mfma_scale_f32_16x16x128_f8f6f4 v[32:35], v[0:7], v[162:169], v[190:193], v133, v133 op_sel_hi:[0,0,0]
	v_mfma_scale_f32_16x16x128_f8f6f4 v[40:43], v[12:19], v[162:169], v[194:197], v133, v133 op_sel_hi:[0,0,0]
	v_mfma_scale_f32_16x16x128_f8f6f4 v[24:27], v[0:7], v[170:177], v[198:201], v133, v133 op_sel_hi:[0,0,0]
	v_mfma_scale_f32_16x16x128_f8f6f4 v[28:31], v[12:19], v[170:177], v[218:221], v133, v133 op_sel_hi:[0,0,0]
	v_mfma_scale_f32_16x16x128_f8f6f4 v[8:11], v[0:7], v[178:185], v[8:11], v133, v133 op_sel_hi:[0,0,0]
	v_mfma_scale_f32_16x16x128_f8f6f4 v[12:15], v[12:19], v[178:185], v[222:225], v133, v133 op_sel_hi:[0,0,0]
	s_setprio 0
	s_setprio 1
	v_mfma_scale_f32_16x16x128_f8f6f4 v[56:59], v[138:145], v[154:161], v[56:59], v133, v133 op_sel_hi:[0,0,0]
	v_mfma_scale_f32_16x16x128_f8f6f4 v[60:63], v[146:153], v[154:161], v[60:63], v133, v133 op_sel_hi:[0,0,0]
	v_mfma_scale_f32_16x16x128_f8f6f4 v[36:39], v[138:145], v[162:169], v[226:229], v133, v133 op_sel_hi:[0,0,0]
	v_mfma_scale_f32_16x16x128_f8f6f4 v[44:47], v[146:153], v[162:169], v[230:233], v133, v133 op_sel_hi:[0,0,0]
	v_mfma_scale_f32_16x16x128_f8f6f4 v[16:19], v[138:145], v[170:177], v[234:237], v133, v133 op_sel_hi:[0,0,0]
	v_mfma_scale_f32_16x16x128_f8f6f4 v[20:23], v[146:153], v[170:177], v[238:241], v133, v133 op_sel_hi:[0,0,0]
	v_mfma_scale_f32_16x16x128_f8f6f4 v[0:3], v[138:145], v[178:185], v[242:245], v133, v133 op_sel_hi:[0,0,0]
	v_mfma_scale_f32_16x16x128_f8f6f4 v[4:7], v[146:153], v[178:185], v[246:249], v133, v133 op_sel_hi:[0,0,0]
	s_barrier
	s_setprio 0
	s_add_i32 s60, s60, 2
	s_add_u32 s58, s58, 0x100
	s_addc_u32 s59, s59, 0
	s_cmp_gt_u32 s60, 5
	s_mov_b64 s[26:27], s[22:23]
	s_cbranch_scc0 .LBB0_190
	s_and_b64 vcc, exec, s[8:9]
	s_cbranch_vccz .LBB0_193
	s_barrier

.LBB0_349:
	s_ashr_i32 s7, s6, 31
	s_lshl_b64 s[10:11], s[6:7], 18
	v_readlane_b32 s14, v254, 49
	v_readlane_b32 s15, v254, 50
	s_add_u32 s10, s14, s10
	s_addc_u32 s11, s15, s11
	s_and_b64 s[14:15], s[12:13], exec
	ds_read_b128 v[0:3], v203
	ds_read_b128 v[4:7], v203 offset:1024
	ds_read_b128 v[8:11], v203 offset:2048
	ds_read_b128 v[12:15], v203 offset:3072
	ds_read_b128 v[16:19], v204
	ds_read_b128 v[20:23], v204 offset:1024
	ds_read_b128 v[24:27], v204 offset:2048
	ds_read_b128 v[28:31], v204 offset:3072
	s_cselect_b32 s7, s11, s23
	s_cselect_b32 s52, s10, s22
	s_ashr_i32 s9, s8, 31
	s_lshl_b64 s[14:15], s[8:9], 18
	s_add_u32 s14, s30, s14
	s_addc_u32 s15, s31, s15
	s_and_b64 s[24:25], s[12:13], exec
	s_cselect_b32 s9, s15, s21
	s_cselect_b32 s53, s14, s20
	s_add_u32 s24, s22, 0x100
	s_addc_u32 s25, s23, 0
	s_add_u32 s26, s22, 0x180
	s_addc_u32 s27, s23, 0
	s_add_u32 s28, s20, 0x100
	s_addc_u32 s29, s21, 0
	ds_read_b128 v[32:35], v205
	ds_read_b128 v[36:39], v205 offset:1024
	ds_read_b128 v[40:43], v205 offset:2048
	ds_read_b128 v[44:47], v205 offset:3072
	ds_read_b128 v[48:51], v205 offset:4096
	ds_read_b128 v[52:55], v205 offset:5120
	ds_read_b128 v[56:59], v205 offset:6144
	ds_read_b128 v[60:63], v205 offset:7168
	s_add_u32 s54, s22, 0x20080
	s_addc_u32 s55, s23, 0
	s_mov_b32 s56, m0
	s_mov_b32 m0, s50
	s_nop 0
	global_load_lds_dwordx4 v202, s[54:55]
	s_mov_b32 m0, s56
	s_add_u32 s54, s22, 0x30080
	s_addc_u32 s55, s23, 0
	s_mov_b32 s56, m0
	s_mov_b32 m0, s51
	s_nop 0
	global_load_lds_dwordx4 v202, s[54:55]
	s_mov_b32 m0, s56
	s_waitcnt vmcnt(8)
	s_waitcnt lgkmcnt(0)
	s_setprio 1
	s_barrier
	v_mfma_scale_f32_16x16x128_f8f6f4 v[64:67], v[0:7], v[32:39], 0, v206, v206 op_sel_hi:[0,0,0]
	v_mfma_scale_f32_16x16x128_f8f6f4 v[68:71], v[8:15], v[32:39], 0, v206, v206 op_sel_hi:[0,0,0]
	v_mfma_scale_f32_16x16x128_f8f6f4 v[72:75], v[0:7], v[40:47], 0, v206, v206 op_sel_hi:[0,0,0]
	v_mfma_scale_f32_16x16x128_f8f6f4 v[76:79], v[8:15], v[40:47], 0, v206, v206 op_sel_hi:[0,0,0]
	v_mfma_scale_f32_16x16x128_f8f6f4 v[80:83], v[0:7], v[48:55], 0, v206, v206 op_sel_hi:[0,0,0]
	v_mfma_scale_f32_16x16x128_f8f6f4 v[84:87], v[8:15], v[48:55], 0, v206, v206 op_sel_hi:[0,0,0]
	v_mfma_scale_f32_16x16x128_f8f6f4 v[88:91], v[0:7], v[56:63], 0, v206, v206 op_sel_hi:[0,0,0]
	s_waitcnt vmcnt(3)
	v_mfma_scale_f32_16x16x128_f8f6f4 v[100:103], v[8:15], v[56:63], 0, v206, v206 op_sel_hi:[0,0,0]
	s_setprio 0
	s_setprio 1
	v_mfma_scale_f32_16x16x128_f8f6f4 v[108:111], v[16:23], v[32:39], 0, v206, v206 op_sel_hi:[0,0,0]
	v_mfma_scale_f32_16x16x128_f8f6f4 v[120:123], v[24:31], v[32:39], 0, v206, v206 op_sel_hi:[0,0,0]
	v_mfma_scale_f32_16x16x128_f8f6f4 v[136:139], v[16:23], v[40:47], 0, v206, v206 op_sel_hi:[0,0,0]
	v_mfma_scale_f32_16x16x128_f8f6f4 v[152:155], v[24:31], v[40:47], 0, v206, v206 op_sel_hi:[0,0,0]
	v_mfma_scale_f32_16x16x128_f8f6f4 v[156:159], v[16:23], v[48:55], 0, v206, v206 op_sel_hi:[0,0,0]
	v_mfma_scale_f32_16x16x128_f8f6f4 v[160:163], v[24:31], v[48:55], 0, v206, v206 op_sel_hi:[0,0,0]
	v_mfma_scale_f32_16x16x128_f8f6f4 v[164:167], v[16:23], v[56:63], 0, v206, v206 op_sel_hi:[0,0,0]
	v_mfma_scale_f32_16x16x128_f8f6f4 v[168:171], v[24:31], v[56:63], 0, v206, v206 op_sel_hi:[0,0,0]
	s_barrier
	s_setprio 0
	ds_read_b128 v[32:35], v205 offset:16384
	ds_read_b128 v[36:39], v205 offset:17408
	ds_read_b128 v[40:43], v205 offset:18432
	ds_read_b128 v[44:47], v205 offset:19456
	ds_read_b128 v[48:51], v205 offset:20480
	ds_read_b128 v[52:55], v205 offset:21504
	ds_read_b128 v[56:59], v205 offset:22528
	ds_read_b128 v[60:63], v205 offset:23552
	s_mov_b32 s54, m0
	s_mov_b32 m0, s17
	s_nop 0
	global_load_lds_dwordx4 v201, s[28:29]
	s_mov_b32 m0, s54
	s_add_u32 s28, s20, 0x10100
	s_addc_u32 s29, s21, 0
	s_mov_b32 s54, m0
	s_mov_b32 m0, s19
	s_nop 0
	global_load_lds_dwordx4 v201, s[28:29]
	s_mov_b32 m0, s54
	s_add_u32 s28, s20, 0x20100
	s_addc_u32 s29, s21, 0
	s_mov_b32 s54, m0
	s_mov_b32 m0, s34
	s_nop 0
	global_load_lds_dwordx4 v201, s[28:29]
	s_mov_b32 m0, s54
	s_add_u32 s28, s20, 0x30100
	s_addc_u32 s29, s21, 0
	s_mov_b32 s54, m0
	s_mov_b32 m0, s35
	s_nop 0
	global_load_lds_dwordx4 v201, s[28:29]
	s_mov_b32 m0, s54
	s_mov_b32 s28, m0
	s_mov_b32 m0, s33
	s_nop 0
	global_load_lds_dwordx4 v202, s[24:25]
	s_mov_b32 m0, s28
	s_add_u32 s28, s22, 0x10100
	s_addc_u32 s29, s23, 0
	s_mov_b32 s54, m0
	s_mov_b32 m0, s36
	s_nop 0
	global_load_lds_dwordx4 v202, s[28:29]
	s_mov_b32 m0, s54
	s_waitcnt vmcnt(8)
	s_waitcnt lgkmcnt(0)
	s_setprio 1
	s_barrier
	v_mfma_scale_f32_16x16x128_f8f6f4 v[176:179], v[0:7], v[32:39], 0, v206, v206 op_sel_hi:[0,0,0]
	v_mfma_scale_f32_16x16x128_f8f6f4 v[180:183], v[8:15], v[32:39], 0, v206, v206 op_sel_hi:[0,0,0]
	v_mfma_scale_f32_16x16x128_f8f6f4 v[184:187], v[0:7], v[40:47], 0, v206, v206 op_sel_hi:[0,0,0]
	v_mfma_scale_f32_16x16x128_f8f6f4 v[188:191], v[8:15], v[40:47], 0, v206, v206 op_sel_hi:[0,0,0]
	v_mfma_scale_f32_16x16x128_f8f6f4 v[192:195], v[0:7], v[48:55], 0, v206, v206 op_sel_hi:[0,0,0]
	v_mfma_scale_f32_16x16x128_f8f6f4 v[196:199], v[8:15], v[48:55], 0, v206, v206 op_sel_hi:[0,0,0]
	v_mfma_scale_f32_16x16x128_f8f6f4 v[210:213], v[0:7], v[56:63], 0, v206, v206 op_sel_hi:[0,0,0]
	v_mfma_scale_f32_16x16x128_f8f6f4 v[214:217], v[8:15], v[56:63], 0, v206, v206 op_sel_hi:[0,0,0]
	s_setprio 0
	s_setprio 1
	v_mfma_scale_f32_16x16x128_f8f6f4 v[218:221], v[16:23], v[32:39], 0, v206, v206 op_sel_hi:[0,0,0]
	v_mfma_scale_f32_16x16x128_f8f6f4 v[222:225], v[24:31], v[32:39], 0, v206, v206 op_sel_hi:[0,0,0]
	v_mfma_scale_f32_16x16x128_f8f6f4 v[226:229], v[16:23], v[40:47], 0, v206, v206 op_sel_hi:[0,0,0]
	v_mfma_scale_f32_16x16x128_f8f6f4 v[230:233], v[24:31], v[40:47], 0, v206, v206 op_sel_hi:[0,0,0]
	v_mfma_scale_f32_16x16x128_f8f6f4 v[234:237], v[16:23], v[48:55], 0, v206, v206 op_sel_hi:[0,0,0]
	v_mfma_scale_f32_16x16x128_f8f6f4 v[238:241], v[24:31], v[48:55], 0, v206, v206 op_sel_hi:[0,0,0]
	v_mfma_scale_f32_16x16x128_f8f6f4 v[242:245], v[16:23], v[56:63], 0, v206, v206 op_sel_hi:[0,0,0]
	v_mfma_scale_f32_16x16x128_f8f6f4 v[246:249], v[24:31], v[56:63], 0, v206, v206 op_sel_hi:[0,0,0]
	s_barrier
	s_setprio 0
	ds_read_b128 v[0:3], v207
	ds_read_b128 v[4:7], v207 offset:1024
	ds_read_b128 v[16:19], v207 offset:2048
	ds_read_b128 v[20:23], v207 offset:3072
	s_waitcnt vmcnt(2)
	ds_read_b128 v[112:115], v208
	ds_read_b128 v[116:119], v208 offset:1024
	ds_read_b128 v[144:147], v208 offset:2048
	ds_read_b128 v[148:151], v208 offset:3072
	ds_read_b128 v[8:11], v205 offset:32768
	ds_read_b128 v[12:15], v205 offset:33792
	ds_read_b128 v[24:27], v205 offset:34816
	ds_read_b128 v[28:31], v205 offset:35840
	ds_read_b128 v[32:35], v205 offset:36864
	ds_read_b128 v[36:39], v205 offset:37888
	ds_read_b128 v[40:43], v205 offset:38912
	ds_read_b128 v[44:47], v205 offset:39936
	s_add_u32 s28, s22, 0x20100
	s_addc_u32 s29, s23, 0
	s_mov_b32 s54, m0
	s_mov_b32 m0, s37
	s_nop 0
	global_load_lds_dwordx4 v202, s[28:29]
	s_mov_b32 m0, s54
	s_add_u32 s28, s22, 0x30100
	s_addc_u32 s29, s23, 0
	s_mov_b32 s54, m0
	s_mov_b32 m0, s38
	s_nop 0
	global_load_lds_dwordx4 v202, s[28:29]
	s_mov_b32 m0, s54
	s_waitcnt vmcnt(8)
	s_waitcnt lgkmcnt(0)
	s_setprio 1
	s_barrier
	v_mfma_scale_f32_16x16x128_f8f6f4 v[128:131], v[0:7], v[8:15], v[64:67], v206, v206 op_sel_hi:[0,0,0]
	v_mfma_scale_f32_16x16x128_f8f6f4 v[124:127], v[16:23], v[8:15], v[68:71], v206, v206 op_sel_hi:[0,0,0]
	v_mfma_scale_f32_16x16x128_f8f6f4 v[104:107], v[0:7], v[24:31], v[72:75], v206, v206 op_sel_hi:[0,0,0]
	v_mfma_scale_f32_16x16x128_f8f6f4 v[96:99], v[16:23], v[24:31], v[76:79], v206, v206 op_sel_hi:[0,0,0]
	v_mfma_scale_f32_16x16x128_f8f6f4 v[92:95], v[0:7], v[32:39], v[80:83], v206, v206 op_sel_hi:[0,0,0]
	v_mfma_scale_f32_16x16x128_f8f6f4 v[84:87], v[16:23], v[32:39], v[84:87], v206, v206 op_sel_hi:[0,0,0]
	v_mfma_scale_f32_16x16x128_f8f6f4 v[68:71], v[0:7], v[40:47], v[88:91], v206, v206 op_sel_hi:[0,0,0]
	v_mfma_scale_f32_16x16x128_f8f6f4 v[56:59], v[16:23], v[40:47], v[100:103], v206, v206 op_sel_hi:[0,0,0]
	s_setprio 0
	s_setprio 1
	v_mfma_scale_f32_16x16x128_f8f6f4 v[140:143], v[112:119], v[8:15], v[108:111], v206, v206 op_sel_hi:[0,0,0]
	v_mfma_scale_f32_16x16x128_f8f6f4 v[132:135], v[144:151], v[8:15], v[120:123], v206, v206 op_sel_hi:[0,0,0]
	v_mfma_scale_f32_16x16x128_f8f6f4 v[108:111], v[112:119], v[24:31], v[136:139], v206, v206 op_sel_hi:[0,0,0]
	v_mfma_scale_f32_16x16x128_f8f6f4 v[100:103], v[144:151], v[24:31], v[152:155], v206, v206 op_sel_hi:[0,0,0]
	v_mfma_scale_f32_16x16x128_f8f6f4 v[88:91], v[112:119], v[32:39], v[156:159], v206, v206 op_sel_hi:[0,0,0]
	v_mfma_scale_f32_16x16x128_f8f6f4 v[80:83], v[144:151], v[32:39], v[160:163], v206, v206 op_sel_hi:[0,0,0]
	v_mfma_scale_f32_16x16x128_f8f6f4 v[52:55], v[112:119], v[40:47], v[164:167], v206, v206 op_sel_hi:[0,0,0]
	v_mfma_scale_f32_16x16x128_f8f6f4 v[48:51], v[144:151], v[40:47], v[168:171], v206, v206 op_sel_hi:[0,0,0]
	s_barrier
	s_setprio 0
	s_add_u32 s28, s20, 0x180
	s_addc_u32 s29, s21, 0
	ds_read_b128 v[32:35], v205 offset:49152
	ds_read_b128 v[36:39], v205 offset:50176
	ds_read_b128 v[152:155], v205 offset:51200
	ds_read_b128 v[156:159], v205 offset:52224
	ds_read_b128 v[160:163], v205 offset:53248
	ds_read_b128 v[164:167], v205 offset:54272
	ds_read_b128 v[168:171], v205 offset:55296
	ds_read_b128 v[172:175], v205 offset:56320
	s_mov_b32 s54, m0
	s_mov_b32 m0, s44
	s_nop 0
	global_load_lds_dwordx4 v201, s[28:29]
	s_mov_b32 m0, s54
	s_add_u32 s28, s20, 0x10180
	s_addc_u32 s29, s21, 0
	s_mov_b32 s54, m0
	s_mov_b32 m0, s45
	s_nop 0
	global_load_lds_dwordx4 v201, s[28:29]
	s_mov_b32 m0, s54
	s_add_u32 s28, s20, 0x20180
	s_addc_u32 s29, s21, 0
	s_mov_b32 s54, m0
	s_mov_b32 m0, s48
	s_nop 0
	global_load_lds_dwordx4 v201, s[28:29]
	s_mov_b32 m0, s54
	s_add_u32 s28, s20, 0x30180
	s_addc_u32 s29, s21, 0
	s_mov_b32 s54, m0
	s_mov_b32 m0, s49
	s_nop 0
	global_load_lds_dwordx4 v201, s[28:29]
	s_mov_b32 m0, s54
	s_mov_b32 s28, m0
	s_mov_b32 m0, s46
	s_nop 0
	global_load_lds_dwordx4 v202, s[26:27]
	s_mov_b32 m0, s28
	s_add_u32 s22, s22, 0x10180
	s_addc_u32 s23, s23, 0
	s_mov_b32 s26, m0
	s_mov_b32 m0, s47
	s_nop 0
	global_load_lds_dwordx4 v202, s[22:23]
	s_mov_b32 m0, s26
	s_waitcnt vmcnt(8)
	s_waitcnt lgkmcnt(0)
	s_setprio 1
	s_barrier
	v_mfma_scale_f32_16x16x128_f8f6f4 v[76:79], v[0:7], v[32:39], v[176:179], v206, v206 op_sel_hi:[0,0,0]
	v_mfma_scale_f32_16x16x128_f8f6f4 v[64:67], v[16:23], v[32:39], v[180:183], v206, v206 op_sel_hi:[0,0,0]
	v_mfma_scale_f32_16x16x128_f8f6f4 v[44:47], v[0:7], v[152:159], v[184:187], v206, v206 op_sel_hi:[0,0,0]
	v_mfma_scale_f32_16x16x128_f8f6f4 v[40:43], v[16:23], v[152:159], v[188:191], v206, v206 op_sel_hi:[0,0,0]
	v_mfma_scale_f32_16x16x128_f8f6f4 v[28:31], v[0:7], v[160:167], v[192:195], v206, v206 op_sel_hi:[0,0,0]
	v_mfma_scale_f32_16x16x128_f8f6f4 v[24:27], v[16:23], v[160:167], v[196:199], v206, v206 op_sel_hi:[0,0,0]
	v_mfma_scale_f32_16x16x128_f8f6f4 v[12:15], v[0:7], v[168:175], v[210:213], v206, v206 op_sel_hi:[0,0,0]
	v_mfma_scale_f32_16x16x128_f8f6f4 v[8:11], v[16:23], v[168:175], v[214:217], v206, v206 op_sel_hi:[0,0,0]
	s_setprio 0
	s_setprio 1
	v_mfma_scale_f32_16x16x128_f8f6f4 v[72:75], v[112:119], v[32:39], v[218:221], v206, v206 op_sel_hi:[0,0,0]
	v_mfma_scale_f32_16x16x128_f8f6f4 v[60:63], v[144:151], v[32:39], v[222:225], v206, v206 op_sel_hi:[0,0,0]
	v_mfma_scale_f32_16x16x128_f8f6f4 v[36:39], v[112:119], v[152:159], v[226:229], v206, v206 op_sel_hi:[0,0,0]
	v_mfma_scale_f32_16x16x128_f8f6f4 v[32:35], v[144:151], v[152:159], v[230:233], v206, v206 op_sel_hi:[0,0,0]
	v_mfma_scale_f32_16x16x128_f8f6f4 v[20:23], v[112:119], v[160:167], v[234:237], v206, v206 op_sel_hi:[0,0,0]
	v_mfma_scale_f32_16x16x128_f8f6f4 v[16:19], v[144:151], v[160:167], v[238:241], v206, v206 op_sel_hi:[0,0,0]
	v_mfma_scale_f32_16x16x128_f8f6f4 v[4:7], v[112:119], v[168:175], v[242:245], v206, v206 op_sel_hi:[0,0,0]
	v_mfma_scale_f32_16x16x128_f8f6f4 v[0:3], v[144:151], v[168:175], v[246:249], v206, v206 op_sel_hi:[0,0,0]
	s_barrier
	s_setprio 0
	s_add_u32 s54, s20, 0x200
	s_addc_u32 s55, s21, 0
	s_mov_b32 s56, 0
.LBB0_350:
	ds_read_b128 v[112:115], v203
	ds_read_b128 v[116:119], v203 offset:1024
	ds_read_b128 v[144:147], v203 offset:2048
	ds_read_b128 v[148:151], v203 offset:3072
	ds_read_b128 v[152:155], v204
	ds_read_b128 v[156:159], v204 offset:1024
	ds_read_b128 v[160:163], v204 offset:2048
	ds_read_b128 v[164:167], v204 offset:3072
	s_add_u32 s20, s24, 0x100
	s_addc_u32 s21, s25, 0
	s_cmp_eq_u32 s56, 4
	s_cselect_b32 s22, s52, s20
	s_cselect_b32 s23, s7, s21
	s_cselect_b32 s28, s53, s54
	s_cselect_b32 s29, s9, s55
	s_add_u32 s26, s22, 0x80
	s_addc_u32 s27, s23, 0
	ds_read_b128 v[168:171], v205
	ds_read_b128 v[172:175], v205 offset:1024
	ds_read_b128 v[176:179], v205 offset:2048
	ds_read_b128 v[180:183], v205 offset:3072
	ds_read_b128 v[184:187], v205 offset:4096
	ds_read_b128 v[188:191], v205 offset:5120
	ds_read_b128 v[192:195], v205 offset:6144
	ds_read_b128 v[196:199], v205 offset:7168
	s_add_u32 s58, s24, 0x20080
	s_addc_u32 s59, s25, 0
	s_mov_b32 s57, m0
	s_mov_b32 m0, s50
	s_nop 0
	global_load_lds_dwordx4 v202, s[58:59]
	s_mov_b32 m0, s57
	s_add_u32 s24, s24, 0x30080
	s_addc_u32 s25, s25, 0
	s_mov_b32 s57, m0
	s_mov_b32 m0, s51
	s_nop 0
	global_load_lds_dwordx4 v202, s[24:25]
	s_mov_b32 m0, s57
	s_waitcnt vmcnt(8)
	s_waitcnt lgkmcnt(0)
	s_setprio 1
	s_barrier
	v_mfma_scale_f32_16x16x128_f8f6f4 v[124:127], v[144:151], v[168:175], v[124:127], v206, v206 op_sel_hi:[0,0,0]
	v_mfma_scale_f32_16x16x128_f8f6f4 v[104:107], v[112:119], v[176:183], v[104:107], v206, v206 op_sel_hi:[0,0,0]
	v_mfma_scale_f32_16x16x128_f8f6f4 v[68:71], v[112:119], v[192:199], v[68:71], v206, v206 op_sel_hi:[0,0,0]
	v_mfma_scale_f32_16x16x128_f8f6f4 v[56:59], v[144:151], v[192:199], v[56:59], v206, v206 op_sel_hi:[0,0,0]
	v_mfma_scale_f32_16x16x128_f8f6f4 v[120:123], v[112:119], v[168:175], v[128:131], v206, v206 op_sel_hi:[0,0,0]
	v_mfma_scale_f32_16x16x128_f8f6f4 v[136:139], v[144:151], v[176:183], v[96:99], v206, v206 op_sel_hi:[0,0,0]
	v_mfma_scale_f32_16x16x128_f8f6f4 v[210:213], v[112:119], v[184:191], v[92:95], v206, v206 op_sel_hi:[0,0,0]
	v_mfma_scale_f32_16x16x128_f8f6f4 v[214:217], v[144:151], v[184:191], v[84:87], v206, v206 op_sel_hi:[0,0,0]
	s_setprio 0
	s_setprio 1
	v_mfma_scale_f32_16x16x128_f8f6f4 v[140:143], v[152:159], v[168:175], v[140:143], v206, v206 op_sel_hi:[0,0,0]
	v_mfma_scale_f32_16x16x128_f8f6f4 v[132:135], v[160:167], v[168:175], v[132:135], v206, v206 op_sel_hi:[0,0,0]
	v_mfma_scale_f32_16x16x128_f8f6f4 v[108:111], v[152:159], v[176:183], v[108:111], v206, v206 op_sel_hi:[0,0,0]
	v_mfma_scale_f32_16x16x128_f8f6f4 v[168:171], v[160:167], v[176:183], v[100:103], v206, v206 op_sel_hi:[0,0,0]
	v_mfma_scale_f32_16x16x128_f8f6f4 v[172:175], v[152:159], v[184:191], v[88:91], v206, v206 op_sel_hi:[0,0,0]
	v_mfma_scale_f32_16x16x128_f8f6f4 v[176:179], v[160:167], v[184:191], v[80:83], v206, v206 op_sel_hi:[0,0,0]
	v_mfma_scale_f32_16x16x128_f8f6f4 v[180:183], v[152:159], v[192:199], v[52:55], v206, v206 op_sel_hi:[0,0,0]
	v_mfma_scale_f32_16x16x128_f8f6f4 v[184:187], v[160:167], v[192:199], v[48:51], v206, v206 op_sel_hi:[0,0,0]
	s_barrier
	s_setprio 0
	s_nop 4
	ds_read_b128 v[48:51], v205 offset:16384
	ds_read_b128 v[52:55], v205 offset:17408
	ds_read_b128 v[80:83], v205 offset:18432
	ds_read_b128 v[84:87], v205 offset:19456
	ds_read_b128 v[88:91], v205 offset:20480
	ds_read_b128 v[92:95], v205 offset:21504
	ds_read_b128 v[96:99], v205 offset:22528
	ds_read_b128 v[100:103], v205 offset:23552
	s_mov_b32 s24, m0
	s_mov_b32 m0, s17
	s_nop 0
	global_load_lds_dwordx4 v201, s[28:29]
	s_mov_b32 m0, s24
	s_add_u32 s24, s28, 0x10000
	s_addc_u32 s25, s29, 0
	s_mov_b32 s57, m0
	s_mov_b32 m0, s19
	s_nop 0
	global_load_lds_dwordx4 v201, s[24:25]
	s_mov_b32 m0, s57
	s_add_u32 s24, s28, 0x20000
	s_addc_u32 s25, s29, 0
	s_mov_b32 s57, m0
	s_mov_b32 m0, s34
	s_nop 0
	global_load_lds_dwordx4 v201, s[24:25]
	s_mov_b32 m0, s57
	s_add_u32 s24, s28, 0x30000
	s_addc_u32 s25, s29, 0
	s_mov_b32 s57, m0
	s_mov_b32 m0, s35
	s_nop 0
	global_load_lds_dwordx4 v201, s[24:25]
	s_mov_b32 m0, s57
	s_mov_b32 s24, m0
	s_mov_b32 m0, s33
	s_nop 0
	global_load_lds_dwordx4 v202, s[22:23]
	s_mov_b32 m0, s24
	s_add_u32 s24, s22, 0x10000
	s_addc_u32 s25, s23, 0
	s_mov_b32 s57, m0
	s_mov_b32 m0, s36
	s_nop 0
	global_load_lds_dwordx4 v202, s[24:25]
	s_mov_b32 m0, s57
	s_waitcnt vmcnt(8)
	s_waitcnt lgkmcnt(0)
	s_setprio 1
	s_barrier
	v_mfma_scale_f32_16x16x128_f8f6f4 v[76:79], v[112:119], v[48:55], v[76:79], v206, v206 op_sel_hi:[0,0,0]
	v_mfma_scale_f32_16x16x128_f8f6f4 v[64:67], v[144:151], v[48:55], v[64:67], v206, v206 op_sel_hi:[0,0,0]
	v_mfma_scale_f32_16x16x128_f8f6f4 v[188:191], v[112:119], v[80:87], v[44:47], v206, v206 op_sel_hi:[0,0,0]
	v_mfma_scale_f32_16x16x128_f8f6f4 v[192:195], v[144:151], v[80:87], v[40:43], v206, v206 op_sel_hi:[0,0,0]
	v_mfma_scale_f32_16x16x128_f8f6f4 v[196:199], v[112:119], v[88:95], v[28:31], v206, v206 op_sel_hi:[0,0,0]
	v_mfma_scale_f32_16x16x128_f8f6f4 v[218:221], v[144:151], v[88:95], v[24:27], v206, v206 op_sel_hi:[0,0,0]
	v_mfma_scale_f32_16x16x128_f8f6f4 v[222:225], v[112:119], v[96:103], v[12:15], v206, v206 op_sel_hi:[0,0,0]
	v_mfma_scale_f32_16x16x128_f8f6f4 v[226:229], v[144:151], v[96:103], v[8:11], v206, v206 op_sel_hi:[0,0,0]
	s_setprio 0
	s_setprio 1
	v_mfma_scale_f32_16x16x128_f8f6f4 v[72:75], v[152:159], v[48:55], v[72:75], v206, v206 op_sel_hi:[0,0,0]
	v_mfma_scale_f32_16x16x128_f8f6f4 v[60:63], v[160:167], v[48:55], v[60:63], v206, v206 op_sel_hi:[0,0,0]
	v_mfma_scale_f32_16x16x128_f8f6f4 v[230:233], v[152:159], v[80:87], v[36:39], v206, v206 op_sel_hi:[0,0,0]
	v_mfma_scale_f32_16x16x128_f8f6f4 v[234:237], v[160:167], v[80:87], v[32:35], v206, v206 op_sel_hi:[0,0,0]
	v_mfma_scale_f32_16x16x128_f8f6f4 v[238:241], v[152:159], v[88:95], v[20:23], v206, v206 op_sel_hi:[0,0,0]
	v_mfma_scale_f32_16x16x128_f8f6f4 v[242:245], v[160:167], v[88:95], v[16:19], v206, v206 op_sel_hi:[0,0,0]
	v_mfma_scale_f32_16x16x128_f8f6f4 v[246:249], v[152:159], v[96:103], v[4:7], v206, v206 op_sel_hi:[0,0,0]
	v_mfma_scale_f32_16x16x128_f8f6f4 v[250:253], v[160:167], v[96:103], v[0:3], v206, v206 op_sel_hi:[0,0,0]
	s_barrier
	s_setprio 0
	s_nop 4
	ds_read_b128 v[0:3], v207
	ds_read_b128 v[4:7], v207 offset:1024
	ds_read_b128 v[16:19], v207 offset:2048
	ds_read_b128 v[20:23], v207 offset:3072
	ds_read_b128 v[112:115], v208
	ds_read_b128 v[116:119], v208 offset:1024
	ds_read_b128 v[144:147], v208 offset:2048
	ds_read_b128 v[148:151], v208 offset:3072
	ds_read_b128 v[8:11], v205 offset:32768
	ds_read_b128 v[12:15], v205 offset:33792
	ds_read_b128 v[24:27], v205 offset:34816
	ds_read_b128 v[28:31], v205 offset:35840
	ds_read_b128 v[32:35], v205 offset:36864
	ds_read_b128 v[36:39], v205 offset:37888
	ds_read_b128 v[40:43], v205 offset:38912
	ds_read_b128 v[44:47], v205 offset:39936
	s_add_u32 s24, s22, 0x20000
	s_addc_u32 s25, s23, 0
	s_mov_b32 s57, m0
	s_mov_b32 m0, s37
	s_nop 0
	global_load_lds_dwordx4 v202, s[24:25]
	s_mov_b32 m0, s57
	s_add_u32 s24, s22, 0x30000
	s_addc_u32 s25, s23, 0
	s_mov_b32 s57, m0
	s_mov_b32 m0, s38
	s_nop 0
	global_load_lds_dwordx4 v202, s[24:25]
	s_mov_b32 m0, s57
	s_waitcnt vmcnt(8)
	s_waitcnt lgkmcnt(0)
	s_setprio 1
	s_barrier
	v_mfma_scale_f32_16x16x128_f8f6f4 v[128:131], v[0:7], v[8:15], v[120:123], v206, v206 op_sel_hi:[0,0,0]
	v_mfma_scale_f32_16x16x128_f8f6f4 v[124:127], v[16:23], v[8:15], v[124:127], v206, v206 op_sel_hi:[0,0,0]
	v_mfma_scale_f32_16x16x128_f8f6f4 v[104:107], v[0:7], v[24:31], v[104:107], v206, v206 op_sel_hi:[0,0,0]
	v_mfma_scale_f32_16x16x128_f8f6f4 v[96:99], v[16:23], v[24:31], v[136:139], v206, v206 op_sel_hi:[0,0,0]
	v_mfma_scale_f32_16x16x128_f8f6f4 v[92:95], v[0:7], v[32:39], v[210:213], v206, v206 op_sel_hi:[0,0,0]
	v_mfma_scale_f32_16x16x128_f8f6f4 v[84:87], v[16:23], v[32:39], v[214:217], v206, v206 op_sel_hi:[0,0,0]
	v_mfma_scale_f32_16x16x128_f8f6f4 v[68:71], v[0:7], v[40:47], v[68:71], v206, v206 op_sel_hi:[0,0,0]
	v_mfma_scale_f32_16x16x128_f8f6f4 v[56:59], v[16:23], v[40:47], v[56:59], v206, v206 op_sel_hi:[0,0,0]
	s_setprio 0
	s_setprio 1
	v_mfma_scale_f32_16x16x128_f8f6f4 v[140:143], v[112:119], v[8:15], v[140:143], v206, v206 op_sel_hi:[0,0,0]
	v_mfma_scale_f32_16x16x128_f8f6f4 v[132:135], v[144:151], v[8:15], v[132:135], v206, v206 op_sel_hi:[0,0,0]
	v_mfma_scale_f32_16x16x128_f8f6f4 v[108:111], v[112:119], v[24:31], v[108:111], v206, v206 op_sel_hi:[0,0,0]
	v_mfma_scale_f32_16x16x128_f8f6f4 v[100:103], v[144:151], v[24:31], v[168:171], v206, v206 op_sel_hi:[0,0,0]
	v_mfma_scale_f32_16x16x128_f8f6f4 v[88:91], v[112:119], v[32:39], v[172:175], v206, v206 op_sel_hi:[0,0,0]
	v_mfma_scale_f32_16x16x128_f8f6f4 v[80:83], v[144:151], v[32:39], v[176:179], v206, v206 op_sel_hi:[0,0,0]
	v_mfma_scale_f32_16x16x128_f8f6f4 v[52:55], v[112:119], v[40:47], v[180:183], v206, v206 op_sel_hi:[0,0,0]
	v_mfma_scale_f32_16x16x128_f8f6f4 v[48:51], v[144:151], v[40:47], v[184:187], v206, v206 op_sel_hi:[0,0,0]
	s_barrier
	s_setprio 0
	s_add_u32 s24, s28, 0x80
	s_addc_u32 s25, s29, 0
	ds_read_b128 v[32:35], v205 offset:49152
	ds_read_b128 v[36:39], v205 offset:50176
	ds_read_b128 v[152:155], v205 offset:51200
	ds_read_b128 v[156:159], v205 offset:52224
	ds_read_b128 v[160:163], v205 offset:53248
	ds_read_b128 v[164:167], v205 offset:54272
	ds_read_b128 v[168:171], v205 offset:55296
	ds_read_b128 v[172:175], v205 offset:56320
	s_mov_b32 s57, m0
	s_mov_b32 m0, s44
	s_nop 0
	global_load_lds_dwordx4 v201, s[24:25]
	s_mov_b32 m0, s57
	s_add_u32 s24, s28, 0x10080
	s_addc_u32 s25, s29, 0
	s_mov_b32 s57, m0
	s_mov_b32 m0, s45
	s_nop 0
	global_load_lds_dwordx4 v201, s[24:25]
	s_mov_b32 m0, s57
	s_add_u32 s24, s28, 0x20080
	s_addc_u32 s25, s29, 0
	s_mov_b32 s57, m0
	s_mov_b32 m0, s48
	s_nop 0
	global_load_lds_dwordx4 v201, s[24:25]
	s_mov_b32 m0, s57
	s_add_u32 s24, s28, 0x30080
	s_addc_u32 s25, s29, 0
	s_mov_b32 s28, m0
	s_mov_b32 m0, s49
	s_nop 0
	global_load_lds_dwordx4 v201, s[24:25]
	s_mov_b32 m0, s28
	s_mov_b32 s24, m0
	s_mov_b32 m0, s46
	s_nop 0
	global_load_lds_dwordx4 v202, s[26:27]
	s_mov_b32 m0, s24
	s_add_u32 s22, s22, 0x10080
	s_addc_u32 s23, s23, 0
	s_mov_b32 s24, m0
	s_mov_b32 m0, s47
	s_nop 0
	global_load_lds_dwordx4 v202, s[22:23]
	s_mov_b32 m0, s24
	s_waitcnt vmcnt(8)
	s_waitcnt lgkmcnt(0)
	s_setprio 1
	s_barrier
	v_mfma_scale_f32_16x16x128_f8f6f4 v[76:79], v[0:7], v[32:39], v[76:79], v206, v206 op_sel_hi:[0,0,0]
	v_mfma_scale_f32_16x16x128_f8f6f4 v[64:67], v[16:23], v[32:39], v[64:67], v206, v206 op_sel_hi:[0,0,0]
	v_mfma_scale_f32_16x16x128_f8f6f4 v[44:47], v[0:7], v[152:159], v[188:191], v206, v206 op_sel_hi:[0,0,0]
	v_mfma_scale_f32_16x16x128_f8f6f4 v[40:43], v[16:23], v[152:159], v[192:195], v206, v206 op_sel_hi:[0,0,0]
	v_mfma_scale_f32_16x16x128_f8f6f4 v[28:31], v[0:7], v[160:167], v[196:199], v206, v206 op_sel_hi:[0,0,0]
	v_mfma_scale_f32_16x16x128_f8f6f4 v[24:27], v[16:23], v[160:167], v[218:221], v206, v206 op_sel_hi:[0,0,0]
	v_mfma_scale_f32_16x16x128_f8f6f4 v[12:15], v[0:7], v[168:175], v[222:225], v206, v206 op_sel_hi:[0,0,0]
	v_mfma_scale_f32_16x16x128_f8f6f4 v[8:11], v[16:23], v[168:175], v[226:229], v206, v206 op_sel_hi:[0,0,0]
	s_setprio 0
	s_setprio 1
	v_mfma_scale_f32_16x16x128_f8f6f4 v[72:75], v[112:119], v[32:39], v[72:75], v206, v206 op_sel_hi:[0,0,0]
	v_mfma_scale_f32_16x16x128_f8f6f4 v[60:63], v[144:151], v[32:39], v[60:63], v206, v206 op_sel_hi:[0,0,0]
	v_mfma_scale_f32_16x16x128_f8f6f4 v[36:39], v[112:119], v[152:159], v[230:233], v206, v206 op_sel_hi:[0,0,0]
	v_mfma_scale_f32_16x16x128_f8f6f4 v[32:35], v[144:151], v[152:159], v[234:237], v206, v206 op_sel_hi:[0,0,0]
	v_mfma_scale_f32_16x16x128_f8f6f4 v[20:23], v[112:119], v[160:167], v[238:241], v206, v206 op_sel_hi:[0,0,0]
	v_mfma_scale_f32_16x16x128_f8f6f4 v[16:19], v[144:151], v[160:167], v[242:245], v206, v206 op_sel_hi:[0,0,0]
	v_mfma_scale_f32_16x16x128_f8f6f4 v[4:7], v[112:119], v[168:175], v[246:249], v206, v206 op_sel_hi:[0,0,0]
	v_mfma_scale_f32_16x16x128_f8f6f4 v[0:3], v[144:151], v[168:175], v[250:253], v206, v206 op_sel_hi:[0,0,0]
	s_barrier
	s_setprio 0
	s_add_i32 s56, s56, 2
	s_add_u32 s54, s54, 0x100
	s_addc_u32 s55, s55, 0
	s_cmp_gt_u32 s56, 5
	s_mov_b64 s[24:25], s[20:21]
	s_cbranch_scc0 .LBB0_350
	s_and_b64 vcc, exec, s[4:5]
	s_cbranch_vccz .LBB0_353
	s_barrier

.LBB0_530:
	s_add_u32 s34, s34, 0x100
	s_addc_u32 s35, s35, 0
	s_and_b64 s[36:37], s[38:39], exec
	s_cselect_b32 s42, s16, s34
	s_cselect_b32 s43, s17, s35
	s_add_u32 s36, s42, 0x80
	s_addc_u32 s37, s43, 0
	s_waitcnt vmcnt(8)
	s_and_b64 s[38:39], s[38:39], exec
	s_waitcnt lgkmcnt(0)
	s_cselect_b32 s38, s26, s15
	s_cselect_b32 s39, s27, s23
	s_add_u32 s40, s38, 0x80
	s_addc_u32 s41, s39, 0
	s_barrier
	s_setprio 1
	s_waitcnt lgkmcnt(6)
	v_mfma_scale_f32_16x16x128_f8f6f4 v[188:191], v[16:23], v[56:63], v[188:191], v205, v205 op_sel_hi:[0,0,0]
	v_mfma_scale_f32_16x16x128_f8f6f4 v[180:183], v[24:31], v[56:63], v[180:183], v205, v205 op_sel_hi:[0,0,0]
	s_waitcnt lgkmcnt(4)
	v_mfma_scale_f32_16x16x128_f8f6f4 v[172:175], v[16:23], v[48:55], v[172:175], v205, v205 op_sel_hi:[0,0,0]
	v_mfma_scale_f32_16x16x128_f8f6f4 v[164:167], v[24:31], v[48:55], v[164:167], v205, v205 op_sel_hi:[0,0,0]
	s_waitcnt lgkmcnt(2)
	v_mfma_scale_f32_16x16x128_f8f6f4 v[156:159], v[16:23], v[40:47], v[156:159], v205, v205 op_sel_hi:[0,0,0]
	v_mfma_scale_f32_16x16x128_f8f6f4 v[148:151], v[24:31], v[40:47], v[148:151], v205, v205 op_sel_hi:[0,0,0]
	s_waitcnt lgkmcnt(0)
	v_mfma_scale_f32_16x16x128_f8f6f4 v[140:143], v[16:23], v[32:39], v[140:143], v205, v205 op_sel_hi:[0,0,0]
	v_mfma_scale_f32_16x16x128_f8f6f4 v[132:135], v[24:31], v[32:39], v[132:135], v205, v205 op_sel_hi:[0,0,0]
	s_setprio 0
	s_setprio 1
	v_mfma_scale_f32_16x16x128_f8f6f4 v[184:187], v[0:7], v[56:63], v[184:187], v205, v205 op_sel_hi:[0,0,0]
	v_mfma_scale_f32_16x16x128_f8f6f4 v[176:179], v[8:15], v[56:63], v[176:179], v205, v205 op_sel_hi:[0,0,0]
	v_mfma_scale_f32_16x16x128_f8f6f4 v[168:171], v[0:7], v[48:55], v[168:171], v205, v205 op_sel_hi:[0,0,0]
	v_mfma_scale_f32_16x16x128_f8f6f4 v[160:163], v[8:15], v[48:55], v[160:163], v205, v205 op_sel_hi:[0,0,0]
	v_mfma_scale_f32_16x16x128_f8f6f4 v[152:155], v[0:7], v[40:47], v[152:155], v205, v205 op_sel_hi:[0,0,0]
	v_mfma_scale_f32_16x16x128_f8f6f4 v[144:147], v[8:15], v[40:47], v[144:147], v205, v205 op_sel_hi:[0,0,0]
	v_mfma_scale_f32_16x16x128_f8f6f4 v[136:139], v[0:7], v[32:39], v[136:139], v205, v205 op_sel_hi:[0,0,0]
	v_mfma_scale_f32_16x16x128_f8f6f4 v[128:131], v[8:15], v[32:39], v[128:131], v205, v205 op_sel_hi:[0,0,0]
	s_setprio 0
	s_barrier
	s_add_u32 s70, s38, 0x10000
	ds_read_b128 v[32:35], v210 offset:16384
	ds_read_b128 v[36:39], v210 offset:17408
	ds_read_b128 v[40:43], v210 offset:18432
	ds_read_b128 v[44:47], v210 offset:19456
	ds_read_b128 v[48:51], v210 offset:20480
	ds_read_b128 v[52:55], v210 offset:21504
	ds_read_b128 v[56:59], v210 offset:22528
	ds_read_b128 v[60:63], v210 offset:23552
	s_mov_b32 s69, m0
	s_mov_b32 m0, s29
	s_nop 0
	global_load_lds_dwordx4 v199, s[38:39]
	s_mov_b32 m0, s69
	s_addc_u32 s71, s39, 0
	s_mov_b32 s69, m0
	s_mov_b32 m0, s47
	s_nop 0
	global_load_lds_dwordx4 v199, s[70:71]
	s_mov_b32 m0, s69
	s_add_u32 s70, s38, 0x20000
	s_addc_u32 s71, s39, 0
	s_mov_b32 s69, m0
	s_mov_b32 m0, s48
	s_nop 0
	global_load_lds_dwordx4 v199, s[70:71]
	s_mov_b32 m0, s69
	s_add_u32 s70, s38, 0x30000
	s_addc_u32 s71, s39, 0
	s_mov_b32 s69, m0
	s_mov_b32 m0, s49
	s_nop 0
	global_load_lds_dwordx4 v199, s[70:71]
	s_mov_b32 m0, s69
	s_nop 0
	s_mov_b32 s69, m0
	s_mov_b32 m0, s46
	s_nop 0
	global_load_lds_dwordx4 v200, s[42:43]
	s_mov_b32 m0, s69
	s_nop 0
	s_mov_b32 s69, m0
	s_mov_b32 m0, s50
	s_nop 0
	global_load_lds_dwordx4 v201, s[42:43]
	s_mov_b32 m0, s69
	s_waitcnt vmcnt(8)
	s_waitcnt lgkmcnt(0)
	s_setprio 1
	s_barrier
	v_mfma_scale_f32_16x16x128_f8f6f4 v[124:127], v[16:23], v[32:39], v[124:127], v205, v205 op_sel_hi:[0,0,0]
	v_mfma_scale_f32_16x16x128_f8f6f4 v[116:119], v[24:31], v[32:39], v[116:119], v205, v205 op_sel_hi:[0,0,0]
	v_mfma_scale_f32_16x16x128_f8f6f4 v[108:111], v[16:23], v[40:47], v[108:111], v205, v205 op_sel_hi:[0,0,0]
	v_mfma_scale_f32_16x16x128_f8f6f4 v[100:103], v[24:31], v[40:47], v[100:103], v205, v205 op_sel_hi:[0,0,0]
	v_mfma_scale_f32_16x16x128_f8f6f4 v[92:95], v[16:23], v[48:55], v[92:95], v205, v205 op_sel_hi:[0,0,0]
	v_mfma_scale_f32_16x16x128_f8f6f4 v[84:87], v[24:31], v[48:55], v[84:87], v205, v205 op_sel_hi:[0,0,0]
	v_mfma_scale_f32_16x16x128_f8f6f4 v[72:75], v[16:23], v[56:63], v[72:75], v205, v205 op_sel_hi:[0,0,0]
	v_mfma_scale_f32_16x16x128_f8f6f4 v[64:67], v[24:31], v[56:63], v[64:67], v205, v205 op_sel_hi:[0,0,0]
	s_setprio 0
	s_setprio 1
	v_mfma_scale_f32_16x16x128_f8f6f4 v[120:123], v[0:7], v[32:39], v[120:123], v205, v205 op_sel_hi:[0,0,0]
	v_mfma_scale_f32_16x16x128_f8f6f4 v[112:115], v[8:15], v[32:39], v[112:115], v205, v205 op_sel_hi:[0,0,0]
	v_mfma_scale_f32_16x16x128_f8f6f4 v[104:107], v[0:7], v[40:47], v[104:107], v205, v205 op_sel_hi:[0,0,0]
	v_mfma_scale_f32_16x16x128_f8f6f4 v[96:99], v[8:15], v[40:47], v[96:99], v205, v205 op_sel_hi:[0,0,0]
	v_mfma_scale_f32_16x16x128_f8f6f4 v[88:91], v[0:7], v[48:55], v[88:91], v205, v205 op_sel_hi:[0,0,0]
	v_mfma_scale_f32_16x16x128_f8f6f4 v[80:83], v[8:15], v[48:55], v[80:83], v205, v205 op_sel_hi:[0,0,0]
	v_mfma_scale_f32_16x16x128_f8f6f4 v[76:79], v[0:7], v[56:63], v[76:79], v205, v205 op_sel_hi:[0,0,0]
	v_mfma_scale_f32_16x16x128_f8f6f4 v[68:71], v[8:15], v[56:63], v[68:71], v205, v205 op_sel_hi:[0,0,0]
	s_barrier
	s_setprio 0
	v_add_u32_e32 v12, 0x18000, v209
	v_add_u32_e32 v28, 0x1c000, v209
	ds_read_b128 v[0:3], v12
	ds_read_b128 v[4:7], v12 offset:1024
	ds_read_b128 v[8:11], v12 offset:2048
	ds_read_b128 v[12:15], v12 offset:3072
	ds_read_b128 v[16:19], v28
	ds_read_b128 v[20:23], v28 offset:1024
	ds_read_b128 v[24:27], v28 offset:2048
	ds_read_b128 v[28:31], v28 offset:3072
	ds_read_b128 v[32:35], v210 offset:32768
	ds_read_b128 v[36:39], v210 offset:33792
	ds_read_b128 v[40:43], v210 offset:34816
	ds_read_b128 v[44:47], v210 offset:35840
	ds_read_b128 v[48:51], v210 offset:36864
	ds_read_b128 v[52:55], v210 offset:37888
	ds_read_b128 v[56:59], v210 offset:38912
	ds_read_b128 v[60:63], v210 offset:39936
	s_mov_b32 s69, m0
	s_mov_b32 m0, s51
	s_nop 0
	global_load_lds_dwordx4 v202, s[42:43]
	s_mov_b32 m0, s69
	s_nop 0
	s_mov_b32 s69, m0
	s_mov_b32 m0, s52
	s_nop 0
	global_load_lds_dwordx4 v203, s[42:43]
	s_mov_b32 m0, s69
	s_waitcnt vmcnt(8)
	s_waitcnt lgkmcnt(0)
	s_setprio 1
	s_barrier
	v_mfma_scale_f32_16x16x128_f8f6f4 v[188:191], v[0:7], v[32:39], v[188:191], v205, v205 op_sel_hi:[0,0,0]
	v_mfma_scale_f32_16x16x128_f8f6f4 v[180:183], v[8:15], v[32:39], v[180:183], v205, v205 op_sel_hi:[0,0,0]
	v_mfma_scale_f32_16x16x128_f8f6f4 v[172:175], v[0:7], v[40:47], v[172:175], v205, v205 op_sel_hi:[0,0,0]
	v_mfma_scale_f32_16x16x128_f8f6f4 v[164:167], v[8:15], v[40:47], v[164:167], v205, v205 op_sel_hi:[0,0,0]
	v_mfma_scale_f32_16x16x128_f8f6f4 v[156:159], v[0:7], v[48:55], v[156:159], v205, v205 op_sel_hi:[0,0,0]
	v_mfma_scale_f32_16x16x128_f8f6f4 v[148:151], v[8:15], v[48:55], v[148:151], v205, v205 op_sel_hi:[0,0,0]
	v_mfma_scale_f32_16x16x128_f8f6f4 v[140:143], v[0:7], v[56:63], v[140:143], v205, v205 op_sel_hi:[0,0,0]
	v_mfma_scale_f32_16x16x128_f8f6f4 v[132:135], v[8:15], v[56:63], v[132:135], v205, v205 op_sel_hi:[0,0,0]
	s_setprio 0
	s_setprio 1
	v_mfma_scale_f32_16x16x128_f8f6f4 v[184:187], v[16:23], v[32:39], v[184:187], v205, v205 op_sel_hi:[0,0,0]
	v_mfma_scale_f32_16x16x128_f8f6f4 v[176:179], v[24:31], v[32:39], v[176:179], v205, v205 op_sel_hi:[0,0,0]
	v_mfma_scale_f32_16x16x128_f8f6f4 v[168:171], v[16:23], v[40:47], v[168:171], v205, v205 op_sel_hi:[0,0,0]
	v_mfma_scale_f32_16x16x128_f8f6f4 v[160:163], v[24:31], v[40:47], v[160:163], v205, v205 op_sel_hi:[0,0,0]
	v_mfma_scale_f32_16x16x128_f8f6f4 v[152:155], v[16:23], v[48:55], v[152:155], v205, v205 op_sel_hi:[0,0,0]
	v_mfma_scale_f32_16x16x128_f8f6f4 v[144:147], v[24:31], v[48:55], v[144:147], v205, v205 op_sel_hi:[0,0,0]
	v_mfma_scale_f32_16x16x128_f8f6f4 v[136:139], v[16:23], v[56:63], v[136:139], v205, v205 op_sel_hi:[0,0,0]
	v_mfma_scale_f32_16x16x128_f8f6f4 v[128:131], v[24:31], v[56:63], v[128:131], v205, v205 op_sel_hi:[0,0,0]
	s_barrier
	s_setprio 0
	ds_read_b128 v[32:35], v210 offset:49152
	ds_read_b128 v[36:39], v210 offset:50176
	ds_read_b128 v[40:43], v210 offset:51200
	ds_read_b128 v[44:47], v210 offset:52224
	ds_read_b128 v[48:51], v210 offset:53248
	ds_read_b128 v[52:55], v210 offset:54272
	ds_read_b128 v[56:59], v210 offset:55296
	ds_read_b128 v[60:63], v210 offset:56320
	s_mov_b32 s42, m0
	s_mov_b32 m0, s55
	s_nop 0
	global_load_lds_dwordx4 v199, s[40:41]
	s_mov_b32 m0, s42
	s_add_u32 s40, s38, 0x10080
	s_addc_u32 s41, s39, 0
	s_mov_b32 s42, m0
	s_mov_b32 m0, s56
	s_nop 0
	global_load_lds_dwordx4 v199, s[40:41]
	s_mov_b32 m0, s42
	s_add_u32 s40, s38, 0x20080
	s_addc_u32 s41, s39, 0
	s_mov_b32 s42, m0
	s_mov_b32 m0, s59
	s_nop 0
	global_load_lds_dwordx4 v199, s[40:41]
	s_mov_b32 m0, s42
	s_add_u32 s38, s38, 0x30080
	s_addc_u32 s39, s39, 0
	s_mov_b32 s40, m0
	s_mov_b32 m0, s60
	s_nop 0
	global_load_lds_dwordx4 v199, s[38:39]
	s_mov_b32 m0, s40
	s_mov_b32 s38, m0
	s_mov_b32 m0, s57
	s_nop 0
	global_load_lds_dwordx4 v200, s[36:37]
	s_mov_b32 m0, s38
	s_nop 0
	s_mov_b32 s38, m0
	s_mov_b32 m0, s58
	s_nop 0
	global_load_lds_dwordx4 v201, s[36:37]
	s_mov_b32 m0, s38
	s_waitcnt vmcnt(8)
	s_waitcnt lgkmcnt(0)
	s_setprio 1
	s_barrier
	v_mfma_scale_f32_16x16x128_f8f6f4 v[124:127], v[0:7], v[32:39], v[124:127], v205, v205 op_sel_hi:[0,0,0]
	v_mfma_scale_f32_16x16x128_f8f6f4 v[116:119], v[8:15], v[32:39], v[116:119], v205, v205 op_sel_hi:[0,0,0]
	v_mfma_scale_f32_16x16x128_f8f6f4 v[108:111], v[0:7], v[40:47], v[108:111], v205, v205 op_sel_hi:[0,0,0]
	v_mfma_scale_f32_16x16x128_f8f6f4 v[100:103], v[8:15], v[40:47], v[100:103], v205, v205 op_sel_hi:[0,0,0]
	v_mfma_scale_f32_16x16x128_f8f6f4 v[92:95], v[0:7], v[48:55], v[92:95], v205, v205 op_sel_hi:[0,0,0]
	v_mfma_scale_f32_16x16x128_f8f6f4 v[84:87], v[8:15], v[48:55], v[84:87], v205, v205 op_sel_hi:[0,0,0]
	v_mfma_scale_f32_16x16x128_f8f6f4 v[72:75], v[0:7], v[56:63], v[72:75], v205, v205 op_sel_hi:[0,0,0]
	v_mfma_scale_f32_16x16x128_f8f6f4 v[64:67], v[8:15], v[56:63], v[64:67], v205, v205 op_sel_hi:[0,0,0]
	s_setprio 0
	s_setprio 1
	v_mfma_scale_f32_16x16x128_f8f6f4 v[120:123], v[16:23], v[32:39], v[120:123], v205, v205 op_sel_hi:[0,0,0]
	v_mfma_scale_f32_16x16x128_f8f6f4 v[112:115], v[24:31], v[32:39], v[112:115], v205, v205 op_sel_hi:[0,0,0]
	v_mfma_scale_f32_16x16x128_f8f6f4 v[104:107], v[16:23], v[40:47], v[104:107], v205, v205 op_sel_hi:[0,0,0]
	v_mfma_scale_f32_16x16x128_f8f6f4 v[96:99], v[24:31], v[40:47], v[96:99], v205, v205 op_sel_hi:[0,0,0]
	v_mfma_scale_f32_16x16x128_f8f6f4 v[88:91], v[16:23], v[48:55], v[88:91], v205, v205 op_sel_hi:[0,0,0]
	v_mfma_scale_f32_16x16x128_f8f6f4 v[80:83], v[24:31], v[48:55], v[80:83], v205, v205 op_sel_hi:[0,0,0]
	v_mfma_scale_f32_16x16x128_f8f6f4 v[76:79], v[16:23], v[56:63], v[76:79], v205, v205 op_sel_hi:[0,0,0]
	v_mfma_scale_f32_16x16x128_f8f6f4 v[68:71], v[24:31], v[56:63], v[68:71], v205, v205 op_sel_hi:[0,0,0]
	s_barrier
	s_setprio 0
	s_add_i32 s25, s25, 2
	s_add_u32 s15, s15, 0x100
	s_addc_u32 s23, s23, 0
	s_cmp_gt_u32 s25, 5
	s_cbranch_scc1 .LBB0_533

.LBB0_645:
	ds_read_b128 v[146:149], v139
	ds_read_b128 v[150:153], v139 offset:1024
	ds_read_b128 v[154:157], v139 offset:2048
	ds_read_b128 v[158:161], v139 offset:3072
	ds_read_b128 v[162:165], v140
	ds_read_b128 v[166:169], v140 offset:1024
	ds_read_b128 v[170:173], v140 offset:2048
	ds_read_b128 v[174:177], v140 offset:3072
	s_add_u32 s24, s22, 0x100
	s_addc_u32 s25, s23, 0
	s_cmp_eq_u32 s13, 4
	s_cselect_b32 s26, s16, s24
	s_cselect_b32 s27, s17, s25
	s_cselect_b32 s30, s18, s1
	s_cselect_b32 s31, s19, s11
	s_add_u32 s28, s26, 0x80
	s_addc_u32 s29, s27, 0
	ds_read_b128 v[178:181], v141
	ds_read_b128 v[182:185], v141 offset:1024
	ds_read_b128 v[186:189], v141 offset:2048
	ds_read_b128 v[190:193], v141 offset:3072
	ds_read_b128 v[194:197], v141 offset:4096
	ds_read_b128 v[198:201], v141 offset:5120
	ds_read_b128 v[202:205], v141 offset:6144
	ds_read_b128 v[206:209], v141 offset:7168
	s_add_u32 s60, s22, 0x20080
	s_addc_u32 s61, s23, 0
	s_mov_b32 s15, m0
	s_mov_b32 m0, s53
	s_nop 0
	global_load_lds_dwordx4 v137, s[60:61]
	s_mov_b32 m0, s15
	s_add_u32 s22, s22, 0x30080
	s_addc_u32 s23, s23, 0
	s_mov_b32 s15, m0
	s_mov_b32 m0, s54
	s_nop 0
	global_load_lds_dwordx4 v137, s[22:23]
	s_mov_b32 m0, s15
	s_waitcnt vmcnt(8)
	s_waitcnt lgkmcnt(0)
	s_setprio 1
	s_barrier
	v_mfma_scale_f32_16x16x128_f8f6f4 v[124:127], v[146:153], v[178:185], v[124:127], v142, v142 op_sel_hi:[0,0,0]
	v_mfma_scale_f32_16x16x128_f8f6f4 v[120:123], v[154:161], v[178:185], v[120:123], v142, v142 op_sel_hi:[0,0,0]
	v_mfma_scale_f32_16x16x128_f8f6f4 v[116:119], v[146:153], v[186:193], v[116:119], v142, v142 op_sel_hi:[0,0,0]
	v_mfma_scale_f32_16x16x128_f8f6f4 v[112:115], v[154:161], v[186:193], v[112:115], v142, v142 op_sel_hi:[0,0,0]
	v_mfma_scale_f32_16x16x128_f8f6f4 v[128:131], v[146:153], v[194:201], v[92:95], v142, v142 op_sel_hi:[0,0,0]
	v_mfma_scale_f32_16x16x128_f8f6f4 v[210:213], v[154:161], v[194:201], v[88:91], v142, v142 op_sel_hi:[0,0,0]
	v_mfma_scale_f32_16x16x128_f8f6f4 v[214:217], v[146:153], v[202:209], v[84:87], v142, v142 op_sel_hi:[0,0,0]
	v_mfma_scale_f32_16x16x128_f8f6f4 v[218:221], v[154:161], v[202:209], v[80:83], v142, v142 op_sel_hi:[0,0,0]
	s_setprio 0
	s_setprio 1
	v_mfma_scale_f32_16x16x128_f8f6f4 v[108:111], v[162:169], v[178:185], v[108:111], v142, v142 op_sel_hi:[0,0,0]
	v_mfma_scale_f32_16x16x128_f8f6f4 v[104:107], v[170:177], v[178:185], v[104:107], v142, v142 op_sel_hi:[0,0,0]
	v_mfma_scale_f32_16x16x128_f8f6f4 v[100:103], v[162:169], v[186:193], v[100:103], v142, v142 op_sel_hi:[0,0,0]
	v_mfma_scale_f32_16x16x128_f8f6f4 v[96:99], v[170:177], v[186:193], v[96:99], v142, v142 op_sel_hi:[0,0,0]
	v_mfma_scale_f32_16x16x128_f8f6f4 v[178:181], v[162:169], v[194:201], v[76:79], v142, v142 op_sel_hi:[0,0,0]
	v_mfma_scale_f32_16x16x128_f8f6f4 v[182:185], v[170:177], v[194:201], v[72:75], v142, v142 op_sel_hi:[0,0,0]
	v_mfma_scale_f32_16x16x128_f8f6f4 v[186:189], v[162:169], v[202:209], v[68:71], v142, v142 op_sel_hi:[0,0,0]
	v_mfma_scale_f32_16x16x128_f8f6f4 v[190:193], v[170:177], v[202:209], v[64:67], v142, v142 op_sel_hi:[0,0,0]
	s_barrier
	s_setprio 0
	s_add_u32 s22, s30, 0x10000
	s_nop 3
	ds_read_b128 v[64:67], v141 offset:16384
	ds_read_b128 v[68:71], v141 offset:17408
	ds_read_b128 v[72:75], v141 offset:18432
	ds_read_b128 v[76:79], v141 offset:19456
	ds_read_b128 v[80:83], v141 offset:20480
	ds_read_b128 v[84:87], v141 offset:21504
	ds_read_b128 v[88:91], v141 offset:22528
	ds_read_b128 v[92:95], v141 offset:23552
	s_mov_b32 s15, m0
	s_mov_b32 m0, s36
	s_nop 0
	global_load_lds_dwordx4 v136, s[30:31]
	s_mov_b32 m0, s15
	s_addc_u32 s23, s31, 0
	s_mov_b32 s15, m0
	s_mov_b32 m0, s37
	s_nop 0
	global_load_lds_dwordx4 v136, s[22:23]
	s_mov_b32 m0, s15
	s_add_u32 s22, s30, 0x20000
	s_addc_u32 s23, s31, 0
	s_mov_b32 s15, m0
	s_mov_b32 m0, s38
	s_nop 0
	global_load_lds_dwordx4 v136, s[22:23]
	s_mov_b32 m0, s15
	s_add_u32 s22, s30, 0x30000
	s_addc_u32 s23, s31, 0
	s_mov_b32 s15, m0
	s_mov_b32 m0, s39
	s_nop 0
	global_load_lds_dwordx4 v136, s[22:23]
	s_mov_b32 m0, s15
	s_add_u32 s22, s26, 0x10000
	s_mov_b32 s15, m0
	s_mov_b32 m0, s35
	s_nop 0
	global_load_lds_dwordx4 v137, s[26:27]
	s_mov_b32 m0, s15
	s_addc_u32 s23, s27, 0
	s_mov_b32 s15, m0
	s_mov_b32 m0, s40
	s_nop 0
	global_load_lds_dwordx4 v137, s[22:23]
	s_mov_b32 m0, s15
	s_waitcnt vmcnt(8)
	s_waitcnt lgkmcnt(0)
	s_setprio 1
	s_barrier
	v_mfma_scale_f32_16x16x128_f8f6f4 v[60:63], v[146:153], v[64:71], v[60:63], v142, v142 op_sel_hi:[0,0,0]
	v_mfma_scale_f32_16x16x128_f8f6f4 v[56:59], v[154:161], v[64:71], v[56:59], v142, v142 op_sel_hi:[0,0,0]
	v_mfma_scale_f32_16x16x128_f8f6f4 v[52:55], v[146:153], v[72:79], v[52:55], v142, v142 op_sel_hi:[0,0,0]
	v_mfma_scale_f32_16x16x128_f8f6f4 v[48:51], v[154:161], v[72:79], v[48:51], v142, v142 op_sel_hi:[0,0,0]
	v_mfma_scale_f32_16x16x128_f8f6f4 v[194:197], v[146:153], v[80:87], v[28:31], v142, v142 op_sel_hi:[0,0,0]
	v_mfma_scale_f32_16x16x128_f8f6f4 v[198:201], v[154:161], v[80:87], v[24:27], v142, v142 op_sel_hi:[0,0,0]
	v_mfma_scale_f32_16x16x128_f8f6f4 v[202:205], v[146:153], v[88:95], v[12:15], v142, v142 op_sel_hi:[0,0,0]
	v_mfma_scale_f32_16x16x128_f8f6f4 v[206:209], v[154:161], v[88:95], v[8:11], v142, v142 op_sel_hi:[0,0,0]
	s_setprio 0
	s_setprio 1
	v_mfma_scale_f32_16x16x128_f8f6f4 v[222:225], v[162:169], v[64:71], v[44:47], v142, v142 op_sel_hi:[0,0,0]
	v_mfma_scale_f32_16x16x128_f8f6f4 v[226:229], v[170:177], v[64:71], v[40:43], v142, v142 op_sel_hi:[0,0,0]
	v_mfma_scale_f32_16x16x128_f8f6f4 v[230:233], v[162:169], v[72:79], v[36:39], v142, v142 op_sel_hi:[0,0,0]
	v_mfma_scale_f32_16x16x128_f8f6f4 v[234:237], v[170:177], v[72:79], v[32:35], v142, v142 op_sel_hi:[0,0,0]
	v_mfma_scale_f32_16x16x128_f8f6f4 v[238:241], v[162:169], v[80:87], v[20:23], v142, v142 op_sel_hi:[0,0,0]
	v_mfma_scale_f32_16x16x128_f8f6f4 v[242:245], v[170:177], v[80:87], v[16:19], v142, v142 op_sel_hi:[0,0,0]
	v_mfma_scale_f32_16x16x128_f8f6f4 v[246:249], v[162:169], v[88:95], v[4:7], v142, v142 op_sel_hi:[0,0,0]
	v_mfma_scale_f32_16x16x128_f8f6f4 v[250:253], v[170:177], v[88:95], v[0:3], v142, v142 op_sel_hi:[0,0,0]
	s_barrier
	s_setprio 0
	s_nop 4
	ds_read_b128 v[0:3], v143
	ds_read_b128 v[4:7], v143 offset:1024
	ds_read_b128 v[16:19], v143 offset:2048
	ds_read_b128 v[20:23], v143 offset:3072
	ds_read_b128 v[146:149], v144
	ds_read_b128 v[150:153], v144 offset:1024
	ds_read_b128 v[154:157], v144 offset:2048
	ds_read_b128 v[158:161], v144 offset:3072
	ds_read_b128 v[8:11], v141 offset:32768
	ds_read_b128 v[12:15], v141 offset:33792
	ds_read_b128 v[24:27], v141 offset:34816
	ds_read_b128 v[28:31], v141 offset:35840
	ds_read_b128 v[32:35], v141 offset:36864
	ds_read_b128 v[36:39], v141 offset:37888
	ds_read_b128 v[40:43], v141 offset:38912
	ds_read_b128 v[44:47], v141 offset:39936
	s_add_u32 s22, s26, 0x20000
	s_addc_u32 s23, s27, 0
	s_mov_b32 s15, m0
	s_mov_b32 m0, s41
	s_nop 0
	global_load_lds_dwordx4 v137, s[22:23]
	s_mov_b32 m0, s15
	s_add_u32 s22, s26, 0x30000
	s_addc_u32 s23, s27, 0
	s_mov_b32 s15, m0
	s_mov_b32 m0, s42
	s_nop 0
	global_load_lds_dwordx4 v137, s[22:23]
	s_mov_b32 m0, s15
	s_waitcnt vmcnt(8)
	s_waitcnt lgkmcnt(0)
	s_setprio 1
	s_barrier
	v_mfma_scale_f32_16x16x128_f8f6f4 v[124:127], v[0:7], v[8:15], v[124:127], v142, v142 op_sel_hi:[0,0,0]
	v_mfma_scale_f32_16x16x128_f8f6f4 v[120:123], v[16:23], v[8:15], v[120:123], v142, v142 op_sel_hi:[0,0,0]
	v_mfma_scale_f32_16x16x128_f8f6f4 v[116:119], v[0:7], v[24:31], v[116:119], v142, v142 op_sel_hi:[0,0,0]
	v_mfma_scale_f32_16x16x128_f8f6f4 v[112:115], v[16:23], v[24:31], v[112:115], v142, v142 op_sel_hi:[0,0,0]
	v_mfma_scale_f32_16x16x128_f8f6f4 v[92:95], v[0:7], v[32:39], v[128:131], v142, v142 op_sel_hi:[0,0,0]
	v_mfma_scale_f32_16x16x128_f8f6f4 v[88:91], v[16:23], v[32:39], v[210:213], v142, v142 op_sel_hi:[0,0,0]
	v_mfma_scale_f32_16x16x128_f8f6f4 v[84:87], v[0:7], v[40:47], v[214:217], v142, v142 op_sel_hi:[0,0,0]
	v_mfma_scale_f32_16x16x128_f8f6f4 v[80:83], v[16:23], v[40:47], v[218:221], v142, v142 op_sel_hi:[0,0,0]
	s_setprio 0
	s_setprio 1
	v_mfma_scale_f32_16x16x128_f8f6f4 v[108:111], v[146:153], v[8:15], v[108:111], v142, v142 op_sel_hi:[0,0,0]
	v_mfma_scale_f32_16x16x128_f8f6f4 v[104:107], v[154:161], v[8:15], v[104:107], v142, v142 op_sel_hi:[0,0,0]
	v_mfma_scale_f32_16x16x128_f8f6f4 v[100:103], v[146:153], v[24:31], v[100:103], v142, v142 op_sel_hi:[0,0,0]
	v_mfma_scale_f32_16x16x128_f8f6f4 v[96:99], v[154:161], v[24:31], v[96:99], v142, v142 op_sel_hi:[0,0,0]
	v_mfma_scale_f32_16x16x128_f8f6f4 v[76:79], v[146:153], v[32:39], v[178:181], v142, v142 op_sel_hi:[0,0,0]
	v_mfma_scale_f32_16x16x128_f8f6f4 v[72:75], v[154:161], v[32:39], v[182:185], v142, v142 op_sel_hi:[0,0,0]
	v_mfma_scale_f32_16x16x128_f8f6f4 v[68:71], v[146:153], v[40:47], v[186:189], v142, v142 op_sel_hi:[0,0,0]
	v_mfma_scale_f32_16x16x128_f8f6f4 v[64:67], v[154:161], v[40:47], v[190:193], v142, v142 op_sel_hi:[0,0,0]
	s_barrier
	s_setprio 0
	s_add_u32 s22, s30, 0x80
	s_addc_u32 s23, s31, 0
	ds_read_b128 v[32:35], v141 offset:49152
	ds_read_b128 v[36:39], v141 offset:50176
	ds_read_b128 v[162:165], v141 offset:51200
	ds_read_b128 v[166:169], v141 offset:52224
	ds_read_b128 v[170:173], v141 offset:53248
	ds_read_b128 v[174:177], v141 offset:54272
	ds_read_b128 v[178:181], v141 offset:55296
	ds_read_b128 v[182:185], v141 offset:56320
	s_mov_b32 s15, m0
	s_mov_b32 m0, s45
	s_nop 0
	global_load_lds_dwordx4 v136, s[22:23]
	s_mov_b32 m0, s15
	s_add_u32 s22, s30, 0x10080
	s_addc_u32 s23, s31, 0
	s_mov_b32 s15, m0
	s_mov_b32 m0, s47
	s_nop 0
	global_load_lds_dwordx4 v136, s[22:23]
	s_mov_b32 m0, s15
	s_add_u32 s22, s30, 0x20080
	s_addc_u32 s23, s31, 0
	s_mov_b32 s15, m0
	s_mov_b32 m0, s50
	s_nop 0
	global_load_lds_dwordx4 v136, s[22:23]
	s_mov_b32 m0, s15
	s_add_u32 s22, s30, 0x30080
	s_addc_u32 s23, s31, 0
	s_mov_b32 s15, m0
	s_mov_b32 m0, s51
	s_nop 0
	global_load_lds_dwordx4 v136, s[22:23]
	s_mov_b32 m0, s15
	s_add_u32 s22, s26, 0x10080
	s_mov_b32 s15, m0
	s_mov_b32 m0, s48
	s_nop 0
	global_load_lds_dwordx4 v137, s[28:29]
	s_mov_b32 m0, s15
	s_addc_u32 s23, s27, 0
	s_mov_b32 s15, m0
	s_mov_b32 m0, s49
	s_nop 0
	global_load_lds_dwordx4 v137, s[22:23]
	s_mov_b32 m0, s15
	s_waitcnt vmcnt(8)
	s_waitcnt lgkmcnt(0)
	s_setprio 1
	s_barrier
	v_mfma_scale_f32_16x16x128_f8f6f4 v[60:63], v[0:7], v[32:39], v[60:63], v142, v142 op_sel_hi:[0,0,0]
	v_mfma_scale_f32_16x16x128_f8f6f4 v[56:59], v[16:23], v[32:39], v[56:59], v142, v142 op_sel_hi:[0,0,0]
	v_mfma_scale_f32_16x16x128_f8f6f4 v[52:55], v[0:7], v[162:169], v[52:55], v142, v142 op_sel_hi:[0,0,0]
	v_mfma_scale_f32_16x16x128_f8f6f4 v[48:51], v[16:23], v[162:169], v[48:51], v142, v142 op_sel_hi:[0,0,0]
	v_mfma_scale_f32_16x16x128_f8f6f4 v[28:31], v[0:7], v[170:177], v[194:197], v142, v142 op_sel_hi:[0,0,0]
	v_mfma_scale_f32_16x16x128_f8f6f4 v[24:27], v[16:23], v[170:177], v[198:201], v142, v142 op_sel_hi:[0,0,0]
	v_mfma_scale_f32_16x16x128_f8f6f4 v[12:15], v[0:7], v[178:185], v[202:205], v142, v142 op_sel_hi:[0,0,0]
	v_mfma_scale_f32_16x16x128_f8f6f4 v[8:11], v[16:23], v[178:185], v[206:209], v142, v142 op_sel_hi:[0,0,0]
	s_setprio 0
	s_setprio 1
	v_mfma_scale_f32_16x16x128_f8f6f4 v[44:47], v[146:153], v[32:39], v[222:225], v142, v142 op_sel_hi:[0,0,0]
	v_mfma_scale_f32_16x16x128_f8f6f4 v[40:43], v[154:161], v[32:39], v[226:229], v142, v142 op_sel_hi:[0,0,0]
	v_mfma_scale_f32_16x16x128_f8f6f4 v[36:39], v[146:153], v[162:169], v[230:233], v142, v142 op_sel_hi:[0,0,0]
	v_mfma_scale_f32_16x16x128_f8f6f4 v[32:35], v[154:161], v[162:169], v[234:237], v142, v142 op_sel_hi:[0,0,0]
	v_mfma_scale_f32_16x16x128_f8f6f4 v[20:23], v[146:153], v[170:177], v[238:241], v142, v142 op_sel_hi:[0,0,0]
	v_mfma_scale_f32_16x16x128_f8f6f4 v[16:19], v[154:161], v[170:177], v[242:245], v142, v142 op_sel_hi:[0,0,0]
	v_mfma_scale_f32_16x16x128_f8f6f4 v[4:7], v[146:153], v[178:185], v[246:249], v142, v142 op_sel_hi:[0,0,0]
	v_mfma_scale_f32_16x16x128_f8f6f4 v[0:3], v[154:161], v[178:185], v[250:253], v142, v142 op_sel_hi:[0,0,0]
	s_barrier
	s_setprio 0
	s_add_i32 s13, s13, 2
	s_add_u32 s1, s1, 0x100
	s_addc_u32 s11, s11, 0
	s_cmp_gt_u32 s13, 5
	s_mov_b64 s[22:23], s[24:25]
	s_cbranch_scc0 .LBB0_645
	s_and_b64 vcc, exec, s[8:9]
	s_cbranch_vccz .LBB0_648
	s_barrier

.LBB0_799:
	s_ashr_i32 s7, s6, 31
	s_lshl_b64 s[10:11], s[6:7], 18
	s_add_u32 s10, s33, s10
	s_addc_u32 s11, s34, s11
	s_and_b64 s[14:15], s[12:13], exec
	ds_read_b128 v[0:3], v135
	ds_read_b128 v[4:7], v135 offset:1024
	ds_read_b128 v[8:11], v135 offset:2048
	ds_read_b128 v[12:15], v135 offset:3072
	ds_read_b128 v[16:19], v136
	ds_read_b128 v[20:23], v136 offset:1024
	ds_read_b128 v[24:27], v136 offset:2048
	ds_read_b128 v[28:31], v136 offset:3072
	s_cselect_b32 s7, s11, s23
	s_cselect_b32 s53, s10, s22
	s_ashr_i32 s9, s8, 31
	s_lshl_b64 s[14:15], s[8:9], 18
	s_add_u32 s14, s30, s14
	s_addc_u32 s15, s31, s15
	s_and_b64 s[24:25], s[12:13], exec
	s_cselect_b32 s9, s15, s21
	s_cselect_b32 s54, s14, s20
	s_add_u32 s24, s22, 0x100
	s_addc_u32 s25, s23, 0
	s_add_u32 s26, s22, 0x180
	s_addc_u32 s27, s23, 0
	s_add_u32 s28, s20, 0x100
	s_addc_u32 s29, s21, 0
	ds_read_b128 v[32:35], v137
	ds_read_b128 v[36:39], v137 offset:1024
	ds_read_b128 v[40:43], v137 offset:2048
	ds_read_b128 v[44:47], v137 offset:3072
	ds_read_b128 v[48:51], v137 offset:4096
	ds_read_b128 v[52:55], v137 offset:5120
	ds_read_b128 v[56:59], v137 offset:6144
	ds_read_b128 v[60:63], v137 offset:7168
	s_add_u32 s56, s22, 0x20080
	s_addc_u32 s57, s23, 0
	s_mov_b32 s55, m0
	s_mov_b32 m0, s50
	s_nop 0
	global_load_lds_dwordx4 v134, s[56:57]
	s_mov_b32 m0, s55
	s_add_u32 s56, s22, 0x30080
	s_addc_u32 s57, s23, 0
	s_mov_b32 s55, m0
	s_mov_b32 m0, s51
	s_nop 0
	global_load_lds_dwordx4 v134, s[56:57]
	s_mov_b32 m0, s55
	s_waitcnt vmcnt(8)
	s_waitcnt lgkmcnt(0)
	s_setprio 1
	s_barrier
	v_mfma_scale_f32_16x16x128_f8f6f4 v[64:67], v[0:7], v[32:39], 0, v138, v138 op_sel_hi:[0,0,0]
	v_mfma_scale_f32_16x16x128_f8f6f4 v[68:71], v[8:15], v[32:39], 0, v138, v138 op_sel_hi:[0,0,0]
	v_mfma_scale_f32_16x16x128_f8f6f4 v[72:75], v[0:7], v[40:47], 0, v138, v138 op_sel_hi:[0,0,0]
	v_mfma_scale_f32_16x16x128_f8f6f4 v[76:79], v[8:15], v[40:47], 0, v138, v138 op_sel_hi:[0,0,0]
	v_mfma_scale_f32_16x16x128_f8f6f4 v[80:83], v[0:7], v[48:55], 0, v138, v138 op_sel_hi:[0,0,0]
	v_mfma_scale_f32_16x16x128_f8f6f4 v[88:91], v[8:15], v[48:55], 0, v138, v138 op_sel_hi:[0,0,0]
	v_mfma_scale_f32_16x16x128_f8f6f4 v[108:111], v[0:7], v[56:63], 0, v138, v138 op_sel_hi:[0,0,0]
	v_mfma_scale_f32_16x16x128_f8f6f4 v[116:119], v[8:15], v[56:63], 0, v138, v138 op_sel_hi:[0,0,0]
	s_setprio 0
	s_setprio 1
	v_mfma_scale_f32_16x16x128_f8f6f4 v[120:123], v[16:23], v[32:39], 0, v138, v138 op_sel_hi:[0,0,0]
	v_mfma_scale_f32_16x16x128_f8f6f4 v[124:127], v[24:31], v[32:39], 0, v138, v138 op_sel_hi:[0,0,0]
	v_mfma_scale_f32_16x16x128_f8f6f4 v[128:131], v[16:23], v[40:47], 0, v138, v138 op_sel_hi:[0,0,0]
	v_mfma_scale_f32_16x16x128_f8f6f4 v[158:161], v[24:31], v[40:47], 0, v138, v138 op_sel_hi:[0,0,0]
	v_mfma_scale_f32_16x16x128_f8f6f4 v[162:165], v[16:23], v[48:55], 0, v138, v138 op_sel_hi:[0,0,0]
	v_mfma_scale_f32_16x16x128_f8f6f4 v[166:169], v[24:31], v[48:55], 0, v138, v138 op_sel_hi:[0,0,0]
	v_mfma_scale_f32_16x16x128_f8f6f4 v[170:173], v[16:23], v[56:63], 0, v138, v138 op_sel_hi:[0,0,0]
	v_mfma_scale_f32_16x16x128_f8f6f4 v[174:177], v[24:31], v[56:63], 0, v138, v138 op_sel_hi:[0,0,0]
	s_barrier
	s_setprio 0
	ds_read_b128 v[32:35], v137 offset:16384
	ds_read_b128 v[36:39], v137 offset:17408
	ds_read_b128 v[40:43], v137 offset:18432
	ds_read_b128 v[44:47], v137 offset:19456
	ds_read_b128 v[48:51], v137 offset:20480
	ds_read_b128 v[52:55], v137 offset:21504
	ds_read_b128 v[56:59], v137 offset:22528
	ds_read_b128 v[60:63], v137 offset:23552
	s_mov_b32 s55, m0
	s_mov_b32 m0, s17
	s_nop 0
	global_load_lds_dwordx4 v133, s[28:29]
	s_mov_b32 m0, s55
	s_add_u32 s28, s20, 0x10100
	s_addc_u32 s29, s21, 0
	s_mov_b32 s55, m0
	s_mov_b32 m0, s19
	s_nop 0
	global_load_lds_dwordx4 v133, s[28:29]
	s_mov_b32 m0, s55
	s_add_u32 s28, s20, 0x20100
	s_addc_u32 s29, s21, 0
	s_mov_b32 s55, m0
	s_mov_b32 m0, s36
	s_nop 0
	global_load_lds_dwordx4 v133, s[28:29]
	s_mov_b32 m0, s55
	s_add_u32 s28, s20, 0x30100
	s_addc_u32 s29, s21, 0
	s_mov_b32 s55, m0
	s_mov_b32 m0, s37
	s_nop 0
	global_load_lds_dwordx4 v133, s[28:29]
	s_mov_b32 m0, s55
	s_mov_b32 s28, m0
	s_mov_b32 m0, s35
	s_nop 0
	global_load_lds_dwordx4 v134, s[24:25]
	s_mov_b32 m0, s28
	s_add_u32 s28, s22, 0x10100
	s_addc_u32 s29, s23, 0
	s_mov_b32 s55, m0
	s_mov_b32 m0, s38
	s_nop 0
	global_load_lds_dwordx4 v134, s[28:29]
	s_mov_b32 m0, s55
	s_waitcnt vmcnt(8)
	s_waitcnt lgkmcnt(0)
	s_setprio 1
	s_barrier
	v_mfma_scale_f32_16x16x128_f8f6f4 v[190:193], v[0:7], v[32:39], 0, v138, v138 op_sel_hi:[0,0,0]
	v_mfma_scale_f32_16x16x128_f8f6f4 v[194:197], v[8:15], v[32:39], 0, v138, v138 op_sel_hi:[0,0,0]
	v_mfma_scale_f32_16x16x128_f8f6f4 v[198:201], v[0:7], v[40:47], 0, v138, v138 op_sel_hi:[0,0,0]
	v_mfma_scale_f32_16x16x128_f8f6f4 v[202:205], v[8:15], v[40:47], 0, v138, v138 op_sel_hi:[0,0,0]
	v_mfma_scale_f32_16x16x128_f8f6f4 v[206:209], v[0:7], v[48:55], 0, v138, v138 op_sel_hi:[0,0,0]
	v_mfma_scale_f32_16x16x128_f8f6f4 v[210:213], v[8:15], v[48:55], 0, v138, v138 op_sel_hi:[0,0,0]
	v_mfma_scale_f32_16x16x128_f8f6f4 v[214:217], v[0:7], v[56:63], 0, v138, v138 op_sel_hi:[0,0,0]
	v_mfma_scale_f32_16x16x128_f8f6f4 v[218:221], v[8:15], v[56:63], 0, v138, v138 op_sel_hi:[0,0,0]
	s_setprio 0
	s_setprio 1
	v_mfma_scale_f32_16x16x128_f8f6f4 v[222:225], v[16:23], v[32:39], 0, v138, v138 op_sel_hi:[0,0,0]
	v_mfma_scale_f32_16x16x128_f8f6f4 v[226:229], v[24:31], v[32:39], 0, v138, v138 op_sel_hi:[0,0,0]
	v_mfma_scale_f32_16x16x128_f8f6f4 v[230:233], v[16:23], v[40:47], 0, v138, v138 op_sel_hi:[0,0,0]
	v_mfma_scale_f32_16x16x128_f8f6f4 v[234:237], v[24:31], v[40:47], 0, v138, v138 op_sel_hi:[0,0,0]
	v_mfma_scale_f32_16x16x128_f8f6f4 v[238:241], v[16:23], v[48:55], 0, v138, v138 op_sel_hi:[0,0,0]
	v_mfma_scale_f32_16x16x128_f8f6f4 v[242:245], v[24:31], v[48:55], 0, v138, v138 op_sel_hi:[0,0,0]
	v_mfma_scale_f32_16x16x128_f8f6f4 v[246:249], v[16:23], v[56:63], 0, v138, v138 op_sel_hi:[0,0,0]
	v_mfma_scale_f32_16x16x128_f8f6f4 v[250:253], v[24:31], v[56:63], 0, v138, v138 op_sel_hi:[0,0,0]
	s_barrier
	s_setprio 0
	ds_read_b128 v[0:3], v139
	ds_read_b128 v[4:7], v139 offset:1024
	ds_read_b128 v[96:99], v139 offset:2048
	ds_read_b128 v[100:103], v139 offset:3072
	ds_read_b128 v[142:145], v140
	ds_read_b128 v[146:149], v140 offset:1024
	ds_read_b128 v[150:153], v140 offset:2048
	ds_read_b128 v[154:157], v140 offset:3072
	ds_read_b128 v[8:11], v137 offset:32768
	ds_read_b128 v[12:15], v137 offset:33792
	ds_read_b128 v[16:19], v137 offset:34816
	ds_read_b128 v[20:23], v137 offset:35840
	ds_read_b128 v[28:31], v137 offset:36864
	ds_read_b128 v[32:35], v137 offset:37888
	ds_read_b128 v[56:59], v137 offset:38912
	ds_read_b128 v[60:63], v137 offset:39936
	s_add_u32 s28, s22, 0x20100
	s_addc_u32 s29, s23, 0
	s_mov_b32 s55, m0
	s_mov_b32 m0, s39
	s_nop 0
	global_load_lds_dwordx4 v134, s[28:29]
	s_mov_b32 m0, s55
	s_add_u32 s28, s22, 0x30100
	s_addc_u32 s29, s23, 0
	s_mov_b32 s55, m0
	s_mov_b32 m0, s40
	s_nop 0
	global_load_lds_dwordx4 v134, s[28:29]
	s_mov_b32 m0, s55
	s_waitcnt vmcnt(8)
	s_waitcnt lgkmcnt(0)
	s_setprio 1
	s_barrier
	v_mfma_scale_f32_16x16x128_f8f6f4 v[104:107], v[0:7], v[8:15], v[64:67], v138, v138 op_sel_hi:[0,0,0]
	v_mfma_scale_f32_16x16x128_f8f6f4 v[112:115], v[96:103], v[8:15], v[68:71], v138, v138 op_sel_hi:[0,0,0]
	v_mfma_scale_f32_16x16x128_f8f6f4 v[92:95], v[0:7], v[16:23], v[72:75], v138, v138 op_sel_hi:[0,0,0]
	v_mfma_scale_f32_16x16x128_f8f6f4 v[84:87], v[96:103], v[16:23], v[76:79], v138, v138 op_sel_hi:[0,0,0]
	v_mfma_scale_f32_16x16x128_f8f6f4 v[64:67], v[0:7], v[28:35], v[80:83], v138, v138 op_sel_hi:[0,0,0]
	v_mfma_scale_f32_16x16x128_f8f6f4 v[52:55], v[96:103], v[28:35], v[88:91], v138, v138 op_sel_hi:[0,0,0]
	v_mfma_scale_f32_16x16x128_f8f6f4 v[36:39], v[0:7], v[56:63], v[108:111], v138, v138 op_sel_hi:[0,0,0]
	v_mfma_scale_f32_16x16x128_f8f6f4 v[24:27], v[96:103], v[56:63], v[116:119], v138, v138 op_sel_hi:[0,0,0]
	s_setprio 0
	s_setprio 1
	v_mfma_scale_f32_16x16x128_f8f6f4 v[120:123], v[142:149], v[8:15], v[120:123], v138, v138 op_sel_hi:[0,0,0]
	v_mfma_scale_f32_16x16x128_f8f6f4 v[124:127], v[150:157], v[8:15], v[124:127], v138, v138 op_sel_hi:[0,0,0]
	v_mfma_scale_f32_16x16x128_f8f6f4 v[116:119], v[142:149], v[16:23], v[128:131], v138, v138 op_sel_hi:[0,0,0]
	v_mfma_scale_f32_16x16x128_f8f6f4 v[108:111], v[150:157], v[16:23], v[158:161], v138, v138 op_sel_hi:[0,0,0]
	v_mfma_scale_f32_16x16x128_f8f6f4 v[76:79], v[142:149], v[28:35], v[162:165], v138, v138 op_sel_hi:[0,0,0]
	v_mfma_scale_f32_16x16x128_f8f6f4 v[72:75], v[150:157], v[28:35], v[166:169], v138, v138 op_sel_hi:[0,0,0]
	v_mfma_scale_f32_16x16x128_f8f6f4 v[44:47], v[142:149], v[56:63], v[170:173], v138, v138 op_sel_hi:[0,0,0]
	v_mfma_scale_f32_16x16x128_f8f6f4 v[40:43], v[150:157], v[56:63], v[174:177], v138, v138 op_sel_hi:[0,0,0]
	s_barrier
	s_setprio 0
	s_add_u32 s28, s20, 0x180
	s_addc_u32 s29, s21, 0
	ds_read_b128 v[158:161], v137 offset:49152
	ds_read_b128 v[162:165], v137 offset:50176
	ds_read_b128 v[166:169], v137 offset:51200
	ds_read_b128 v[170:173], v137 offset:52224
	ds_read_b128 v[174:177], v137 offset:53248
	ds_read_b128 v[178:181], v137 offset:54272
	ds_read_b128 v[182:185], v137 offset:55296
	ds_read_b128 v[186:189], v137 offset:56320
	s_mov_b32 s55, m0
	s_mov_b32 m0, s44
	s_nop 0
	global_load_lds_dwordx4 v133, s[28:29]
	s_mov_b32 m0, s55
	s_add_u32 s28, s20, 0x10180
	s_addc_u32 s29, s21, 0
	s_mov_b32 s55, m0
	s_mov_b32 m0, s45
	s_nop 0
	global_load_lds_dwordx4 v133, s[28:29]
	s_mov_b32 m0, s55
	s_add_u32 s28, s20, 0x20180
	s_addc_u32 s29, s21, 0
	s_mov_b32 s55, m0
	s_mov_b32 m0, s48
	s_nop 0
	global_load_lds_dwordx4 v133, s[28:29]
	s_mov_b32 m0, s55
	s_add_u32 s28, s20, 0x30180
	s_addc_u32 s29, s21, 0
	s_mov_b32 s55, m0
	s_mov_b32 m0, s49
	s_nop 0
	global_load_lds_dwordx4 v133, s[28:29]
	s_mov_b32 m0, s55
	s_mov_b32 s28, m0
	s_mov_b32 m0, s46
	s_nop 0
	global_load_lds_dwordx4 v134, s[26:27]
	s_mov_b32 m0, s28
	s_add_u32 s22, s22, 0x10180
	s_addc_u32 s23, s23, 0
	s_mov_b32 s26, m0
	s_mov_b32 m0, s47
	s_nop 0
	global_load_lds_dwordx4 v134, s[22:23]
	s_mov_b32 m0, s26
	s_waitcnt vmcnt(8)
	s_waitcnt lgkmcnt(0)
	s_setprio 1
	s_barrier
	v_mfma_scale_f32_16x16x128_f8f6f4 v[88:91], v[0:7], v[158:165], v[190:193], v138, v138 op_sel_hi:[0,0,0]
	v_mfma_scale_f32_16x16x128_f8f6f4 v[80:83], v[96:103], v[158:165], v[194:197], v138, v138 op_sel_hi:[0,0,0]
	v_mfma_scale_f32_16x16x128_f8f6f4 v[56:59], v[0:7], v[166:173], v[198:201], v138, v138 op_sel_hi:[0,0,0]
	v_mfma_scale_f32_16x16x128_f8f6f4 v[48:51], v[96:103], v[166:173], v[202:205], v138, v138 op_sel_hi:[0,0,0]
	v_mfma_scale_f32_16x16x128_f8f6f4 v[28:31], v[0:7], v[174:181], v[206:209], v138, v138 op_sel_hi:[0,0,0]
	v_mfma_scale_f32_16x16x128_f8f6f4 v[16:19], v[96:103], v[174:181], v[210:213], v138, v138 op_sel_hi:[0,0,0]
	v_mfma_scale_f32_16x16x128_f8f6f4 v[12:15], v[0:7], v[182:189], v[214:217], v138, v138 op_sel_hi:[0,0,0]
	v_mfma_scale_f32_16x16x128_f8f6f4 v[8:11], v[96:103], v[182:189], v[218:221], v138, v138 op_sel_hi:[0,0,0]
	s_setprio 0
	s_setprio 1
	v_mfma_scale_f32_16x16x128_f8f6f4 v[100:103], v[142:149], v[158:165], v[222:225], v138, v138 op_sel_hi:[0,0,0]
	v_mfma_scale_f32_16x16x128_f8f6f4 v[96:99], v[150:157], v[158:165], v[226:229], v138, v138 op_sel_hi:[0,0,0]
	v_mfma_scale_f32_16x16x128_f8f6f4 v[68:71], v[142:149], v[166:173], v[230:233], v138, v138 op_sel_hi:[0,0,0]
	v_mfma_scale_f32_16x16x128_f8f6f4 v[60:63], v[150:157], v[166:173], v[234:237], v138, v138 op_sel_hi:[0,0,0]
	v_mfma_scale_f32_16x16x128_f8f6f4 v[32:35], v[142:149], v[174:181], v[238:241], v138, v138 op_sel_hi:[0,0,0]
	v_mfma_scale_f32_16x16x128_f8f6f4 v[20:23], v[150:157], v[174:181], v[242:245], v138, v138 op_sel_hi:[0,0,0]
	v_mfma_scale_f32_16x16x128_f8f6f4 v[4:7], v[142:149], v[182:189], v[246:249], v138, v138 op_sel_hi:[0,0,0]
	v_mfma_scale_f32_16x16x128_f8f6f4 v[0:3], v[150:157], v[182:189], v[250:253], v138, v138 op_sel_hi:[0,0,0]
	s_barrier
	s_setprio 0
	s_add_u32 s55, s20, 0x200
	s_addc_u32 s56, s21, 0
	s_mov_b32 s57, 0
.LBB0_800:
	ds_read_b128 v[142:145], v135
	ds_read_b128 v[146:149], v135 offset:1024
	ds_read_b128 v[150:153], v135 offset:2048
	ds_read_b128 v[154:157], v135 offset:3072
	ds_read_b128 v[158:161], v136
	ds_read_b128 v[162:165], v136 offset:1024
	ds_read_b128 v[166:169], v136 offset:2048
	ds_read_b128 v[170:173], v136 offset:3072
	s_add_u32 s20, s24, 0x100
	s_addc_u32 s21, s25, 0
	s_cmp_eq_u32 s57, 4
	s_cselect_b32 s22, s53, s20
	s_cselect_b32 s23, s7, s21
	s_cselect_b32 s28, s54, s55
	s_cselect_b32 s29, s9, s56
	s_add_u32 s26, s22, 0x80
	s_addc_u32 s27, s23, 0
	ds_read_b128 v[174:177], v137
	ds_read_b128 v[178:181], v137 offset:1024
	ds_read_b128 v[182:185], v137 offset:2048
	ds_read_b128 v[186:189], v137 offset:3072
	ds_read_b128 v[190:193], v137 offset:4096
	ds_read_b128 v[194:197], v137 offset:5120
	ds_read_b128 v[198:201], v137 offset:6144
	ds_read_b128 v[202:205], v137 offset:7168
	s_add_u32 s58, s24, 0x20080
	s_addc_u32 s59, s25, 0
	s_mov_b32 s60, m0
	s_mov_b32 m0, s50
	s_nop 0
	global_load_lds_dwordx4 v134, s[58:59]
	s_mov_b32 m0, s60
	s_add_u32 s24, s24, 0x30080
	s_addc_u32 s25, s25, 0
	s_mov_b32 s58, m0
	s_mov_b32 m0, s51
	s_nop 0
	global_load_lds_dwordx4 v134, s[24:25]
	s_mov_b32 m0, s58
	s_waitcnt vmcnt(8)
	s_waitcnt lgkmcnt(0)
	s_setprio 1
	s_barrier
	v_mfma_scale_f32_16x16x128_f8f6f4 v[92:95], v[142:149], v[182:189], v[92:95], v138, v138 op_sel_hi:[0,0,0]
	v_mfma_scale_f32_16x16x128_f8f6f4 v[84:87], v[150:157], v[182:189], v[84:87], v138, v138 op_sel_hi:[0,0,0]
	v_mfma_scale_f32_16x16x128_f8f6f4 v[64:67], v[142:149], v[190:197], v[64:67], v138, v138 op_sel_hi:[0,0,0]
	v_mfma_scale_f32_16x16x128_f8f6f4 v[52:55], v[150:157], v[190:197], v[52:55], v138, v138 op_sel_hi:[0,0,0]
	v_mfma_scale_f32_16x16x128_f8f6f4 v[24:27], v[150:157], v[198:205], v[24:27], v138, v138 op_sel_hi:[0,0,0]
	v_mfma_scale_f32_16x16x128_f8f6f4 v[128:131], v[142:149], v[174:181], v[104:107], v138, v138 op_sel_hi:[0,0,0]
	v_mfma_scale_f32_16x16x128_f8f6f4 v[206:209], v[150:157], v[174:181], v[112:115], v138, v138 op_sel_hi:[0,0,0]
	v_mfma_scale_f32_16x16x128_f8f6f4 v[210:213], v[142:149], v[198:205], v[36:39], v138, v138 op_sel_hi:[0,0,0]
	s_setprio 0
	s_setprio 1
	v_mfma_scale_f32_16x16x128_f8f6f4 v[120:123], v[158:165], v[174:181], v[120:123], v138, v138 op_sel_hi:[0,0,0]
	v_mfma_scale_f32_16x16x128_f8f6f4 v[124:127], v[166:173], v[174:181], v[124:127], v138, v138 op_sel_hi:[0,0,0]
	v_mfma_scale_f32_16x16x128_f8f6f4 v[44:47], v[158:165], v[198:205], v[44:47], v138, v138 op_sel_hi:[0,0,0]
	v_mfma_scale_f32_16x16x128_f8f6f4 v[174:177], v[158:165], v[182:189], v[116:119], v138, v138 op_sel_hi:[0,0,0]
	v_mfma_scale_f32_16x16x128_f8f6f4 v[178:181], v[166:173], v[182:189], v[108:111], v138, v138 op_sel_hi:[0,0,0]
	v_mfma_scale_f32_16x16x128_f8f6f4 v[182:185], v[158:165], v[190:197], v[76:79], v138, v138 op_sel_hi:[0,0,0]
	v_mfma_scale_f32_16x16x128_f8f6f4 v[186:189], v[166:173], v[190:197], v[72:75], v138, v138 op_sel_hi:[0,0,0]
	v_mfma_scale_f32_16x16x128_f8f6f4 v[190:193], v[166:173], v[198:205], v[40:43], v138, v138 op_sel_hi:[0,0,0]
	s_barrier
	s_setprio 0
	ds_read_b128 v[36:39], v137 offset:16384
	s_nop 3
	ds_read_b128 v[40:43], v137 offset:17408
	ds_read_b128 v[72:75], v137 offset:18432
	ds_read_b128 v[76:79], v137 offset:19456
	ds_read_b128 v[104:107], v137 offset:20480
	ds_read_b128 v[108:111], v137 offset:21504
	ds_read_b128 v[112:115], v137 offset:22528
	ds_read_b128 v[116:119], v137 offset:23552
	s_mov_b32 s24, m0
	s_mov_b32 m0, s17
	s_nop 0
	global_load_lds_dwordx4 v133, s[28:29]
	s_mov_b32 m0, s24
	s_add_u32 s24, s28, 0x10000
	s_addc_u32 s25, s29, 0
	s_mov_b32 s58, m0
	s_mov_b32 m0, s19
	s_nop 0
	global_load_lds_dwordx4 v133, s[24:25]
	s_mov_b32 m0, s58
	s_add_u32 s24, s28, 0x20000
	s_addc_u32 s25, s29, 0
	s_mov_b32 s58, m0
	s_mov_b32 m0, s36
	s_nop 0
	global_load_lds_dwordx4 v133, s[24:25]
	s_mov_b32 m0, s58
	s_add_u32 s24, s28, 0x30000
	s_addc_u32 s25, s29, 0
	s_mov_b32 s58, m0
	s_mov_b32 m0, s37
	s_nop 0
	global_load_lds_dwordx4 v133, s[24:25]
	s_mov_b32 m0, s58
	s_mov_b32 s24, m0
	s_mov_b32 m0, s35
	s_nop 0
	global_load_lds_dwordx4 v134, s[22:23]
	s_mov_b32 m0, s24
	s_add_u32 s24, s22, 0x10000
	s_addc_u32 s25, s23, 0
	s_mov_b32 s58, m0
	s_mov_b32 m0, s38
	s_nop 0
	global_load_lds_dwordx4 v134, s[24:25]
	s_mov_b32 m0, s58
	s_waitcnt vmcnt(8)
	s_waitcnt lgkmcnt(0)
	s_setprio 1
	s_barrier
	v_mfma_scale_f32_16x16x128_f8f6f4 v[88:91], v[142:149], v[36:43], v[88:91], v138, v138 op_sel_hi:[0,0,0]
	v_mfma_scale_f32_16x16x128_f8f6f4 v[80:83], v[150:157], v[36:43], v[80:83], v138, v138 op_sel_hi:[0,0,0]
	v_mfma_scale_f32_16x16x128_f8f6f4 v[48:51], v[150:157], v[72:79], v[48:51], v138, v138 op_sel_hi:[0,0,0]
	v_mfma_scale_f32_16x16x128_f8f6f4 v[194:197], v[142:149], v[72:79], v[56:59], v138, v138 op_sel_hi:[0,0,0]
	v_mfma_scale_f32_16x16x128_f8f6f4 v[198:201], v[142:149], v[104:111], v[28:31], v138, v138 op_sel_hi:[0,0,0]
	v_mfma_scale_f32_16x16x128_f8f6f4 v[202:205], v[150:157], v[104:111], v[16:19], v138, v138 op_sel_hi:[0,0,0]
	v_mfma_scale_f32_16x16x128_f8f6f4 v[214:217], v[142:149], v[112:119], v[12:15], v138, v138 op_sel_hi:[0,0,0]
	v_mfma_scale_f32_16x16x128_f8f6f4 v[218:221], v[150:157], v[112:119], v[8:11], v138, v138 op_sel_hi:[0,0,0]
	s_setprio 0
	s_setprio 1
	v_mfma_scale_f32_16x16x128_f8f6f4 v[68:71], v[158:165], v[72:79], v[68:71], v138, v138 op_sel_hi:[0,0,0]
	v_mfma_scale_f32_16x16x128_f8f6f4 v[222:225], v[158:165], v[36:43], v[100:103], v138, v138 op_sel_hi:[0,0,0]
	v_mfma_scale_f32_16x16x128_f8f6f4 v[226:229], v[166:173], v[36:43], v[96:99], v138, v138 op_sel_hi:[0,0,0]
	v_mfma_scale_f32_16x16x128_f8f6f4 v[230:233], v[166:173], v[72:79], v[60:63], v138, v138 op_sel_hi:[0,0,0]
	v_mfma_scale_f32_16x16x128_f8f6f4 v[234:237], v[158:165], v[104:111], v[32:35], v138, v138 op_sel_hi:[0,0,0]
	v_mfma_scale_f32_16x16x128_f8f6f4 v[238:241], v[166:173], v[104:111], v[20:23], v138, v138 op_sel_hi:[0,0,0]
	v_mfma_scale_f32_16x16x128_f8f6f4 v[242:245], v[158:165], v[112:119], v[4:7], v138, v138 op_sel_hi:[0,0,0]
	v_mfma_scale_f32_16x16x128_f8f6f4 v[246:249], v[166:173], v[112:119], v[0:3], v138, v138 op_sel_hi:[0,0,0]
	s_barrier
	s_setprio 0
	s_nop 4
	ds_read_b128 v[0:3], v139
	ds_read_b128 v[4:7], v139 offset:1024
	ds_read_b128 v[96:99], v139 offset:2048
	ds_read_b128 v[100:103], v139 offset:3072
	ds_read_b128 v[142:145], v140
	ds_read_b128 v[146:149], v140 offset:1024
	ds_read_b128 v[150:153], v140 offset:2048
	ds_read_b128 v[154:157], v140 offset:3072
	ds_read_b128 v[8:11], v137 offset:32768
	ds_read_b128 v[12:15], v137 offset:33792
	ds_read_b128 v[16:19], v137 offset:34816
	ds_read_b128 v[20:23], v137 offset:35840
	ds_read_b128 v[28:31], v137 offset:36864
	ds_read_b128 v[32:35], v137 offset:37888
	ds_read_b128 v[56:59], v137 offset:38912
	ds_read_b128 v[60:63], v137 offset:39936
	s_add_u32 s24, s22, 0x20000
	s_addc_u32 s25, s23, 0
	s_mov_b32 s58, m0
	s_mov_b32 m0, s39
	s_nop 0
	global_load_lds_dwordx4 v134, s[24:25]
	s_mov_b32 m0, s58
	s_add_u32 s24, s22, 0x30000
	s_addc_u32 s25, s23, 0
	s_mov_b32 s58, m0
	s_mov_b32 m0, s40
	s_nop 0
	global_load_lds_dwordx4 v134, s[24:25]
	s_mov_b32 m0, s58
	s_waitcnt vmcnt(8)
	s_waitcnt lgkmcnt(0)
	s_setprio 1
	s_barrier
	v_mfma_scale_f32_16x16x128_f8f6f4 v[104:107], v[0:7], v[8:15], v[128:131], v138, v138 op_sel_hi:[0,0,0]
	v_mfma_scale_f32_16x16x128_f8f6f4 v[112:115], v[96:103], v[8:15], v[206:209], v138, v138 op_sel_hi:[0,0,0]
	v_mfma_scale_f32_16x16x128_f8f6f4 v[92:95], v[0:7], v[16:23], v[92:95], v138, v138 op_sel_hi:[0,0,0]
	v_mfma_scale_f32_16x16x128_f8f6f4 v[84:87], v[96:103], v[16:23], v[84:87], v138, v138 op_sel_hi:[0,0,0]
	v_mfma_scale_f32_16x16x128_f8f6f4 v[64:67], v[0:7], v[28:35], v[64:67], v138, v138 op_sel_hi:[0,0,0]
	v_mfma_scale_f32_16x16x128_f8f6f4 v[52:55], v[96:103], v[28:35], v[52:55], v138, v138 op_sel_hi:[0,0,0]
	v_mfma_scale_f32_16x16x128_f8f6f4 v[36:39], v[0:7], v[56:63], v[210:213], v138, v138 op_sel_hi:[0,0,0]
	v_mfma_scale_f32_16x16x128_f8f6f4 v[24:27], v[96:103], v[56:63], v[24:27], v138, v138 op_sel_hi:[0,0,0]
	s_setprio 0
	s_setprio 1
	v_mfma_scale_f32_16x16x128_f8f6f4 v[120:123], v[142:149], v[8:15], v[120:123], v138, v138 op_sel_hi:[0,0,0]
	v_mfma_scale_f32_16x16x128_f8f6f4 v[124:127], v[150:157], v[8:15], v[124:127], v138, v138 op_sel_hi:[0,0,0]
	v_mfma_scale_f32_16x16x128_f8f6f4 v[116:119], v[142:149], v[16:23], v[174:177], v138, v138 op_sel_hi:[0,0,0]
	v_mfma_scale_f32_16x16x128_f8f6f4 v[108:111], v[150:157], v[16:23], v[178:181], v138, v138 op_sel_hi:[0,0,0]
	v_mfma_scale_f32_16x16x128_f8f6f4 v[76:79], v[142:149], v[28:35], v[182:185], v138, v138 op_sel_hi:[0,0,0]
	v_mfma_scale_f32_16x16x128_f8f6f4 v[72:75], v[150:157], v[28:35], v[186:189], v138, v138 op_sel_hi:[0,0,0]
	v_mfma_scale_f32_16x16x128_f8f6f4 v[44:47], v[142:149], v[56:63], v[44:47], v138, v138 op_sel_hi:[0,0,0]
	v_mfma_scale_f32_16x16x128_f8f6f4 v[40:43], v[150:157], v[56:63], v[190:193], v138, v138 op_sel_hi:[0,0,0]
	s_barrier
	s_setprio 0
	s_add_u32 s24, s28, 0x80
	s_addc_u32 s25, s29, 0
	ds_read_b128 v[158:161], v137 offset:49152
	ds_read_b128 v[162:165], v137 offset:50176
	ds_read_b128 v[166:169], v137 offset:51200
	ds_read_b128 v[170:173], v137 offset:52224
	ds_read_b128 v[174:177], v137 offset:53248
	ds_read_b128 v[178:181], v137 offset:54272
	ds_read_b128 v[182:185], v137 offset:55296
	ds_read_b128 v[186:189], v137 offset:56320
	s_mov_b32 s58, m0
	s_mov_b32 m0, s44
	s_nop 0
	global_load_lds_dwordx4 v133, s[24:25]
	s_mov_b32 m0, s58
	s_add_u32 s24, s28, 0x10080
	s_addc_u32 s25, s29, 0
	s_mov_b32 s58, m0
	s_mov_b32 m0, s45
	s_nop 0
	global_load_lds_dwordx4 v133, s[24:25]
	s_mov_b32 m0, s58
	s_add_u32 s24, s28, 0x20080
	s_addc_u32 s25, s29, 0
	s_mov_b32 s58, m0
	s_mov_b32 m0, s48
	s_nop 0
	global_load_lds_dwordx4 v133, s[24:25]
	s_mov_b32 m0, s58
	s_add_u32 s24, s28, 0x30080
	s_addc_u32 s25, s29, 0
	s_mov_b32 s28, m0
	s_mov_b32 m0, s49
	s_nop 0
	global_load_lds_dwordx4 v133, s[24:25]
	s_mov_b32 m0, s28
	s_mov_b32 s24, m0
	s_mov_b32 m0, s46
	s_nop 0
	global_load_lds_dwordx4 v134, s[26:27]
	s_mov_b32 m0, s24
	s_add_u32 s22, s22, 0x10080
	s_addc_u32 s23, s23, 0
	s_mov_b32 s24, m0
	s_mov_b32 m0, s47
	s_nop 0
	global_load_lds_dwordx4 v134, s[22:23]
	s_mov_b32 m0, s24
	s_waitcnt vmcnt(8)
	s_waitcnt lgkmcnt(0)
	s_setprio 1
	s_barrier
	v_mfma_scale_f32_16x16x128_f8f6f4 v[88:91], v[0:7], v[158:165], v[88:91], v138, v138 op_sel_hi:[0,0,0]
	v_mfma_scale_f32_16x16x128_f8f6f4 v[80:83], v[96:103], v[158:165], v[80:83], v138, v138 op_sel_hi:[0,0,0]
	v_mfma_scale_f32_16x16x128_f8f6f4 v[56:59], v[0:7], v[166:173], v[194:197], v138, v138 op_sel_hi:[0,0,0]
	v_mfma_scale_f32_16x16x128_f8f6f4 v[48:51], v[96:103], v[166:173], v[48:51], v138, v138 op_sel_hi:[0,0,0]
	v_mfma_scale_f32_16x16x128_f8f6f4 v[28:31], v[0:7], v[174:181], v[198:201], v138, v138 op_sel_hi:[0,0,0]
	v_mfma_scale_f32_16x16x128_f8f6f4 v[16:19], v[96:103], v[174:181], v[202:205], v138, v138 op_sel_hi:[0,0,0]
	v_mfma_scale_f32_16x16x128_f8f6f4 v[12:15], v[0:7], v[182:189], v[214:217], v138, v138 op_sel_hi:[0,0,0]
	v_mfma_scale_f32_16x16x128_f8f6f4 v[8:11], v[96:103], v[182:189], v[218:221], v138, v138 op_sel_hi:[0,0,0]
	s_setprio 0
	s_setprio 1
	v_mfma_scale_f32_16x16x128_f8f6f4 v[100:103], v[142:149], v[158:165], v[222:225], v138, v138 op_sel_hi:[0,0,0]
	v_mfma_scale_f32_16x16x128_f8f6f4 v[96:99], v[150:157], v[158:165], v[226:229], v138, v138 op_sel_hi:[0,0,0]
	v_mfma_scale_f32_16x16x128_f8f6f4 v[68:71], v[142:149], v[166:173], v[68:71], v138, v138 op_sel_hi:[0,0,0]
	v_mfma_scale_f32_16x16x128_f8f6f4 v[60:63], v[150:157], v[166:173], v[230:233], v138, v138 op_sel_hi:[0,0,0]
	v_mfma_scale_f32_16x16x128_f8f6f4 v[32:35], v[142:149], v[174:181], v[234:237], v138, v138 op_sel_hi:[0,0,0]
	v_mfma_scale_f32_16x16x128_f8f6f4 v[20:23], v[150:157], v[174:181], v[238:241], v138, v138 op_sel_hi:[0,0,0]
	v_mfma_scale_f32_16x16x128_f8f6f4 v[4:7], v[142:149], v[182:189], v[242:245], v138, v138 op_sel_hi:[0,0,0]
	v_mfma_scale_f32_16x16x128_f8f6f4 v[0:3], v[150:157], v[182:189], v[246:249], v138, v138 op_sel_hi:[0,0,0]
	s_barrier
	s_setprio 0
	s_add_i32 s57, s57, 2
	s_add_u32 s55, s55, 0x100
	s_addc_u32 s56, s56, 0
	s_cmp_gt_u32 s57, 5
	s_mov_b64 s[24:25], s[20:21]
	s_cbranch_scc0 .LBB0_800
	s_and_b64 vcc, exec, s[4:5]
	s_cbranch_vccz .LBB0_803
	s_barrier

.LBB0_1042:
	s_ashr_i32 s7, s6, 31
	s_lshl_b64 s[10:11], s[6:7], 18
	v_readlane_b32 s14, v254, 49
	v_readlane_b32 s15, v254, 50
	s_add_u32 s10, s14, s10
	s_addc_u32 s11, s15, s11
	s_and_b64 s[14:15], s[12:13], exec
	ds_read_b128 v[0:3], v203
	ds_read_b128 v[4:7], v203 offset:1024
	ds_read_b128 v[8:11], v203 offset:2048
	ds_read_b128 v[12:15], v203 offset:3072
	ds_read_b128 v[16:19], v204
	ds_read_b128 v[20:23], v204 offset:1024
	ds_read_b128 v[24:27], v204 offset:2048
	ds_read_b128 v[28:31], v204 offset:3072
	s_cselect_b32 s7, s11, s23
	s_cselect_b32 s52, s10, s22
	s_ashr_i32 s9, s8, 31
	s_lshl_b64 s[14:15], s[8:9], 18
	s_add_u32 s14, s30, s14
	s_addc_u32 s15, s31, s15
	s_and_b64 s[24:25], s[12:13], exec
	s_cselect_b32 s9, s15, s21
	s_cselect_b32 s53, s14, s20
	s_add_u32 s24, s22, 0x100
	s_addc_u32 s25, s23, 0
	s_add_u32 s26, s22, 0x180
	s_addc_u32 s27, s23, 0
	s_add_u32 s28, s20, 0x100
	s_addc_u32 s29, s21, 0
	ds_read_b128 v[32:35], v205
	ds_read_b128 v[36:39], v205 offset:1024
	ds_read_b128 v[40:43], v205 offset:2048
	ds_read_b128 v[44:47], v205 offset:3072
	ds_read_b128 v[48:51], v205 offset:4096
	ds_read_b128 v[52:55], v205 offset:5120
	ds_read_b128 v[56:59], v205 offset:6144
	ds_read_b128 v[60:63], v205 offset:7168
	s_add_u32 s54, s22, 0x20080
	s_addc_u32 s55, s23, 0
	s_mov_b32 s56, m0
	s_mov_b32 m0, s50
	s_nop 0
	global_load_lds_dwordx4 v202, s[54:55]
	s_mov_b32 m0, s56
	s_add_u32 s54, s22, 0x30080
	s_addc_u32 s55, s23, 0
	s_mov_b32 s56, m0
	s_mov_b32 m0, s51
	s_nop 0
	global_load_lds_dwordx4 v202, s[54:55]
	s_mov_b32 m0, s56
	s_waitcnt vmcnt(8)
	s_waitcnt lgkmcnt(0)
	s_setprio 1
	s_barrier
	s_waitcnt vmcnt(4) lgkmcnt(6)
	v_mfma_scale_f32_16x16x128_f8f6f4 v[64:67], v[0:7], v[32:39], 0, v206, v206 op_sel_hi:[0,0,0]
	s_waitcnt vmcnt(3)
	v_mfma_scale_f32_16x16x128_f8f6f4 v[68:71], v[8:15], v[32:39], 0, v206, v206 op_sel_hi:[0,0,0]
	s_waitcnt vmcnt(2) lgkmcnt(4)
	v_mfma_scale_f32_16x16x128_f8f6f4 v[72:75], v[0:7], v[40:47], 0, v206, v206 op_sel_hi:[0,0,0]
	s_waitcnt vmcnt(0)
	v_mfma_scale_f32_16x16x128_f8f6f4 v[76:79], v[8:15], v[40:47], 0, v206, v206 op_sel_hi:[0,0,0]
	v_mfma_scale_f32_16x16x128_f8f6f4 v[80:83], v[0:7], v[48:55], 0, v206, v206 op_sel_hi:[0,0,0]
	v_mfma_scale_f32_16x16x128_f8f6f4 v[84:87], v[8:15], v[48:55], 0, v206, v206 op_sel_hi:[0,0,0]
	v_mfma_scale_f32_16x16x128_f8f6f4 v[88:91], v[0:7], v[56:63], 0, v206, v206 op_sel_hi:[0,0,0]
	v_mfma_scale_f32_16x16x128_f8f6f4 v[100:103], v[8:15], v[56:63], 0, v206, v206 op_sel_hi:[0,0,0]
	s_setprio 0
	s_setprio 1
	v_mfma_scale_f32_16x16x128_f8f6f4 v[108:111], v[16:23], v[32:39], 0, v206, v206 op_sel_hi:[0,0,0]
	v_mfma_scale_f32_16x16x128_f8f6f4 v[120:123], v[24:31], v[32:39], 0, v206, v206 op_sel_hi:[0,0,0]
	v_mfma_scale_f32_16x16x128_f8f6f4 v[136:139], v[16:23], v[40:47], 0, v206, v206 op_sel_hi:[0,0,0]
	v_mfma_scale_f32_16x16x128_f8f6f4 v[152:155], v[24:31], v[40:47], 0, v206, v206 op_sel_hi:[0,0,0]
	v_mfma_scale_f32_16x16x128_f8f6f4 v[156:159], v[16:23], v[48:55], 0, v206, v206 op_sel_hi:[0,0,0]
	v_mfma_scale_f32_16x16x128_f8f6f4 v[160:163], v[24:31], v[48:55], 0, v206, v206 op_sel_hi:[0,0,0]
	v_mfma_scale_f32_16x16x128_f8f6f4 v[164:167], v[16:23], v[56:63], 0, v206, v206 op_sel_hi:[0,0,0]
	v_mfma_scale_f32_16x16x128_f8f6f4 v[168:171], v[24:31], v[56:63], 0, v206, v206 op_sel_hi:[0,0,0]
	s_barrier
	s_setprio 0
	ds_read_b128 v[32:35], v205 offset:16384
	ds_read_b128 v[36:39], v205 offset:17408
	ds_read_b128 v[40:43], v205 offset:18432
	ds_read_b128 v[44:47], v205 offset:19456
	ds_read_b128 v[48:51], v205 offset:20480
	ds_read_b128 v[52:55], v205 offset:21504
	ds_read_b128 v[56:59], v205 offset:22528
	ds_read_b128 v[60:63], v205 offset:23552
	s_mov_b32 s54, m0
	s_mov_b32 m0, s17
	s_nop 0
	global_load_lds_dwordx4 v201, s[28:29]
	s_mov_b32 m0, s54
	s_add_u32 s28, s20, 0x10100
	s_addc_u32 s29, s21, 0
	s_mov_b32 s54, m0
	s_mov_b32 m0, s19
	s_nop 0
	global_load_lds_dwordx4 v201, s[28:29]
	s_mov_b32 m0, s54
	s_add_u32 s28, s20, 0x20100
	s_addc_u32 s29, s21, 0
	s_mov_b32 s54, m0
	s_mov_b32 m0, s34
	s_nop 0
	global_load_lds_dwordx4 v201, s[28:29]
	s_mov_b32 m0, s54
	s_add_u32 s28, s20, 0x30100
	s_addc_u32 s29, s21, 0
	s_mov_b32 s54, m0
	s_mov_b32 m0, s35
	s_nop 0
	global_load_lds_dwordx4 v201, s[28:29]
	s_mov_b32 m0, s54
	s_mov_b32 s28, m0
	s_mov_b32 m0, s33
	s_nop 0
	global_load_lds_dwordx4 v202, s[24:25]
	s_mov_b32 m0, s28
	s_add_u32 s28, s22, 0x10100
	s_addc_u32 s29, s23, 0
	s_mov_b32 s54, m0
	s_mov_b32 m0, s36
	s_nop 0
	global_load_lds_dwordx4 v202, s[28:29]
	s_mov_b32 m0, s54
	s_waitcnt vmcnt(8)
	s_waitcnt lgkmcnt(0)
	s_setprio 1
	s_barrier
	v_mfma_scale_f32_16x16x128_f8f6f4 v[176:179], v[0:7], v[32:39], 0, v206, v206 op_sel_hi:[0,0,0]
	v_mfma_scale_f32_16x16x128_f8f6f4 v[180:183], v[8:15], v[32:39], 0, v206, v206 op_sel_hi:[0,0,0]
	v_mfma_scale_f32_16x16x128_f8f6f4 v[184:187], v[0:7], v[40:47], 0, v206, v206 op_sel_hi:[0,0,0]
	v_mfma_scale_f32_16x16x128_f8f6f4 v[188:191], v[8:15], v[40:47], 0, v206, v206 op_sel_hi:[0,0,0]
	v_mfma_scale_f32_16x16x128_f8f6f4 v[192:195], v[0:7], v[48:55], 0, v206, v206 op_sel_hi:[0,0,0]
	v_mfma_scale_f32_16x16x128_f8f6f4 v[196:199], v[8:15], v[48:55], 0, v206, v206 op_sel_hi:[0,0,0]
	v_mfma_scale_f32_16x16x128_f8f6f4 v[210:213], v[0:7], v[56:63], 0, v206, v206 op_sel_hi:[0,0,0]
	v_mfma_scale_f32_16x16x128_f8f6f4 v[214:217], v[8:15], v[56:63], 0, v206, v206 op_sel_hi:[0,0,0]
	s_setprio 0
	s_setprio 1
	v_mfma_scale_f32_16x16x128_f8f6f4 v[218:221], v[16:23], v[32:39], 0, v206, v206 op_sel_hi:[0,0,0]
	v_mfma_scale_f32_16x16x128_f8f6f4 v[222:225], v[24:31], v[32:39], 0, v206, v206 op_sel_hi:[0,0,0]
	v_mfma_scale_f32_16x16x128_f8f6f4 v[226:229], v[16:23], v[40:47], 0, v206, v206 op_sel_hi:[0,0,0]
	v_mfma_scale_f32_16x16x128_f8f6f4 v[230:233], v[24:31], v[40:47], 0, v206, v206 op_sel_hi:[0,0,0]
	v_mfma_scale_f32_16x16x128_f8f6f4 v[234:237], v[16:23], v[48:55], 0, v206, v206 op_sel_hi:[0,0,0]
	v_mfma_scale_f32_16x16x128_f8f6f4 v[238:241], v[24:31], v[48:55], 0, v206, v206 op_sel_hi:[0,0,0]
	v_mfma_scale_f32_16x16x128_f8f6f4 v[242:245], v[16:23], v[56:63], 0, v206, v206 op_sel_hi:[0,0,0]
	v_mfma_scale_f32_16x16x128_f8f6f4 v[246:249], v[24:31], v[56:63], 0, v206, v206 op_sel_hi:[0,0,0]
	s_barrier
	s_setprio 0
	ds_read_b128 v[0:3], v207
	ds_read_b128 v[4:7], v207 offset:1024
	ds_read_b128 v[16:19], v207 offset:2048
	ds_read_b128 v[20:23], v207 offset:3072
	ds_read_b128 v[112:115], v208
	ds_read_b128 v[116:119], v208 offset:1024
	ds_read_b128 v[144:147], v208 offset:2048
	ds_read_b128 v[148:151], v208 offset:3072
	ds_read_b128 v[8:11], v205 offset:32768
	ds_read_b128 v[12:15], v205 offset:33792
	ds_read_b128 v[24:27], v205 offset:34816
	ds_read_b128 v[28:31], v205 offset:35840
	ds_read_b128 v[32:35], v205 offset:36864
	ds_read_b128 v[36:39], v205 offset:37888
	ds_read_b128 v[40:43], v205 offset:38912
	ds_read_b128 v[44:47], v205 offset:39936
	s_add_u32 s28, s22, 0x20100
	s_addc_u32 s29, s23, 0
	s_mov_b32 s54, m0
	s_mov_b32 m0, s37
	s_nop 0
	global_load_lds_dwordx4 v202, s[28:29]
	s_mov_b32 m0, s54
	s_add_u32 s28, s22, 0x30100
	s_addc_u32 s29, s23, 0
	s_mov_b32 s54, m0
	s_mov_b32 m0, s38
	s_nop 0
	global_load_lds_dwordx4 v202, s[28:29]
	s_mov_b32 m0, s54
	s_waitcnt vmcnt(8)
	s_waitcnt lgkmcnt(0)
	s_setprio 1
	s_barrier
	v_mfma_scale_f32_16x16x128_f8f6f4 v[128:131], v[0:7], v[8:15], v[64:67], v206, v206 op_sel_hi:[0,0,0]
	v_mfma_scale_f32_16x16x128_f8f6f4 v[124:127], v[16:23], v[8:15], v[68:71], v206, v206 op_sel_hi:[0,0,0]
	v_mfma_scale_f32_16x16x128_f8f6f4 v[104:107], v[0:7], v[24:31], v[72:75], v206, v206 op_sel_hi:[0,0,0]
	v_mfma_scale_f32_16x16x128_f8f6f4 v[96:99], v[16:23], v[24:31], v[76:79], v206, v206 op_sel_hi:[0,0,0]
	v_mfma_scale_f32_16x16x128_f8f6f4 v[92:95], v[0:7], v[32:39], v[80:83], v206, v206 op_sel_hi:[0,0,0]
	v_mfma_scale_f32_16x16x128_f8f6f4 v[84:87], v[16:23], v[32:39], v[84:87], v206, v206 op_sel_hi:[0,0,0]
	v_mfma_scale_f32_16x16x128_f8f6f4 v[68:71], v[0:7], v[40:47], v[88:91], v206, v206 op_sel_hi:[0,0,0]
	v_mfma_scale_f32_16x16x128_f8f6f4 v[56:59], v[16:23], v[40:47], v[100:103], v206, v206 op_sel_hi:[0,0,0]
	s_setprio 0
	s_setprio 1
	v_mfma_scale_f32_16x16x128_f8f6f4 v[140:143], v[112:119], v[8:15], v[108:111], v206, v206 op_sel_hi:[0,0,0]
	v_mfma_scale_f32_16x16x128_f8f6f4 v[132:135], v[144:151], v[8:15], v[120:123], v206, v206 op_sel_hi:[0,0,0]
	v_mfma_scale_f32_16x16x128_f8f6f4 v[108:111], v[112:119], v[24:31], v[136:139], v206, v206 op_sel_hi:[0,0,0]
	v_mfma_scale_f32_16x16x128_f8f6f4 v[100:103], v[144:151], v[24:31], v[152:155], v206, v206 op_sel_hi:[0,0,0]
	v_mfma_scale_f32_16x16x128_f8f6f4 v[88:91], v[112:119], v[32:39], v[156:159], v206, v206 op_sel_hi:[0,0,0]
	v_mfma_scale_f32_16x16x128_f8f6f4 v[80:83], v[144:151], v[32:39], v[160:163], v206, v206 op_sel_hi:[0,0,0]
	v_mfma_scale_f32_16x16x128_f8f6f4 v[52:55], v[112:119], v[40:47], v[164:167], v206, v206 op_sel_hi:[0,0,0]
	v_mfma_scale_f32_16x16x128_f8f6f4 v[48:51], v[144:151], v[40:47], v[168:171], v206, v206 op_sel_hi:[0,0,0]
	s_barrier
	s_setprio 0
	s_add_u32 s28, s20, 0x180
	s_addc_u32 s29, s21, 0
	ds_read_b128 v[32:35], v205 offset:49152
	ds_read_b128 v[36:39], v205 offset:50176
	ds_read_b128 v[152:155], v205 offset:51200
	ds_read_b128 v[156:159], v205 offset:52224
	ds_read_b128 v[160:163], v205 offset:53248
	ds_read_b128 v[164:167], v205 offset:54272
	ds_read_b128 v[168:171], v205 offset:55296
	ds_read_b128 v[172:175], v205 offset:56320
	s_mov_b32 s54, m0
	s_mov_b32 m0, s44
	s_nop 0
	global_load_lds_dwordx4 v201, s[28:29]
	s_mov_b32 m0, s54
	s_add_u32 s28, s20, 0x10180
	s_addc_u32 s29, s21, 0
	s_mov_b32 s54, m0
	s_mov_b32 m0, s45
	s_nop 0
	global_load_lds_dwordx4 v201, s[28:29]
	s_mov_b32 m0, s54
	s_add_u32 s28, s20, 0x20180
	s_addc_u32 s29, s21, 0
	s_mov_b32 s54, m0
	s_mov_b32 m0, s48
	s_nop 0
	global_load_lds_dwordx4 v201, s[28:29]
	s_mov_b32 m0, s54
	s_add_u32 s28, s20, 0x30180
	s_addc_u32 s29, s21, 0
	s_mov_b32 s54, m0
	s_mov_b32 m0, s49
	s_nop 0
	global_load_lds_dwordx4 v201, s[28:29]
	s_mov_b32 m0, s54
	s_mov_b32 s28, m0
	s_mov_b32 m0, s46
	s_nop 0
	global_load_lds_dwordx4 v202, s[26:27]
	s_mov_b32 m0, s28
	s_add_u32 s22, s22, 0x10180
	s_addc_u32 s23, s23, 0
	s_mov_b32 s26, m0
	s_mov_b32 m0, s47
	s_nop 0
	global_load_lds_dwordx4 v202, s[22:23]
	s_mov_b32 m0, s26
	s_waitcnt vmcnt(8)
	s_waitcnt lgkmcnt(0)
	s_setprio 1
	s_barrier
	v_mfma_scale_f32_16x16x128_f8f6f4 v[76:79], v[0:7], v[32:39], v[176:179], v206, v206 op_sel_hi:[0,0,0]
	v_mfma_scale_f32_16x16x128_f8f6f4 v[64:67], v[16:23], v[32:39], v[180:183], v206, v206 op_sel_hi:[0,0,0]
	v_mfma_scale_f32_16x16x128_f8f6f4 v[44:47], v[0:7], v[152:159], v[184:187], v206, v206 op_sel_hi:[0,0,0]
	v_mfma_scale_f32_16x16x128_f8f6f4 v[40:43], v[16:23], v[152:159], v[188:191], v206, v206 op_sel_hi:[0,0,0]
	v_mfma_scale_f32_16x16x128_f8f6f4 v[28:31], v[0:7], v[160:167], v[192:195], v206, v206 op_sel_hi:[0,0,0]
	v_mfma_scale_f32_16x16x128_f8f6f4 v[24:27], v[16:23], v[160:167], v[196:199], v206, v206 op_sel_hi:[0,0,0]
	v_mfma_scale_f32_16x16x128_f8f6f4 v[12:15], v[0:7], v[168:175], v[210:213], v206, v206 op_sel_hi:[0,0,0]
	v_mfma_scale_f32_16x16x128_f8f6f4 v[8:11], v[16:23], v[168:175], v[214:217], v206, v206 op_sel_hi:[0,0,0]
	s_setprio 0
	s_setprio 1
	v_mfma_scale_f32_16x16x128_f8f6f4 v[72:75], v[112:119], v[32:39], v[218:221], v206, v206 op_sel_hi:[0,0,0]
	v_mfma_scale_f32_16x16x128_f8f6f4 v[60:63], v[144:151], v[32:39], v[222:225], v206, v206 op_sel_hi:[0,0,0]
	v_mfma_scale_f32_16x16x128_f8f6f4 v[36:39], v[112:119], v[152:159], v[226:229], v206, v206 op_sel_hi:[0,0,0]
	v_mfma_scale_f32_16x16x128_f8f6f4 v[32:35], v[144:151], v[152:159], v[230:233], v206, v206 op_sel_hi:[0,0,0]
	v_mfma_scale_f32_16x16x128_f8f6f4 v[20:23], v[112:119], v[160:167], v[234:237], v206, v206 op_sel_hi:[0,0,0]
	v_mfma_scale_f32_16x16x128_f8f6f4 v[16:19], v[144:151], v[160:167], v[238:241], v206, v206 op_sel_hi:[0,0,0]
	v_mfma_scale_f32_16x16x128_f8f6f4 v[4:7], v[112:119], v[168:175], v[242:245], v206, v206 op_sel_hi:[0,0,0]
	v_mfma_scale_f32_16x16x128_f8f6f4 v[0:3], v[144:151], v[168:175], v[246:249], v206, v206 op_sel_hi:[0,0,0]
	s_barrier
	s_setprio 0
	s_add_u32 s54, s20, 0x200
	s_addc_u32 s55, s21, 0
	s_mov_b32 s56, 0

.LBB0_1223:
	s_add_u32 s34, s34, 0x100
	s_addc_u32 s35, s35, 0
	s_and_b64 s[36:37], s[38:39], exec
	s_cselect_b32 s42, s16, s34
	s_cselect_b32 s43, s17, s35
	s_add_u32 s36, s42, 0x80
	s_addc_u32 s37, s43, 0
	s_waitcnt vmcnt(8)
	s_and_b64 s[38:39], s[38:39], exec
	s_waitcnt lgkmcnt(0)
	s_cselect_b32 s38, s26, s15
	s_cselect_b32 s39, s27, s23
	s_add_u32 s40, s38, 0x80
	s_addc_u32 s41, s39, 0
	s_barrier
	s_setprio 1
	s_waitcnt lgkmcnt(6)
	v_mfma_scale_f32_16x16x128_f8f6f4 v[188:191], v[16:23], v[56:63], v[188:191], v205, v205 op_sel_hi:[0,0,0]
	v_mfma_scale_f32_16x16x128_f8f6f4 v[180:183], v[24:31], v[56:63], v[180:183], v205, v205 op_sel_hi:[0,0,0]
	s_waitcnt lgkmcnt(4)
	v_mfma_scale_f32_16x16x128_f8f6f4 v[172:175], v[16:23], v[48:55], v[172:175], v205, v205 op_sel_hi:[0,0,0]
	v_mfma_scale_f32_16x16x128_f8f6f4 v[164:167], v[24:31], v[48:55], v[164:167], v205, v205 op_sel_hi:[0,0,0]
	s_waitcnt lgkmcnt(2)
	v_mfma_scale_f32_16x16x128_f8f6f4 v[156:159], v[16:23], v[40:47], v[156:159], v205, v205 op_sel_hi:[0,0,0]
	v_mfma_scale_f32_16x16x128_f8f6f4 v[148:151], v[24:31], v[40:47], v[148:151], v205, v205 op_sel_hi:[0,0,0]
	s_waitcnt lgkmcnt(0)
	v_mfma_scale_f32_16x16x128_f8f6f4 v[140:143], v[16:23], v[32:39], v[140:143], v205, v205 op_sel_hi:[0,0,0]
	v_mfma_scale_f32_16x16x128_f8f6f4 v[132:135], v[24:31], v[32:39], v[132:135], v205, v205 op_sel_hi:[0,0,0]
	s_setprio 0
	s_setprio 1
	v_mfma_scale_f32_16x16x128_f8f6f4 v[184:187], v[0:7], v[56:63], v[184:187], v205, v205 op_sel_hi:[0,0,0]
	v_mfma_scale_f32_16x16x128_f8f6f4 v[176:179], v[8:15], v[56:63], v[176:179], v205, v205 op_sel_hi:[0,0,0]
	v_mfma_scale_f32_16x16x128_f8f6f4 v[168:171], v[0:7], v[48:55], v[168:171], v205, v205 op_sel_hi:[0,0,0]
	v_mfma_scale_f32_16x16x128_f8f6f4 v[160:163], v[8:15], v[48:55], v[160:163], v205, v205 op_sel_hi:[0,0,0]
	v_mfma_scale_f32_16x16x128_f8f6f4 v[152:155], v[0:7], v[40:47], v[152:155], v205, v205 op_sel_hi:[0,0,0]
	v_mfma_scale_f32_16x16x128_f8f6f4 v[144:147], v[8:15], v[40:47], v[144:147], v205, v205 op_sel_hi:[0,0,0]
	v_mfma_scale_f32_16x16x128_f8f6f4 v[136:139], v[0:7], v[32:39], v[136:139], v205, v205 op_sel_hi:[0,0,0]
	v_mfma_scale_f32_16x16x128_f8f6f4 v[128:131], v[8:15], v[32:39], v[128:131], v205, v205 op_sel_hi:[0,0,0]
	s_setprio 0
	s_barrier
	s_add_u32 s72, s38, 0x10000
	ds_read_b128 v[32:35], v210 offset:16384
	ds_read_b128 v[36:39], v210 offset:17408
	ds_read_b128 v[40:43], v210 offset:18432
	ds_read_b128 v[44:47], v210 offset:19456
	ds_read_b128 v[48:51], v210 offset:20480
	ds_read_b128 v[52:55], v210 offset:21504
	ds_read_b128 v[56:59], v210 offset:22528
	ds_read_b128 v[60:63], v210 offset:23552
	s_mov_b32 s71, m0
	s_mov_b32 m0, s29
	s_nop 0
	global_load_lds_dwordx4 v199, s[38:39]
	s_mov_b32 m0, s71
	s_addc_u32 s73, s39, 0
	s_mov_b32 s71, m0
	s_mov_b32 m0, s49
	s_nop 0
	global_load_lds_dwordx4 v199, s[72:73]
	s_mov_b32 m0, s71
	s_add_u32 s72, s38, 0x20000
	s_addc_u32 s73, s39, 0
	s_mov_b32 s71, m0
	s_mov_b32 m0, s50
	s_nop 0
	global_load_lds_dwordx4 v199, s[72:73]
	s_mov_b32 m0, s71
	s_add_u32 s72, s38, 0x30000
	s_addc_u32 s73, s39, 0
	s_mov_b32 s71, m0
	s_mov_b32 m0, s51
	s_nop 0
	global_load_lds_dwordx4 v199, s[72:73]
	s_mov_b32 m0, s71
	s_nop 0
	s_mov_b32 s71, m0
	s_mov_b32 m0, s48
	s_nop 0
	global_load_lds_dwordx4 v200, s[42:43]
	s_mov_b32 m0, s71
	s_nop 0
	s_mov_b32 s71, m0
	s_mov_b32 m0, s52
	s_nop 0
	global_load_lds_dwordx4 v201, s[42:43]
	s_mov_b32 m0, s71
	s_waitcnt vmcnt(8)
	s_waitcnt lgkmcnt(0)
	s_setprio 1
	s_barrier
	v_mfma_scale_f32_16x16x128_f8f6f4 v[124:127], v[16:23], v[32:39], v[124:127], v205, v205 op_sel_hi:[0,0,0]
	v_mfma_scale_f32_16x16x128_f8f6f4 v[116:119], v[24:31], v[32:39], v[116:119], v205, v205 op_sel_hi:[0,0,0]
	v_mfma_scale_f32_16x16x128_f8f6f4 v[108:111], v[16:23], v[40:47], v[108:111], v205, v205 op_sel_hi:[0,0,0]
	v_mfma_scale_f32_16x16x128_f8f6f4 v[100:103], v[24:31], v[40:47], v[100:103], v205, v205 op_sel_hi:[0,0,0]
	v_mfma_scale_f32_16x16x128_f8f6f4 v[92:95], v[16:23], v[48:55], v[92:95], v205, v205 op_sel_hi:[0,0,0]
	v_mfma_scale_f32_16x16x128_f8f6f4 v[84:87], v[24:31], v[48:55], v[84:87], v205, v205 op_sel_hi:[0,0,0]
	v_mfma_scale_f32_16x16x128_f8f6f4 v[72:75], v[16:23], v[56:63], v[72:75], v205, v205 op_sel_hi:[0,0,0]
	v_mfma_scale_f32_16x16x128_f8f6f4 v[64:67], v[24:31], v[56:63], v[64:67], v205, v205 op_sel_hi:[0,0,0]
	s_setprio 0
	s_setprio 1
	v_mfma_scale_f32_16x16x128_f8f6f4 v[120:123], v[0:7], v[32:39], v[120:123], v205, v205 op_sel_hi:[0,0,0]
	v_mfma_scale_f32_16x16x128_f8f6f4 v[112:115], v[8:15], v[32:39], v[112:115], v205, v205 op_sel_hi:[0,0,0]
	v_mfma_scale_f32_16x16x128_f8f6f4 v[104:107], v[0:7], v[40:47], v[104:107], v205, v205 op_sel_hi:[0,0,0]
	v_mfma_scale_f32_16x16x128_f8f6f4 v[96:99], v[8:15], v[40:47], v[96:99], v205, v205 op_sel_hi:[0,0,0]
	v_mfma_scale_f32_16x16x128_f8f6f4 v[88:91], v[0:7], v[48:55], v[88:91], v205, v205 op_sel_hi:[0,0,0]
	v_mfma_scale_f32_16x16x128_f8f6f4 v[80:83], v[8:15], v[48:55], v[80:83], v205, v205 op_sel_hi:[0,0,0]
	v_mfma_scale_f32_16x16x128_f8f6f4 v[76:79], v[0:7], v[56:63], v[76:79], v205, v205 op_sel_hi:[0,0,0]
	v_mfma_scale_f32_16x16x128_f8f6f4 v[68:71], v[8:15], v[56:63], v[68:71], v205, v205 op_sel_hi:[0,0,0]
	s_barrier
	s_setprio 0
	v_add_u32_e32 v12, 0x18000, v209
	v_add_u32_e32 v28, 0x1c000, v209
	ds_read_b128 v[0:3], v12
	ds_read_b128 v[4:7], v12 offset:1024
	ds_read_b128 v[8:11], v12 offset:2048
	ds_read_b128 v[12:15], v12 offset:3072
	ds_read_b128 v[16:19], v28
	ds_read_b128 v[20:23], v28 offset:1024
	ds_read_b128 v[24:27], v28 offset:2048
	ds_read_b128 v[28:31], v28 offset:3072
	ds_read_b128 v[32:35], v210 offset:32768
	ds_read_b128 v[36:39], v210 offset:33792
	ds_read_b128 v[40:43], v210 offset:34816
	ds_read_b128 v[44:47], v210 offset:35840
	ds_read_b128 v[48:51], v210 offset:36864
	ds_read_b128 v[52:55], v210 offset:37888
	ds_read_b128 v[56:59], v210 offset:38912
	ds_read_b128 v[60:63], v210 offset:39936
	s_mov_b32 s71, m0
	s_mov_b32 m0, s53
	s_nop 0
	global_load_lds_dwordx4 v202, s[42:43]
	s_mov_b32 m0, s71
	s_nop 0
	s_mov_b32 s71, m0
	s_mov_b32 m0, s54
	s_nop 0
	global_load_lds_dwordx4 v203, s[42:43]
	s_mov_b32 m0, s71
	s_waitcnt vmcnt(8)
	s_waitcnt lgkmcnt(0)
	s_setprio 1
	s_barrier
	v_mfma_scale_f32_16x16x128_f8f6f4 v[188:191], v[0:7], v[32:39], v[188:191], v205, v205 op_sel_hi:[0,0,0]
	v_mfma_scale_f32_16x16x128_f8f6f4 v[180:183], v[8:15], v[32:39], v[180:183], v205, v205 op_sel_hi:[0,0,0]
	v_mfma_scale_f32_16x16x128_f8f6f4 v[172:175], v[0:7], v[40:47], v[172:175], v205, v205 op_sel_hi:[0,0,0]
	v_mfma_scale_f32_16x16x128_f8f6f4 v[164:167], v[8:15], v[40:47], v[164:167], v205, v205 op_sel_hi:[0,0,0]
	v_mfma_scale_f32_16x16x128_f8f6f4 v[156:159], v[0:7], v[48:55], v[156:159], v205, v205 op_sel_hi:[0,0,0]
	v_mfma_scale_f32_16x16x128_f8f6f4 v[148:151], v[8:15], v[48:55], v[148:151], v205, v205 op_sel_hi:[0,0,0]
	v_mfma_scale_f32_16x16x128_f8f6f4 v[140:143], v[0:7], v[56:63], v[140:143], v205, v205 op_sel_hi:[0,0,0]
	v_mfma_scale_f32_16x16x128_f8f6f4 v[132:135], v[8:15], v[56:63], v[132:135], v205, v205 op_sel_hi:[0,0,0]
	s_setprio 0
	s_setprio 1
	v_mfma_scale_f32_16x16x128_f8f6f4 v[184:187], v[16:23], v[32:39], v[184:187], v205, v205 op_sel_hi:[0,0,0]
	v_mfma_scale_f32_16x16x128_f8f6f4 v[176:179], v[24:31], v[32:39], v[176:179], v205, v205 op_sel_hi:[0,0,0]
	v_mfma_scale_f32_16x16x128_f8f6f4 v[168:171], v[16:23], v[40:47], v[168:171], v205, v205 op_sel_hi:[0,0,0]
	v_mfma_scale_f32_16x16x128_f8f6f4 v[160:163], v[24:31], v[40:47], v[160:163], v205, v205 op_sel_hi:[0,0,0]
	v_mfma_scale_f32_16x16x128_f8f6f4 v[152:155], v[16:23], v[48:55], v[152:155], v205, v205 op_sel_hi:[0,0,0]
	v_mfma_scale_f32_16x16x128_f8f6f4 v[144:147], v[24:31], v[48:55], v[144:147], v205, v205 op_sel_hi:[0,0,0]
	v_mfma_scale_f32_16x16x128_f8f6f4 v[136:139], v[16:23], v[56:63], v[136:139], v205, v205 op_sel_hi:[0,0,0]
	v_mfma_scale_f32_16x16x128_f8f6f4 v[128:131], v[24:31], v[56:63], v[128:131], v205, v205 op_sel_hi:[0,0,0]
	s_barrier
	s_setprio 0
	ds_read_b128 v[32:35], v210 offset:49152
	ds_read_b128 v[36:39], v210 offset:50176
	ds_read_b128 v[40:43], v210 offset:51200
	ds_read_b128 v[44:47], v210 offset:52224
	ds_read_b128 v[48:51], v210 offset:53248
	ds_read_b128 v[52:55], v210 offset:54272
	ds_read_b128 v[56:59], v210 offset:55296
	ds_read_b128 v[60:63], v210 offset:56320
	s_mov_b32 s42, m0
	s_mov_b32 m0, s57
	s_nop 0
	global_load_lds_dwordx4 v199, s[40:41]
	s_mov_b32 m0, s42
	s_add_u32 s40, s38, 0x10080
	s_addc_u32 s41, s39, 0
	s_mov_b32 s42, m0
	s_mov_b32 m0, s58
	s_nop 0
	global_load_lds_dwordx4 v199, s[40:41]
	s_mov_b32 m0, s42
	s_add_u32 s40, s38, 0x20080
	s_addc_u32 s41, s39, 0
	s_mov_b32 s42, m0
	s_mov_b32 m0, s61
	s_nop 0
	global_load_lds_dwordx4 v199, s[40:41]
	s_mov_b32 m0, s42
	s_add_u32 s38, s38, 0x30080
	s_addc_u32 s39, s39, 0
	s_mov_b32 s40, m0
	s_mov_b32 m0, s62
	s_nop 0
	global_load_lds_dwordx4 v199, s[38:39]
	s_mov_b32 m0, s40
	s_mov_b32 s38, m0
	s_mov_b32 m0, s59
	s_nop 0
	global_load_lds_dwordx4 v200, s[36:37]
	s_mov_b32 m0, s38
	s_nop 0
	s_mov_b32 s38, m0
	s_mov_b32 m0, s60
	s_nop 0
	global_load_lds_dwordx4 v201, s[36:37]
	s_mov_b32 m0, s38
	s_waitcnt vmcnt(8)
	s_waitcnt lgkmcnt(0)
	s_setprio 1
	s_barrier
	v_mfma_scale_f32_16x16x128_f8f6f4 v[124:127], v[0:7], v[32:39], v[124:127], v205, v205 op_sel_hi:[0,0,0]
	v_mfma_scale_f32_16x16x128_f8f6f4 v[116:119], v[8:15], v[32:39], v[116:119], v205, v205 op_sel_hi:[0,0,0]
	v_mfma_scale_f32_16x16x128_f8f6f4 v[108:111], v[0:7], v[40:47], v[108:111], v205, v205 op_sel_hi:[0,0,0]
	v_mfma_scale_f32_16x16x128_f8f6f4 v[100:103], v[8:15], v[40:47], v[100:103], v205, v205 op_sel_hi:[0,0,0]
	v_mfma_scale_f32_16x16x128_f8f6f4 v[92:95], v[0:7], v[48:55], v[92:95], v205, v205 op_sel_hi:[0,0,0]
	v_mfma_scale_f32_16x16x128_f8f6f4 v[84:87], v[8:15], v[48:55], v[84:87], v205, v205 op_sel_hi:[0,0,0]
	v_mfma_scale_f32_16x16x128_f8f6f4 v[72:75], v[0:7], v[56:63], v[72:75], v205, v205 op_sel_hi:[0,0,0]
	v_mfma_scale_f32_16x16x128_f8f6f4 v[64:67], v[8:15], v[56:63], v[64:67], v205, v205 op_sel_hi:[0,0,0]
	s_setprio 0
	s_setprio 1
	v_mfma_scale_f32_16x16x128_f8f6f4 v[120:123], v[16:23], v[32:39], v[120:123], v205, v205 op_sel_hi:[0,0,0]
	v_mfma_scale_f32_16x16x128_f8f6f4 v[112:115], v[24:31], v[32:39], v[112:115], v205, v205 op_sel_hi:[0,0,0]
	v_mfma_scale_f32_16x16x128_f8f6f4 v[104:107], v[16:23], v[40:47], v[104:107], v205, v205 op_sel_hi:[0,0,0]
	v_mfma_scale_f32_16x16x128_f8f6f4 v[96:99], v[24:31], v[40:47], v[96:99], v205, v205 op_sel_hi:[0,0,0]
	v_mfma_scale_f32_16x16x128_f8f6f4 v[88:91], v[16:23], v[48:55], v[88:91], v205, v205 op_sel_hi:[0,0,0]
	v_mfma_scale_f32_16x16x128_f8f6f4 v[80:83], v[24:31], v[48:55], v[80:83], v205, v205 op_sel_hi:[0,0,0]
	v_mfma_scale_f32_16x16x128_f8f6f4 v[76:79], v[16:23], v[56:63], v[76:79], v205, v205 op_sel_hi:[0,0,0]
	v_mfma_scale_f32_16x16x128_f8f6f4 v[68:71], v[24:31], v[56:63], v[68:71], v205, v205 op_sel_hi:[0,0,0]
	s_barrier
	s_setprio 0
	s_add_i32 s25, s25, 2
	s_add_u32 s15, s15, 0x100
	s_addc_u32 s23, s23, 0
	s_cmp_gt_u32 s25, 5
	s_cbranch_scc1 .LBB0_1226

.LBB0_1338:
	ds_read_b128 v[146:149], v139
	ds_read_b128 v[150:153], v139 offset:1024
	ds_read_b128 v[154:157], v139 offset:2048
	ds_read_b128 v[158:161], v139 offset:3072
	ds_read_b128 v[162:165], v140
	ds_read_b128 v[166:169], v140 offset:1024
	ds_read_b128 v[170:173], v140 offset:2048
	ds_read_b128 v[174:177], v140 offset:3072
	s_add_u32 s24, s22, 0x100
	s_addc_u32 s25, s23, 0
	s_cmp_eq_u32 s13, 4
	s_cselect_b32 s26, s16, s24
	s_cselect_b32 s27, s17, s25
	s_cselect_b32 s30, s18, s1
	s_cselect_b32 s31, s19, s11
	s_add_u32 s28, s26, 0x80
	s_addc_u32 s29, s27, 0
	ds_read_b128 v[178:181], v141
	ds_read_b128 v[182:185], v141 offset:1024
	ds_read_b128 v[186:189], v141 offset:2048
	ds_read_b128 v[190:193], v141 offset:3072
	ds_read_b128 v[194:197], v141 offset:4096
	ds_read_b128 v[198:201], v141 offset:5120
	ds_read_b128 v[202:205], v141 offset:6144
	ds_read_b128 v[206:209], v141 offset:7168
	s_add_u32 s62, s22, 0x20080
	s_addc_u32 s63, s23, 0
	s_mov_b32 s15, m0
	s_mov_b32 m0, s55
	s_nop 0
	global_load_lds_dwordx4 v137, s[62:63]
	s_mov_b32 m0, s15
	s_add_u32 s22, s22, 0x30080
	s_addc_u32 s23, s23, 0
	s_mov_b32 s15, m0
	s_mov_b32 m0, s56
	s_nop 0
	global_load_lds_dwordx4 v137, s[22:23]
	s_mov_b32 m0, s15
	s_waitcnt vmcnt(8)
	s_waitcnt lgkmcnt(0)
	s_setprio 1
	s_barrier
	v_mfma_scale_f32_16x16x128_f8f6f4 v[124:127], v[146:153], v[178:185], v[124:127], v142, v142 op_sel_hi:[0,0,0]
	v_mfma_scale_f32_16x16x128_f8f6f4 v[120:123], v[154:161], v[178:185], v[120:123], v142, v142 op_sel_hi:[0,0,0]
	v_mfma_scale_f32_16x16x128_f8f6f4 v[116:119], v[146:153], v[186:193], v[116:119], v142, v142 op_sel_hi:[0,0,0]
	v_mfma_scale_f32_16x16x128_f8f6f4 v[112:115], v[154:161], v[186:193], v[112:115], v142, v142 op_sel_hi:[0,0,0]
	v_mfma_scale_f32_16x16x128_f8f6f4 v[128:131], v[146:153], v[194:201], v[92:95], v142, v142 op_sel_hi:[0,0,0]
	v_mfma_scale_f32_16x16x128_f8f6f4 v[210:213], v[154:161], v[194:201], v[88:91], v142, v142 op_sel_hi:[0,0,0]
	v_mfma_scale_f32_16x16x128_f8f6f4 v[214:217], v[146:153], v[202:209], v[84:87], v142, v142 op_sel_hi:[0,0,0]
	v_mfma_scale_f32_16x16x128_f8f6f4 v[218:221], v[154:161], v[202:209], v[80:83], v142, v142 op_sel_hi:[0,0,0]
	s_setprio 0
	s_setprio 1
	v_mfma_scale_f32_16x16x128_f8f6f4 v[108:111], v[162:169], v[178:185], v[108:111], v142, v142 op_sel_hi:[0,0,0]
	v_mfma_scale_f32_16x16x128_f8f6f4 v[104:107], v[170:177], v[178:185], v[104:107], v142, v142 op_sel_hi:[0,0,0]
	v_mfma_scale_f32_16x16x128_f8f6f4 v[100:103], v[162:169], v[186:193], v[100:103], v142, v142 op_sel_hi:[0,0,0]
	v_mfma_scale_f32_16x16x128_f8f6f4 v[96:99], v[170:177], v[186:193], v[96:99], v142, v142 op_sel_hi:[0,0,0]
	v_mfma_scale_f32_16x16x128_f8f6f4 v[178:181], v[162:169], v[194:201], v[76:79], v142, v142 op_sel_hi:[0,0,0]
	v_mfma_scale_f32_16x16x128_f8f6f4 v[182:185], v[170:177], v[194:201], v[72:75], v142, v142 op_sel_hi:[0,0,0]
	v_mfma_scale_f32_16x16x128_f8f6f4 v[186:189], v[162:169], v[202:209], v[68:71], v142, v142 op_sel_hi:[0,0,0]
	v_mfma_scale_f32_16x16x128_f8f6f4 v[190:193], v[170:177], v[202:209], v[64:67], v142, v142 op_sel_hi:[0,0,0]
	s_barrier
	s_setprio 0
	s_add_u32 s22, s30, 0x10000
	s_nop 3
	ds_read_b128 v[64:67], v141 offset:16384
	ds_read_b128 v[68:71], v141 offset:17408
	ds_read_b128 v[72:75], v141 offset:18432
	ds_read_b128 v[76:79], v141 offset:19456
	ds_read_b128 v[80:83], v141 offset:20480
	ds_read_b128 v[84:87], v141 offset:21504
	ds_read_b128 v[88:91], v141 offset:22528
	ds_read_b128 v[92:95], v141 offset:23552
	s_mov_b32 s15, m0
	s_mov_b32 m0, s38
	s_nop 0
	global_load_lds_dwordx4 v136, s[30:31]
	s_mov_b32 m0, s15
	s_addc_u32 s23, s31, 0
	s_mov_b32 s15, m0
	s_mov_b32 m0, s39
	s_nop 0
	global_load_lds_dwordx4 v136, s[22:23]
	s_mov_b32 m0, s15
	s_add_u32 s22, s30, 0x20000
	s_addc_u32 s23, s31, 0
	s_mov_b32 s15, m0
	s_mov_b32 m0, s40
	s_nop 0
	global_load_lds_dwordx4 v136, s[22:23]
	s_mov_b32 m0, s15
	s_add_u32 s22, s30, 0x30000
	s_addc_u32 s23, s31, 0
	s_mov_b32 s15, m0
	s_mov_b32 m0, s41
	s_nop 0
	global_load_lds_dwordx4 v136, s[22:23]
	s_mov_b32 m0, s15
	s_add_u32 s22, s26, 0x10000
	s_mov_b32 s15, m0
	s_mov_b32 m0, s37
	s_nop 0
	global_load_lds_dwordx4 v137, s[26:27]
	s_mov_b32 m0, s15
	s_addc_u32 s23, s27, 0
	s_mov_b32 s15, m0
	s_mov_b32 m0, s42
	s_nop 0
	global_load_lds_dwordx4 v137, s[22:23]
	s_mov_b32 m0, s15
	s_waitcnt vmcnt(8)
	s_waitcnt lgkmcnt(0)
	s_setprio 1
	s_barrier
	v_mfma_scale_f32_16x16x128_f8f6f4 v[60:63], v[146:153], v[64:71], v[60:63], v142, v142 op_sel_hi:[0,0,0]
	v_mfma_scale_f32_16x16x128_f8f6f4 v[56:59], v[154:161], v[64:71], v[56:59], v142, v142 op_sel_hi:[0,0,0]
	v_mfma_scale_f32_16x16x128_f8f6f4 v[52:55], v[146:153], v[72:79], v[52:55], v142, v142 op_sel_hi:[0,0,0]
	v_mfma_scale_f32_16x16x128_f8f6f4 v[48:51], v[154:161], v[72:79], v[48:51], v142, v142 op_sel_hi:[0,0,0]
	v_mfma_scale_f32_16x16x128_f8f6f4 v[194:197], v[146:153], v[80:87], v[28:31], v142, v142 op_sel_hi:[0,0,0]
	v_mfma_scale_f32_16x16x128_f8f6f4 v[198:201], v[154:161], v[80:87], v[24:27], v142, v142 op_sel_hi:[0,0,0]
	v_mfma_scale_f32_16x16x128_f8f6f4 v[202:205], v[146:153], v[88:95], v[12:15], v142, v142 op_sel_hi:[0,0,0]
	v_mfma_scale_f32_16x16x128_f8f6f4 v[206:209], v[154:161], v[88:95], v[8:11], v142, v142 op_sel_hi:[0,0,0]
	s_setprio 0
	s_setprio 1
	v_mfma_scale_f32_16x16x128_f8f6f4 v[222:225], v[162:169], v[64:71], v[44:47], v142, v142 op_sel_hi:[0,0,0]
	v_mfma_scale_f32_16x16x128_f8f6f4 v[226:229], v[170:177], v[64:71], v[40:43], v142, v142 op_sel_hi:[0,0,0]
	v_mfma_scale_f32_16x16x128_f8f6f4 v[230:233], v[162:169], v[72:79], v[36:39], v142, v142 op_sel_hi:[0,0,0]
	v_mfma_scale_f32_16x16x128_f8f6f4 v[234:237], v[170:177], v[72:79], v[32:35], v142, v142 op_sel_hi:[0,0,0]
	v_mfma_scale_f32_16x16x128_f8f6f4 v[238:241], v[162:169], v[80:87], v[20:23], v142, v142 op_sel_hi:[0,0,0]
	v_mfma_scale_f32_16x16x128_f8f6f4 v[242:245], v[170:177], v[80:87], v[16:19], v142, v142 op_sel_hi:[0,0,0]
	v_mfma_scale_f32_16x16x128_f8f6f4 v[246:249], v[162:169], v[88:95], v[4:7], v142, v142 op_sel_hi:[0,0,0]
	v_mfma_scale_f32_16x16x128_f8f6f4 v[250:253], v[170:177], v[88:95], v[0:3], v142, v142 op_sel_hi:[0,0,0]
	s_barrier
	s_setprio 0
	s_nop 4
	ds_read_b128 v[0:3], v143
	ds_read_b128 v[4:7], v143 offset:1024
	ds_read_b128 v[16:19], v143 offset:2048
	ds_read_b128 v[20:23], v143 offset:3072
	ds_read_b128 v[146:149], v144
	ds_read_b128 v[150:153], v144 offset:1024
	ds_read_b128 v[154:157], v144 offset:2048
	ds_read_b128 v[158:161], v144 offset:3072
	ds_read_b128 v[8:11], v141 offset:32768
	ds_read_b128 v[12:15], v141 offset:33792
	ds_read_b128 v[24:27], v141 offset:34816
	ds_read_b128 v[28:31], v141 offset:35840
	ds_read_b128 v[32:35], v141 offset:36864
	ds_read_b128 v[36:39], v141 offset:37888
	ds_read_b128 v[40:43], v141 offset:38912
	ds_read_b128 v[44:47], v141 offset:39936
	s_add_u32 s22, s26, 0x20000
	s_addc_u32 s23, s27, 0
	s_mov_b32 s15, m0
	s_mov_b32 m0, s43
	s_nop 0
	global_load_lds_dwordx4 v137, s[22:23]
	s_mov_b32 m0, s15
	s_add_u32 s22, s26, 0x30000
	s_addc_u32 s23, s27, 0
	s_mov_b32 s15, m0
	s_mov_b32 m0, s44
	s_nop 0
	global_load_lds_dwordx4 v137, s[22:23]
	s_mov_b32 m0, s15
	s_waitcnt vmcnt(8)
	s_waitcnt lgkmcnt(0)
	s_setprio 1
	s_barrier
	v_mfma_scale_f32_16x16x128_f8f6f4 v[124:127], v[0:7], v[8:15], v[124:127], v142, v142 op_sel_hi:[0,0,0]
	v_mfma_scale_f32_16x16x128_f8f6f4 v[120:123], v[16:23], v[8:15], v[120:123], v142, v142 op_sel_hi:[0,0,0]
	v_mfma_scale_f32_16x16x128_f8f6f4 v[116:119], v[0:7], v[24:31], v[116:119], v142, v142 op_sel_hi:[0,0,0]
	v_mfma_scale_f32_16x16x128_f8f6f4 v[112:115], v[16:23], v[24:31], v[112:115], v142, v142 op_sel_hi:[0,0,0]
	v_mfma_scale_f32_16x16x128_f8f6f4 v[92:95], v[0:7], v[32:39], v[128:131], v142, v142 op_sel_hi:[0,0,0]
	v_mfma_scale_f32_16x16x128_f8f6f4 v[88:91], v[16:23], v[32:39], v[210:213], v142, v142 op_sel_hi:[0,0,0]
	v_mfma_scale_f32_16x16x128_f8f6f4 v[84:87], v[0:7], v[40:47], v[214:217], v142, v142 op_sel_hi:[0,0,0]
	v_mfma_scale_f32_16x16x128_f8f6f4 v[80:83], v[16:23], v[40:47], v[218:221], v142, v142 op_sel_hi:[0,0,0]
	s_setprio 0
	s_setprio 1
	v_mfma_scale_f32_16x16x128_f8f6f4 v[108:111], v[146:153], v[8:15], v[108:111], v142, v142 op_sel_hi:[0,0,0]
	v_mfma_scale_f32_16x16x128_f8f6f4 v[104:107], v[154:161], v[8:15], v[104:107], v142, v142 op_sel_hi:[0,0,0]
	v_mfma_scale_f32_16x16x128_f8f6f4 v[100:103], v[146:153], v[24:31], v[100:103], v142, v142 op_sel_hi:[0,0,0]
	v_mfma_scale_f32_16x16x128_f8f6f4 v[96:99], v[154:161], v[24:31], v[96:99], v142, v142 op_sel_hi:[0,0,0]
	v_mfma_scale_f32_16x16x128_f8f6f4 v[76:79], v[146:153], v[32:39], v[178:181], v142, v142 op_sel_hi:[0,0,0]
	v_mfma_scale_f32_16x16x128_f8f6f4 v[72:75], v[154:161], v[32:39], v[182:185], v142, v142 op_sel_hi:[0,0,0]
	v_mfma_scale_f32_16x16x128_f8f6f4 v[68:71], v[146:153], v[40:47], v[186:189], v142, v142 op_sel_hi:[0,0,0]
	v_mfma_scale_f32_16x16x128_f8f6f4 v[64:67], v[154:161], v[40:47], v[190:193], v142, v142 op_sel_hi:[0,0,0]
	s_barrier
	s_setprio 0
	s_add_u32 s22, s30, 0x80
	s_addc_u32 s23, s31, 0
	ds_read_b128 v[32:35], v141 offset:49152
	ds_read_b128 v[36:39], v141 offset:50176
	ds_read_b128 v[162:165], v141 offset:51200
	ds_read_b128 v[166:169], v141 offset:52224
	ds_read_b128 v[170:173], v141 offset:53248
	ds_read_b128 v[174:177], v141 offset:54272
	ds_read_b128 v[178:181], v141 offset:55296
	ds_read_b128 v[182:185], v141 offset:56320
	s_mov_b32 s15, m0
	s_mov_b32 m0, s47
	s_nop 0
	global_load_lds_dwordx4 v136, s[22:23]
	s_mov_b32 m0, s15
	s_add_u32 s22, s30, 0x10080
	s_addc_u32 s23, s31, 0
	s_mov_b32 s15, m0
	s_mov_b32 m0, s49
	s_nop 0
	global_load_lds_dwordx4 v136, s[22:23]
	s_mov_b32 m0, s15
	s_add_u32 s22, s30, 0x20080
	s_addc_u32 s23, s31, 0
	s_mov_b32 s15, m0
	s_mov_b32 m0, s52
	s_nop 0
	global_load_lds_dwordx4 v136, s[22:23]
	s_mov_b32 m0, s15
	s_add_u32 s22, s30, 0x30080
	s_addc_u32 s23, s31, 0
	s_mov_b32 s15, m0
	s_mov_b32 m0, s53
	s_nop 0
	global_load_lds_dwordx4 v136, s[22:23]
	s_mov_b32 m0, s15
	s_add_u32 s22, s26, 0x10080
	s_mov_b32 s15, m0
	s_mov_b32 m0, s50
	s_nop 0
	global_load_lds_dwordx4 v137, s[28:29]
	s_mov_b32 m0, s15
	s_addc_u32 s23, s27, 0
	s_mov_b32 s15, m0
	s_mov_b32 m0, s51
	s_nop 0
	global_load_lds_dwordx4 v137, s[22:23]
	s_mov_b32 m0, s15
	s_waitcnt vmcnt(8)
	s_waitcnt lgkmcnt(0)
	s_setprio 1
	s_barrier
	v_mfma_scale_f32_16x16x128_f8f6f4 v[60:63], v[0:7], v[32:39], v[60:63], v142, v142 op_sel_hi:[0,0,0]
	v_mfma_scale_f32_16x16x128_f8f6f4 v[56:59], v[16:23], v[32:39], v[56:59], v142, v142 op_sel_hi:[0,0,0]
	v_mfma_scale_f32_16x16x128_f8f6f4 v[52:55], v[0:7], v[162:169], v[52:55], v142, v142 op_sel_hi:[0,0,0]
	v_mfma_scale_f32_16x16x128_f8f6f4 v[48:51], v[16:23], v[162:169], v[48:51], v142, v142 op_sel_hi:[0,0,0]
	v_mfma_scale_f32_16x16x128_f8f6f4 v[28:31], v[0:7], v[170:177], v[194:197], v142, v142 op_sel_hi:[0,0,0]
	v_mfma_scale_f32_16x16x128_f8f6f4 v[24:27], v[16:23], v[170:177], v[198:201], v142, v142 op_sel_hi:[0,0,0]
	v_mfma_scale_f32_16x16x128_f8f6f4 v[12:15], v[0:7], v[178:185], v[202:205], v142, v142 op_sel_hi:[0,0,0]
	v_mfma_scale_f32_16x16x128_f8f6f4 v[8:11], v[16:23], v[178:185], v[206:209], v142, v142 op_sel_hi:[0,0,0]
	s_setprio 0
	s_setprio 1
	v_mfma_scale_f32_16x16x128_f8f6f4 v[44:47], v[146:153], v[32:39], v[222:225], v142, v142 op_sel_hi:[0,0,0]
	v_mfma_scale_f32_16x16x128_f8f6f4 v[40:43], v[154:161], v[32:39], v[226:229], v142, v142 op_sel_hi:[0,0,0]
	v_mfma_scale_f32_16x16x128_f8f6f4 v[36:39], v[146:153], v[162:169], v[230:233], v142, v142 op_sel_hi:[0,0,0]
	v_mfma_scale_f32_16x16x128_f8f6f4 v[32:35], v[154:161], v[162:169], v[234:237], v142, v142 op_sel_hi:[0,0,0]
	v_mfma_scale_f32_16x16x128_f8f6f4 v[20:23], v[146:153], v[170:177], v[238:241], v142, v142 op_sel_hi:[0,0,0]
	v_mfma_scale_f32_16x16x128_f8f6f4 v[16:19], v[154:161], v[170:177], v[242:245], v142, v142 op_sel_hi:[0,0,0]
	v_mfma_scale_f32_16x16x128_f8f6f4 v[4:7], v[146:153], v[178:185], v[246:249], v142, v142 op_sel_hi:[0,0,0]
	v_mfma_scale_f32_16x16x128_f8f6f4 v[0:3], v[154:161], v[178:185], v[250:253], v142, v142 op_sel_hi:[0,0,0]
	s_barrier
	s_setprio 0
	s_add_i32 s13, s13, 2
	s_add_u32 s1, s1, 0x100
	s_addc_u32 s11, s11, 0
	s_cmp_gt_u32 s13, 5
	s_mov_b64 s[22:23], s[24:25]
	s_cbranch_scc0 .LBB0_1338
	s_and_b64 vcc, exec, s[8:9]
	s_cbranch_vccz .LBB0_1341
	s_barrier

.LBB0_2302:
	s_ashr_i32 s9, s8, 31
	s_lshl_b64 s[12:13], s[8:9], 18
	v_readlane_b32 s16, v254, 49
	v_readlane_b32 s17, v254, 50
	s_add_u32 s12, s16, s12
	s_addc_u32 s13, s17, s13
	s_and_b64 s[16:17], s[14:15], exec
	ds_read_b128 v[0:3], v203
	ds_read_b128 v[4:7], v203 offset:1024
	ds_read_b128 v[8:11], v203 offset:2048
	ds_read_b128 v[12:15], v203 offset:3072
	ds_read_b128 v[16:19], v204
	ds_read_b128 v[20:23], v204 offset:1024
	ds_read_b128 v[24:27], v204 offset:2048
	ds_read_b128 v[28:31], v204 offset:3072
	s_cselect_b32 s9, s13, s25
	s_cselect_b32 s54, s12, s24
	s_ashr_i32 s11, s10, 31
	s_lshl_b64 s[16:17], s[10:11], 18
	s_add_u32 s16, s33, s16
	s_addc_u32 s17, s34, s17
	s_and_b64 s[26:27], s[14:15], exec
	s_cselect_b32 s11, s17, s23
	s_cselect_b32 s55, s16, s22
	s_add_u32 s26, s24, 0x100
	s_addc_u32 s27, s25, 0
	s_add_u32 s28, s24, 0x180
	s_addc_u32 s29, s25, 0
	s_add_u32 s30, s22, 0x100
	s_addc_u32 s31, s23, 0
	ds_read_b128 v[32:35], v205
	ds_read_b128 v[36:39], v205 offset:1024
	ds_read_b128 v[40:43], v205 offset:2048
	ds_read_b128 v[44:47], v205 offset:3072
	ds_read_b128 v[48:51], v205 offset:4096
	ds_read_b128 v[52:55], v205 offset:5120
	ds_read_b128 v[56:59], v205 offset:6144
	ds_read_b128 v[60:63], v205 offset:7168
	s_add_u32 s56, s24, 0x20080
	s_addc_u32 s57, s25, 0
	s_mov_b32 s58, m0
	s_mov_b32 m0, s52
	s_nop 0
	global_load_lds_dwordx4 v202, s[56:57]
	s_mov_b32 m0, s58
	s_add_u32 s56, s24, 0x30080
	s_addc_u32 s57, s25, 0
	s_mov_b32 s58, m0
	s_mov_b32 m0, s53
	s_nop 0
	global_load_lds_dwordx4 v202, s[56:57]
	s_mov_b32 m0, s58
	s_waitcnt vmcnt(8)
	s_waitcnt lgkmcnt(0)
	s_setprio 1
	s_barrier
	s_waitcnt vmcnt(4) lgkmcnt(6)
	v_mfma_scale_f32_16x16x128_f8f6f4 v[64:67], v[0:7], v[32:39], 0, v206, v206 op_sel_hi:[0,0,0]
	s_waitcnt vmcnt(3)
	v_mfma_scale_f32_16x16x128_f8f6f4 v[68:71], v[8:15], v[32:39], 0, v206, v206 op_sel_hi:[0,0,0]
	s_waitcnt vmcnt(2) lgkmcnt(4)
	v_mfma_scale_f32_16x16x128_f8f6f4 v[72:75], v[0:7], v[40:47], 0, v206, v206 op_sel_hi:[0,0,0]
	s_waitcnt vmcnt(0)
	v_mfma_scale_f32_16x16x128_f8f6f4 v[76:79], v[8:15], v[40:47], 0, v206, v206 op_sel_hi:[0,0,0]
	v_mfma_scale_f32_16x16x128_f8f6f4 v[80:83], v[0:7], v[48:55], 0, v206, v206 op_sel_hi:[0,0,0]
	v_mfma_scale_f32_16x16x128_f8f6f4 v[84:87], v[8:15], v[48:55], 0, v206, v206 op_sel_hi:[0,0,0]
	v_mfma_scale_f32_16x16x128_f8f6f4 v[88:91], v[0:7], v[56:63], 0, v206, v206 op_sel_hi:[0,0,0]
	v_mfma_scale_f32_16x16x128_f8f6f4 v[100:103], v[8:15], v[56:63], 0, v206, v206 op_sel_hi:[0,0,0]
	s_setprio 0
	s_setprio 1
	v_mfma_scale_f32_16x16x128_f8f6f4 v[108:111], v[16:23], v[32:39], 0, v206, v206 op_sel_hi:[0,0,0]
	v_mfma_scale_f32_16x16x128_f8f6f4 v[120:123], v[24:31], v[32:39], 0, v206, v206 op_sel_hi:[0,0,0]
	v_mfma_scale_f32_16x16x128_f8f6f4 v[132:135], v[16:23], v[40:47], 0, v206, v206 op_sel_hi:[0,0,0]
	v_mfma_scale_f32_16x16x128_f8f6f4 v[152:155], v[24:31], v[40:47], 0, v206, v206 op_sel_hi:[0,0,0]
	v_mfma_scale_f32_16x16x128_f8f6f4 v[156:159], v[16:23], v[48:55], 0, v206, v206 op_sel_hi:[0,0,0]
	v_mfma_scale_f32_16x16x128_f8f6f4 v[160:163], v[24:31], v[48:55], 0, v206, v206 op_sel_hi:[0,0,0]
	v_mfma_scale_f32_16x16x128_f8f6f4 v[164:167], v[16:23], v[56:63], 0, v206, v206 op_sel_hi:[0,0,0]
	v_mfma_scale_f32_16x16x128_f8f6f4 v[168:171], v[24:31], v[56:63], 0, v206, v206 op_sel_hi:[0,0,0]
	s_barrier
	s_setprio 0
	ds_read_b128 v[32:35], v205 offset:16384
	ds_read_b128 v[36:39], v205 offset:17408
	ds_read_b128 v[40:43], v205 offset:18432
	ds_read_b128 v[44:47], v205 offset:19456
	ds_read_b128 v[48:51], v205 offset:20480
	ds_read_b128 v[52:55], v205 offset:21504
	ds_read_b128 v[56:59], v205 offset:22528
	ds_read_b128 v[60:63], v205 offset:23552
	s_mov_b32 s56, m0
	s_mov_b32 m0, s19
	s_nop 0
	global_load_lds_dwordx4 v201, s[30:31]
	s_mov_b32 m0, s56
	s_add_u32 s30, s22, 0x10100
	s_addc_u32 s31, s23, 0
	s_mov_b32 s56, m0
	s_mov_b32 m0, s21
	s_nop 0
	global_load_lds_dwordx4 v201, s[30:31]
	s_mov_b32 m0, s56
	s_add_u32 s30, s22, 0x20100
	s_addc_u32 s31, s23, 0
	s_mov_b32 s56, m0
	s_mov_b32 m0, s36
	s_nop 0
	global_load_lds_dwordx4 v201, s[30:31]
	s_mov_b32 m0, s56
	s_add_u32 s30, s22, 0x30100
	s_addc_u32 s31, s23, 0
	s_mov_b32 s56, m0
	s_mov_b32 m0, s37
	s_nop 0
	global_load_lds_dwordx4 v201, s[30:31]
	s_mov_b32 m0, s56
	s_mov_b32 s30, m0
	s_mov_b32 m0, s35
	s_nop 0
	global_load_lds_dwordx4 v202, s[26:27]
	s_mov_b32 m0, s30
	s_add_u32 s30, s24, 0x10100
	s_addc_u32 s31, s25, 0
	s_mov_b32 s56, m0
	s_mov_b32 m0, s38
	s_nop 0
	global_load_lds_dwordx4 v202, s[30:31]
	s_mov_b32 m0, s56
	s_waitcnt vmcnt(8)
	s_waitcnt lgkmcnt(0)
	s_setprio 1
	s_barrier
	v_mfma_scale_f32_16x16x128_f8f6f4 v[176:179], v[0:7], v[32:39], 0, v206, v206 op_sel_hi:[0,0,0]
	v_mfma_scale_f32_16x16x128_f8f6f4 v[180:183], v[8:15], v[32:39], 0, v206, v206 op_sel_hi:[0,0,0]
	v_mfma_scale_f32_16x16x128_f8f6f4 v[184:187], v[0:7], v[40:47], 0, v206, v206 op_sel_hi:[0,0,0]
	v_mfma_scale_f32_16x16x128_f8f6f4 v[188:191], v[8:15], v[40:47], 0, v206, v206 op_sel_hi:[0,0,0]
	v_mfma_scale_f32_16x16x128_f8f6f4 v[192:195], v[0:7], v[48:55], 0, v206, v206 op_sel_hi:[0,0,0]
	v_mfma_scale_f32_16x16x128_f8f6f4 v[196:199], v[8:15], v[48:55], 0, v206, v206 op_sel_hi:[0,0,0]
	v_mfma_scale_f32_16x16x128_f8f6f4 v[210:213], v[0:7], v[56:63], 0, v206, v206 op_sel_hi:[0,0,0]
	v_mfma_scale_f32_16x16x128_f8f6f4 v[214:217], v[8:15], v[56:63], 0, v206, v206 op_sel_hi:[0,0,0]
	s_setprio 0
	s_setprio 1
	v_mfma_scale_f32_16x16x128_f8f6f4 v[218:221], v[16:23], v[32:39], 0, v206, v206 op_sel_hi:[0,0,0]
	v_mfma_scale_f32_16x16x128_f8f6f4 v[222:225], v[24:31], v[32:39], 0, v206, v206 op_sel_hi:[0,0,0]
	v_mfma_scale_f32_16x16x128_f8f6f4 v[226:229], v[16:23], v[40:47], 0, v206, v206 op_sel_hi:[0,0,0]
	v_mfma_scale_f32_16x16x128_f8f6f4 v[230:233], v[24:31], v[40:47], 0, v206, v206 op_sel_hi:[0,0,0]
	v_mfma_scale_f32_16x16x128_f8f6f4 v[234:237], v[16:23], v[48:55], 0, v206, v206 op_sel_hi:[0,0,0]
	v_mfma_scale_f32_16x16x128_f8f6f4 v[238:241], v[24:31], v[48:55], 0, v206, v206 op_sel_hi:[0,0,0]
	v_mfma_scale_f32_16x16x128_f8f6f4 v[242:245], v[16:23], v[56:63], 0, v206, v206 op_sel_hi:[0,0,0]
	v_mfma_scale_f32_16x16x128_f8f6f4 v[246:249], v[24:31], v[56:63], 0, v206, v206 op_sel_hi:[0,0,0]
	s_barrier
	s_setprio 0
	ds_read_b128 v[0:3], v207
	ds_read_b128 v[4:7], v207 offset:1024
	ds_read_b128 v[16:19], v207 offset:2048
	ds_read_b128 v[20:23], v207 offset:3072
	ds_read_b128 v[112:115], v208
	ds_read_b128 v[116:119], v208 offset:1024
	ds_read_b128 v[144:147], v208 offset:2048
	ds_read_b128 v[148:151], v208 offset:3072
	ds_read_b128 v[8:11], v205 offset:32768
	ds_read_b128 v[12:15], v205 offset:33792
	ds_read_b128 v[24:27], v205 offset:34816
	ds_read_b128 v[28:31], v205 offset:35840
	ds_read_b128 v[32:35], v205 offset:36864
	ds_read_b128 v[36:39], v205 offset:37888
	ds_read_b128 v[40:43], v205 offset:38912
	ds_read_b128 v[44:47], v205 offset:39936
	s_add_u32 s30, s24, 0x20100
	s_addc_u32 s31, s25, 0
	s_mov_b32 s56, m0
	s_mov_b32 m0, s39
	s_nop 0
	global_load_lds_dwordx4 v202, s[30:31]
	s_mov_b32 m0, s56
	s_add_u32 s30, s24, 0x30100
	s_addc_u32 s31, s25, 0
	s_mov_b32 s56, m0
	s_mov_b32 m0, s40
	s_nop 0
	global_load_lds_dwordx4 v202, s[30:31]
	s_mov_b32 m0, s56
	s_waitcnt vmcnt(8)
	s_waitcnt lgkmcnt(0)
	s_setprio 1
	s_barrier
	v_mfma_scale_f32_16x16x128_f8f6f4 v[128:131], v[0:7], v[8:15], v[64:67], v206, v206 op_sel_hi:[0,0,0]
	v_mfma_scale_f32_16x16x128_f8f6f4 v[124:127], v[16:23], v[8:15], v[68:71], v206, v206 op_sel_hi:[0,0,0]
	v_mfma_scale_f32_16x16x128_f8f6f4 v[104:107], v[0:7], v[24:31], v[72:75], v206, v206 op_sel_hi:[0,0,0]
	v_mfma_scale_f32_16x16x128_f8f6f4 v[96:99], v[16:23], v[24:31], v[76:79], v206, v206 op_sel_hi:[0,0,0]
	v_mfma_scale_f32_16x16x128_f8f6f4 v[92:95], v[0:7], v[32:39], v[80:83], v206, v206 op_sel_hi:[0,0,0]
	v_mfma_scale_f32_16x16x128_f8f6f4 v[84:87], v[16:23], v[32:39], v[84:87], v206, v206 op_sel_hi:[0,0,0]
	v_mfma_scale_f32_16x16x128_f8f6f4 v[68:71], v[0:7], v[40:47], v[88:91], v206, v206 op_sel_hi:[0,0,0]
	v_mfma_scale_f32_16x16x128_f8f6f4 v[56:59], v[16:23], v[40:47], v[100:103], v206, v206 op_sel_hi:[0,0,0]
	s_setprio 0
	s_setprio 1
	v_mfma_scale_f32_16x16x128_f8f6f4 v[140:143], v[112:119], v[8:15], v[108:111], v206, v206 op_sel_hi:[0,0,0]
	v_mfma_scale_f32_16x16x128_f8f6f4 v[136:139], v[144:151], v[8:15], v[120:123], v206, v206 op_sel_hi:[0,0,0]
	v_mfma_scale_f32_16x16x128_f8f6f4 v[108:111], v[112:119], v[24:31], v[132:135], v206, v206 op_sel_hi:[0,0,0]
	v_mfma_scale_f32_16x16x128_f8f6f4 v[100:103], v[144:151], v[24:31], v[152:155], v206, v206 op_sel_hi:[0,0,0]
	v_mfma_scale_f32_16x16x128_f8f6f4 v[88:91], v[112:119], v[32:39], v[156:159], v206, v206 op_sel_hi:[0,0,0]
	v_mfma_scale_f32_16x16x128_f8f6f4 v[80:83], v[144:151], v[32:39], v[160:163], v206, v206 op_sel_hi:[0,0,0]
	v_mfma_scale_f32_16x16x128_f8f6f4 v[52:55], v[112:119], v[40:47], v[164:167], v206, v206 op_sel_hi:[0,0,0]
	v_mfma_scale_f32_16x16x128_f8f6f4 v[48:51], v[144:151], v[40:47], v[168:171], v206, v206 op_sel_hi:[0,0,0]
	s_barrier
	s_setprio 0
	s_add_u32 s30, s22, 0x180
	s_addc_u32 s31, s23, 0
	ds_read_b128 v[32:35], v205 offset:49152
	ds_read_b128 v[36:39], v205 offset:50176
	ds_read_b128 v[152:155], v205 offset:51200
	ds_read_b128 v[156:159], v205 offset:52224
	ds_read_b128 v[160:163], v205 offset:53248
	ds_read_b128 v[164:167], v205 offset:54272
	ds_read_b128 v[168:171], v205 offset:55296
	ds_read_b128 v[172:175], v205 offset:56320
	s_mov_b32 s56, m0
	s_mov_b32 m0, s46
	s_nop 0
	global_load_lds_dwordx4 v201, s[30:31]
	s_mov_b32 m0, s56
	s_add_u32 s30, s22, 0x10180
	s_addc_u32 s31, s23, 0
	s_mov_b32 s56, m0
	s_mov_b32 m0, s47
	s_nop 0
	global_load_lds_dwordx4 v201, s[30:31]
	s_mov_b32 m0, s56
	s_add_u32 s30, s22, 0x20180
	s_addc_u32 s31, s23, 0
	s_mov_b32 s56, m0
	s_mov_b32 m0, s50
	s_nop 0
	global_load_lds_dwordx4 v201, s[30:31]
	s_mov_b32 m0, s56
	s_add_u32 s30, s22, 0x30180
	s_addc_u32 s31, s23, 0
	s_mov_b32 s56, m0
	s_mov_b32 m0, s51
	s_nop 0
	global_load_lds_dwordx4 v201, s[30:31]
	s_mov_b32 m0, s56
	s_mov_b32 s30, m0
	s_mov_b32 m0, s48
	s_nop 0
	global_load_lds_dwordx4 v202, s[28:29]
	s_mov_b32 m0, s30
	s_add_u32 s24, s24, 0x10180
	s_addc_u32 s25, s25, 0
	s_mov_b32 s28, m0
	s_mov_b32 m0, s49
	s_nop 0
	global_load_lds_dwordx4 v202, s[24:25]
	s_mov_b32 m0, s28
	s_waitcnt vmcnt(8)
	s_waitcnt lgkmcnt(0)
	s_setprio 1
	s_barrier
	v_mfma_scale_f32_16x16x128_f8f6f4 v[76:79], v[0:7], v[32:39], v[176:179], v206, v206 op_sel_hi:[0,0,0]
	v_mfma_scale_f32_16x16x128_f8f6f4 v[64:67], v[16:23], v[32:39], v[180:183], v206, v206 op_sel_hi:[0,0,0]
	v_mfma_scale_f32_16x16x128_f8f6f4 v[44:47], v[0:7], v[152:159], v[184:187], v206, v206 op_sel_hi:[0,0,0]
	v_mfma_scale_f32_16x16x128_f8f6f4 v[40:43], v[16:23], v[152:159], v[188:191], v206, v206 op_sel_hi:[0,0,0]
	v_mfma_scale_f32_16x16x128_f8f6f4 v[28:31], v[0:7], v[160:167], v[192:195], v206, v206 op_sel_hi:[0,0,0]
	v_mfma_scale_f32_16x16x128_f8f6f4 v[24:27], v[16:23], v[160:167], v[196:199], v206, v206 op_sel_hi:[0,0,0]
	v_mfma_scale_f32_16x16x128_f8f6f4 v[12:15], v[0:7], v[168:175], v[210:213], v206, v206 op_sel_hi:[0,0,0]
	v_mfma_scale_f32_16x16x128_f8f6f4 v[8:11], v[16:23], v[168:175], v[214:217], v206, v206 op_sel_hi:[0,0,0]
	s_setprio 0
	s_setprio 1
	v_mfma_scale_f32_16x16x128_f8f6f4 v[72:75], v[112:119], v[32:39], v[218:221], v206, v206 op_sel_hi:[0,0,0]
	v_mfma_scale_f32_16x16x128_f8f6f4 v[60:63], v[144:151], v[32:39], v[222:225], v206, v206 op_sel_hi:[0,0,0]
	v_mfma_scale_f32_16x16x128_f8f6f4 v[36:39], v[112:119], v[152:159], v[226:229], v206, v206 op_sel_hi:[0,0,0]
	v_mfma_scale_f32_16x16x128_f8f6f4 v[32:35], v[144:151], v[152:159], v[230:233], v206, v206 op_sel_hi:[0,0,0]
	v_mfma_scale_f32_16x16x128_f8f6f4 v[20:23], v[112:119], v[160:167], v[234:237], v206, v206 op_sel_hi:[0,0,0]
	v_mfma_scale_f32_16x16x128_f8f6f4 v[16:19], v[144:151], v[160:167], v[238:241], v206, v206 op_sel_hi:[0,0,0]
	v_mfma_scale_f32_16x16x128_f8f6f4 v[4:7], v[112:119], v[168:175], v[242:245], v206, v206 op_sel_hi:[0,0,0]
	v_mfma_scale_f32_16x16x128_f8f6f4 v[0:3], v[144:151], v[168:175], v[246:249], v206, v206 op_sel_hi:[0,0,0]
	s_barrier
	s_setprio 0
	s_add_u32 s56, s22, 0x200
	s_addc_u32 s57, s23, 0
	s_mov_b32 s58, 0
.LBB0_2303:
	ds_read_b128 v[112:115], v203
	ds_read_b128 v[116:119], v203 offset:1024
	ds_read_b128 v[144:147], v203 offset:2048
	ds_read_b128 v[148:151], v203 offset:3072
	ds_read_b128 v[152:155], v204
	ds_read_b128 v[156:159], v204 offset:1024
	ds_read_b128 v[160:163], v204 offset:2048
	ds_read_b128 v[164:167], v204 offset:3072
	s_add_u32 s22, s26, 0x100
	s_addc_u32 s23, s27, 0
	s_cmp_eq_u32 s58, 4
	s_cselect_b32 s24, s54, s22
	s_cselect_b32 s25, s9, s23
	s_cselect_b32 s30, s55, s56
	s_cselect_b32 s31, s11, s57
	s_add_u32 s28, s24, 0x80
	s_addc_u32 s29, s25, 0
	ds_read_b128 v[168:171], v205
	ds_read_b128 v[172:175], v205 offset:1024
	ds_read_b128 v[176:179], v205 offset:2048
	ds_read_b128 v[180:183], v205 offset:3072
	ds_read_b128 v[184:187], v205 offset:4096
	ds_read_b128 v[188:191], v205 offset:5120
	ds_read_b128 v[192:195], v205 offset:6144
	ds_read_b128 v[196:199], v205 offset:7168
	s_add_u32 s60, s26, 0x20080
	s_addc_u32 s61, s27, 0
	s_mov_b32 s59, m0
	s_mov_b32 m0, s52
	s_nop 0
	global_load_lds_dwordx4 v202, s[60:61]
	s_mov_b32 m0, s59
	s_add_u32 s26, s26, 0x30080
	s_addc_u32 s27, s27, 0
	s_mov_b32 s59, m0
	s_mov_b32 m0, s53
	s_nop 0
	global_load_lds_dwordx4 v202, s[26:27]
	s_mov_b32 m0, s59
	s_waitcnt vmcnt(8)
	s_waitcnt lgkmcnt(0)
	s_setprio 1
	s_barrier
	v_mfma_scale_f32_16x16x128_f8f6f4 v[124:127], v[144:151], v[168:175], v[124:127], v206, v206 op_sel_hi:[0,0,0]
	v_mfma_scale_f32_16x16x128_f8f6f4 v[104:107], v[112:119], v[176:183], v[104:107], v206, v206 op_sel_hi:[0,0,0]
	v_mfma_scale_f32_16x16x128_f8f6f4 v[68:71], v[112:119], v[192:199], v[68:71], v206, v206 op_sel_hi:[0,0,0]
	v_mfma_scale_f32_16x16x128_f8f6f4 v[56:59], v[144:151], v[192:199], v[56:59], v206, v206 op_sel_hi:[0,0,0]
	v_mfma_scale_f32_16x16x128_f8f6f4 v[120:123], v[112:119], v[168:175], v[128:131], v206, v206 op_sel_hi:[0,0,0]
	v_mfma_scale_f32_16x16x128_f8f6f4 v[132:135], v[144:151], v[176:183], v[96:99], v206, v206 op_sel_hi:[0,0,0]
	v_mfma_scale_f32_16x16x128_f8f6f4 v[210:213], v[112:119], v[184:191], v[92:95], v206, v206 op_sel_hi:[0,0,0]
	v_mfma_scale_f32_16x16x128_f8f6f4 v[214:217], v[144:151], v[184:191], v[84:87], v206, v206 op_sel_hi:[0,0,0]
	s_setprio 0
	s_setprio 1
	v_mfma_scale_f32_16x16x128_f8f6f4 v[140:143], v[152:159], v[168:175], v[140:143], v206, v206 op_sel_hi:[0,0,0]
	v_mfma_scale_f32_16x16x128_f8f6f4 v[136:139], v[160:167], v[168:175], v[136:139], v206, v206 op_sel_hi:[0,0,0]
	v_mfma_scale_f32_16x16x128_f8f6f4 v[108:111], v[152:159], v[176:183], v[108:111], v206, v206 op_sel_hi:[0,0,0]
	v_mfma_scale_f32_16x16x128_f8f6f4 v[168:171], v[160:167], v[176:183], v[100:103], v206, v206 op_sel_hi:[0,0,0]
	v_mfma_scale_f32_16x16x128_f8f6f4 v[172:175], v[152:159], v[184:191], v[88:91], v206, v206 op_sel_hi:[0,0,0]
	v_mfma_scale_f32_16x16x128_f8f6f4 v[176:179], v[160:167], v[184:191], v[80:83], v206, v206 op_sel_hi:[0,0,0]
	v_mfma_scale_f32_16x16x128_f8f6f4 v[180:183], v[152:159], v[192:199], v[52:55], v206, v206 op_sel_hi:[0,0,0]
	v_mfma_scale_f32_16x16x128_f8f6f4 v[184:187], v[160:167], v[192:199], v[48:51], v206, v206 op_sel_hi:[0,0,0]
	s_barrier
	s_setprio 0
	s_nop 4
	ds_read_b128 v[48:51], v205 offset:16384
	ds_read_b128 v[52:55], v205 offset:17408
	ds_read_b128 v[80:83], v205 offset:18432
	ds_read_b128 v[84:87], v205 offset:19456
	ds_read_b128 v[88:91], v205 offset:20480
	ds_read_b128 v[92:95], v205 offset:21504
	ds_read_b128 v[96:99], v205 offset:22528
	ds_read_b128 v[100:103], v205 offset:23552
	s_mov_b32 s26, m0
	s_mov_b32 m0, s19
	s_nop 0
	global_load_lds_dwordx4 v201, s[30:31]
	s_mov_b32 m0, s26
	s_add_u32 s26, s30, 0x10000
	s_addc_u32 s27, s31, 0
	s_mov_b32 s59, m0
	s_mov_b32 m0, s21
	s_nop 0
	global_load_lds_dwordx4 v201, s[26:27]
	s_mov_b32 m0, s59
	s_add_u32 s26, s30, 0x20000
	s_addc_u32 s27, s31, 0
	s_mov_b32 s59, m0
	s_mov_b32 m0, s36
	s_nop 0
	global_load_lds_dwordx4 v201, s[26:27]
	s_mov_b32 m0, s59
	s_add_u32 s26, s30, 0x30000
	s_addc_u32 s27, s31, 0
	s_mov_b32 s59, m0
	s_mov_b32 m0, s37
	s_nop 0
	global_load_lds_dwordx4 v201, s[26:27]
	s_mov_b32 m0, s59
	s_mov_b32 s26, m0
	s_mov_b32 m0, s35
	s_nop 0
	global_load_lds_dwordx4 v202, s[24:25]
	s_mov_b32 m0, s26
	s_add_u32 s26, s24, 0x10000
	s_addc_u32 s27, s25, 0
	s_mov_b32 s59, m0
	s_mov_b32 m0, s38
	s_nop 0
	global_load_lds_dwordx4 v202, s[26:27]
	s_mov_b32 m0, s59
	s_waitcnt vmcnt(8)
	s_waitcnt lgkmcnt(0)
	s_setprio 1
	s_barrier
	v_mfma_scale_f32_16x16x128_f8f6f4 v[76:79], v[112:119], v[48:55], v[76:79], v206, v206 op_sel_hi:[0,0,0]
	v_mfma_scale_f32_16x16x128_f8f6f4 v[64:67], v[144:151], v[48:55], v[64:67], v206, v206 op_sel_hi:[0,0,0]
	v_mfma_scale_f32_16x16x128_f8f6f4 v[188:191], v[112:119], v[80:87], v[44:47], v206, v206 op_sel_hi:[0,0,0]
	v_mfma_scale_f32_16x16x128_f8f6f4 v[192:195], v[144:151], v[80:87], v[40:43], v206, v206 op_sel_hi:[0,0,0]
	v_mfma_scale_f32_16x16x128_f8f6f4 v[196:199], v[112:119], v[88:95], v[28:31], v206, v206 op_sel_hi:[0,0,0]
	v_mfma_scale_f32_16x16x128_f8f6f4 v[218:221], v[144:151], v[88:95], v[24:27], v206, v206 op_sel_hi:[0,0,0]
	v_mfma_scale_f32_16x16x128_f8f6f4 v[222:225], v[112:119], v[96:103], v[12:15], v206, v206 op_sel_hi:[0,0,0]
	v_mfma_scale_f32_16x16x128_f8f6f4 v[226:229], v[144:151], v[96:103], v[8:11], v206, v206 op_sel_hi:[0,0,0]
	s_setprio 0
	s_setprio 1
	v_mfma_scale_f32_16x16x128_f8f6f4 v[72:75], v[152:159], v[48:55], v[72:75], v206, v206 op_sel_hi:[0,0,0]
	v_mfma_scale_f32_16x16x128_f8f6f4 v[60:63], v[160:167], v[48:55], v[60:63], v206, v206 op_sel_hi:[0,0,0]
	v_mfma_scale_f32_16x16x128_f8f6f4 v[230:233], v[152:159], v[80:87], v[36:39], v206, v206 op_sel_hi:[0,0,0]
	v_mfma_scale_f32_16x16x128_f8f6f4 v[234:237], v[160:167], v[80:87], v[32:35], v206, v206 op_sel_hi:[0,0,0]
	v_mfma_scale_f32_16x16x128_f8f6f4 v[238:241], v[152:159], v[88:95], v[20:23], v206, v206 op_sel_hi:[0,0,0]
	v_mfma_scale_f32_16x16x128_f8f6f4 v[242:245], v[160:167], v[88:95], v[16:19], v206, v206 op_sel_hi:[0,0,0]
	v_mfma_scale_f32_16x16x128_f8f6f4 v[246:249], v[152:159], v[96:103], v[4:7], v206, v206 op_sel_hi:[0,0,0]
	v_mfma_scale_f32_16x16x128_f8f6f4 v[250:253], v[160:167], v[96:103], v[0:3], v206, v206 op_sel_hi:[0,0,0]
	s_barrier
	s_setprio 0
	s_nop 4
	ds_read_b128 v[0:3], v207
	ds_read_b128 v[4:7], v207 offset:1024
	ds_read_b128 v[16:19], v207 offset:2048
	ds_read_b128 v[20:23], v207 offset:3072
	ds_read_b128 v[112:115], v208
	ds_read_b128 v[116:119], v208 offset:1024
	ds_read_b128 v[144:147], v208 offset:2048
	ds_read_b128 v[148:151], v208 offset:3072
	ds_read_b128 v[8:11], v205 offset:32768
	ds_read_b128 v[12:15], v205 offset:33792
	ds_read_b128 v[24:27], v205 offset:34816
	ds_read_b128 v[28:31], v205 offset:35840
	ds_read_b128 v[32:35], v205 offset:36864
	ds_read_b128 v[36:39], v205 offset:37888
	ds_read_b128 v[40:43], v205 offset:38912
	ds_read_b128 v[44:47], v205 offset:39936
	s_add_u32 s26, s24, 0x20000
	s_addc_u32 s27, s25, 0
	s_mov_b32 s59, m0
	s_mov_b32 m0, s39
	s_nop 0
	global_load_lds_dwordx4 v202, s[26:27]
	s_mov_b32 m0, s59
	s_add_u32 s26, s24, 0x30000
	s_addc_u32 s27, s25, 0
	s_mov_b32 s59, m0
	s_mov_b32 m0, s40
	s_nop 0
	global_load_lds_dwordx4 v202, s[26:27]
	s_mov_b32 m0, s59
	s_waitcnt vmcnt(8)
	s_waitcnt lgkmcnt(0)
	s_setprio 1
	s_barrier
	v_mfma_scale_f32_16x16x128_f8f6f4 v[128:131], v[0:7], v[8:15], v[120:123], v206, v206 op_sel_hi:[0,0,0]
	v_mfma_scale_f32_16x16x128_f8f6f4 v[124:127], v[16:23], v[8:15], v[124:127], v206, v206 op_sel_hi:[0,0,0]
	v_mfma_scale_f32_16x16x128_f8f6f4 v[104:107], v[0:7], v[24:31], v[104:107], v206, v206 op_sel_hi:[0,0,0]
	v_mfma_scale_f32_16x16x128_f8f6f4 v[96:99], v[16:23], v[24:31], v[132:135], v206, v206 op_sel_hi:[0,0,0]
	v_mfma_scale_f32_16x16x128_f8f6f4 v[92:95], v[0:7], v[32:39], v[210:213], v206, v206 op_sel_hi:[0,0,0]
	v_mfma_scale_f32_16x16x128_f8f6f4 v[84:87], v[16:23], v[32:39], v[214:217], v206, v206 op_sel_hi:[0,0,0]
	v_mfma_scale_f32_16x16x128_f8f6f4 v[68:71], v[0:7], v[40:47], v[68:71], v206, v206 op_sel_hi:[0,0,0]
	v_mfma_scale_f32_16x16x128_f8f6f4 v[56:59], v[16:23], v[40:47], v[56:59], v206, v206 op_sel_hi:[0,0,0]
	s_setprio 0
	s_setprio 1
	v_mfma_scale_f32_16x16x128_f8f6f4 v[140:143], v[112:119], v[8:15], v[140:143], v206, v206 op_sel_hi:[0,0,0]
	v_mfma_scale_f32_16x16x128_f8f6f4 v[136:139], v[144:151], v[8:15], v[136:139], v206, v206 op_sel_hi:[0,0,0]
	v_mfma_scale_f32_16x16x128_f8f6f4 v[108:111], v[112:119], v[24:31], v[108:111], v206, v206 op_sel_hi:[0,0,0]
	v_mfma_scale_f32_16x16x128_f8f6f4 v[100:103], v[144:151], v[24:31], v[168:171], v206, v206 op_sel_hi:[0,0,0]
	v_mfma_scale_f32_16x16x128_f8f6f4 v[88:91], v[112:119], v[32:39], v[172:175], v206, v206 op_sel_hi:[0,0,0]
	v_mfma_scale_f32_16x16x128_f8f6f4 v[80:83], v[144:151], v[32:39], v[176:179], v206, v206 op_sel_hi:[0,0,0]
	v_mfma_scale_f32_16x16x128_f8f6f4 v[52:55], v[112:119], v[40:47], v[180:183], v206, v206 op_sel_hi:[0,0,0]
	v_mfma_scale_f32_16x16x128_f8f6f4 v[48:51], v[144:151], v[40:47], v[184:187], v206, v206 op_sel_hi:[0,0,0]
	s_barrier
	s_setprio 0
	s_add_u32 s26, s30, 0x80
	s_addc_u32 s27, s31, 0
	ds_read_b128 v[32:35], v205 offset:49152
	ds_read_b128 v[36:39], v205 offset:50176
	ds_read_b128 v[152:155], v205 offset:51200
	ds_read_b128 v[156:159], v205 offset:52224
	ds_read_b128 v[160:163], v205 offset:53248
	ds_read_b128 v[164:167], v205 offset:54272
	ds_read_b128 v[168:171], v205 offset:55296
	ds_read_b128 v[172:175], v205 offset:56320
	s_mov_b32 s59, m0
	s_mov_b32 m0, s46
	s_nop 0
	global_load_lds_dwordx4 v201, s[26:27]
	s_mov_b32 m0, s59
	s_add_u32 s26, s30, 0x10080
	s_addc_u32 s27, s31, 0
	s_mov_b32 s59, m0
	s_mov_b32 m0, s47
	s_nop 0
	global_load_lds_dwordx4 v201, s[26:27]
	s_mov_b32 m0, s59
	s_add_u32 s26, s30, 0x20080
	s_addc_u32 s27, s31, 0
	s_mov_b32 s59, m0
	s_mov_b32 m0, s50
	s_nop 0
	global_load_lds_dwordx4 v201, s[26:27]
	s_mov_b32 m0, s59
	s_add_u32 s26, s30, 0x30080
	s_addc_u32 s27, s31, 0
	s_mov_b32 s30, m0
	s_mov_b32 m0, s51
	s_nop 0
	global_load_lds_dwordx4 v201, s[26:27]
	s_mov_b32 m0, s30
	s_mov_b32 s26, m0
	s_mov_b32 m0, s48
	s_nop 0
	global_load_lds_dwordx4 v202, s[28:29]
	s_mov_b32 m0, s26
	s_add_u32 s24, s24, 0x10080
	s_addc_u32 s25, s25, 0
	s_mov_b32 s26, m0
	s_mov_b32 m0, s49
	s_nop 0
	global_load_lds_dwordx4 v202, s[24:25]
	s_mov_b32 m0, s26
	s_waitcnt vmcnt(8)
	s_waitcnt lgkmcnt(0)
	s_setprio 1
	s_barrier
	v_mfma_scale_f32_16x16x128_f8f6f4 v[76:79], v[0:7], v[32:39], v[76:79], v206, v206 op_sel_hi:[0,0,0]
	v_mfma_scale_f32_16x16x128_f8f6f4 v[64:67], v[16:23], v[32:39], v[64:67], v206, v206 op_sel_hi:[0,0,0]
	v_mfma_scale_f32_16x16x128_f8f6f4 v[44:47], v[0:7], v[152:159], v[188:191], v206, v206 op_sel_hi:[0,0,0]
	v_mfma_scale_f32_16x16x128_f8f6f4 v[40:43], v[16:23], v[152:159], v[192:195], v206, v206 op_sel_hi:[0,0,0]
	v_mfma_scale_f32_16x16x128_f8f6f4 v[28:31], v[0:7], v[160:167], v[196:199], v206, v206 op_sel_hi:[0,0,0]
	v_mfma_scale_f32_16x16x128_f8f6f4 v[24:27], v[16:23], v[160:167], v[218:221], v206, v206 op_sel_hi:[0,0,0]
	v_mfma_scale_f32_16x16x128_f8f6f4 v[12:15], v[0:7], v[168:175], v[222:225], v206, v206 op_sel_hi:[0,0,0]
	v_mfma_scale_f32_16x16x128_f8f6f4 v[8:11], v[16:23], v[168:175], v[226:229], v206, v206 op_sel_hi:[0,0,0]
	s_setprio 0
	s_setprio 1
	v_mfma_scale_f32_16x16x128_f8f6f4 v[72:75], v[112:119], v[32:39], v[72:75], v206, v206 op_sel_hi:[0,0,0]
	v_mfma_scale_f32_16x16x128_f8f6f4 v[60:63], v[144:151], v[32:39], v[60:63], v206, v206 op_sel_hi:[0,0,0]
	v_mfma_scale_f32_16x16x128_f8f6f4 v[36:39], v[112:119], v[152:159], v[230:233], v206, v206 op_sel_hi:[0,0,0]
	v_mfma_scale_f32_16x16x128_f8f6f4 v[32:35], v[144:151], v[152:159], v[234:237], v206, v206 op_sel_hi:[0,0,0]
	v_mfma_scale_f32_16x16x128_f8f6f4 v[20:23], v[112:119], v[160:167], v[238:241], v206, v206 op_sel_hi:[0,0,0]
	v_mfma_scale_f32_16x16x128_f8f6f4 v[16:19], v[144:151], v[160:167], v[242:245], v206, v206 op_sel_hi:[0,0,0]
	v_mfma_scale_f32_16x16x128_f8f6f4 v[4:7], v[112:119], v[168:175], v[246:249], v206, v206 op_sel_hi:[0,0,0]
	v_mfma_scale_f32_16x16x128_f8f6f4 v[0:3], v[144:151], v[168:175], v[250:253], v206, v206 op_sel_hi:[0,0,0]
	s_barrier
	s_setprio 0
	s_add_i32 s58, s58, 2
	s_add_u32 s56, s56, 0x100
	s_addc_u32 s57, s57, 0
	s_cmp_gt_u32 s58, 5
	s_mov_b64 s[26:27], s[22:23]
	s_cbranch_scc0 .LBB0_2303
	s_and_b64 vcc, exec, s[4:5]
	s_cbranch_vccz .LBB0_2306
	s_barrier
